# v17 plus the vmcnt(N) and lgkmcnt(0) waits before each segment barrier merged into one s_waitcnt (72 sites)
# speedup vs baseline: 1.0052x; 1.0052x over previous
.LBB0_260:
	s_ashr_i32 s41, s40, 31
	s_lshl_b64 s[42:43], s[40:41], 19
	s_add_u32 s42, s54, s42
	s_addc_u32 s43, s55, s43
	s_and_b64 s[44:45], s[4:5], exec
	ds_read_b128 v[0:3], v219
	ds_read_b128 v[4:7], v219 offset:1024
	ds_read_b128 v[8:11], v219 offset:2048
	s_waitcnt vmcnt(2)
	ds_read_b128 v[12:15], v219 offset:3072
	s_waitcnt vmcnt(1)
	ds_read_b128 v[16:19], v220
	s_waitcnt vmcnt(0)
	ds_read_b128 v[20:23], v220 offset:1024
	ds_read_b128 v[24:27], v220 offset:2048
	ds_read_b128 v[28:31], v220 offset:3072
	s_cselect_b32 s7, s43, s13
	s_cselect_b32 s11, s42, s12
	s_ashr_i32 s39, s38, 31
	s_lshl_b64 s[44:45], s[38:39], 19
	s_add_u32 s44, s56, s44
	s_addc_u32 s45, s57, s45
	s_and_b64 s[46:47], s[4:5], exec
	s_cselect_b32 s39, s45, s9
	s_cselect_b32 s41, s44, s8
	s_add_u32 s46, s12, 0x100
	s_addc_u32 s47, s13, 0
	s_add_u32 s52, s8, 0x100
	s_addc_u32 s53, s9, 0
	s_add_u32 s48, s12, 0x180
	s_addc_u32 s49, s13, 0
	ds_read_b128 v[32:35], v221
	ds_read_b128 v[36:39], v221 offset:1024
	ds_read_b128 v[40:43], v221 offset:2048
	ds_read_b128 v[44:47], v221 offset:3072
	ds_read_b128 v[48:51], v221 offset:4096
	ds_read_b128 v[52:55], v221 offset:5120
	ds_read_b128 v[56:59], v221 offset:6144
	ds_read_b128 v[60:63], v221 offset:7168
	s_add_u32 s50, s8, 0x180
	s_addc_u32 s51, s9, 0
	s_add_u32 s76, s12, 0x40080
	s_addc_u32 s77, s13, 0
	s_add_i32 m0, s59, 0xc000
	s_nop 0
	global_load_lds_dwordx4 v215, s[76:77]
	s_nop 0
	s_add_i32 m0, s59, 0xe000
	s_nop 0
	global_load_lds_dwordx4 v217, s[76:77]
	s_waitcnt vmcnt(8) lgkmcnt(0)
	s_barrier
	s_waitcnt lgkmcnt(7)
	v_mfma_i32_16x16x64_i8 v[64:67], v[0:3], v[32:35], 0
	s_mov_b32 s76, 0
	v_mfma_i32_16x16x64_i8 v[68:71], v[8:11], v[32:35], 0
	s_waitcnt lgkmcnt(5)
	v_mfma_i32_16x16x64_i8 v[72:75], v[0:3], v[40:43], 0
	v_mfma_i32_16x16x64_i8 v[76:79], v[8:11], v[40:43], 0
	s_waitcnt lgkmcnt(3)
	v_mfma_i32_16x16x64_i8 v[84:87], v[8:11], v[48:51], 0
	s_waitcnt lgkmcnt(1)
	v_mfma_i32_16x16x64_i8 v[88:91], v[0:3], v[56:59], 0
	v_mfma_i32_16x16x64_i8 v[140:143], v[4:7], v[36:39], v[64:67]
	v_mfma_i32_16x16x64_i8 v[144:147], v[12:15], v[36:39], v[68:71]
	v_mfma_i32_16x16x64_i8 v[152:155], v[4:7], v[44:47], v[72:75]
	v_mfma_i32_16x16x64_i8 v[156:159], v[12:15], v[44:47], v[76:79]
	v_mfma_i32_16x16x64_i8 v[80:83], v[0:3], v[48:51], 0
	v_mfma_i32_16x16x64_i8 v[84:87], v[12:15], v[52:55], v[84:87]
	s_waitcnt lgkmcnt(0)
	v_mfma_i32_16x16x64_i8 v[88:91], v[4:7], v[60:63], v[88:91]
	v_mfma_i32_16x16x64_i8 v[92:95], v[8:11], v[56:59], 0
	v_mfma_i32_16x16x64_i8 v[80:83], v[4:7], v[52:55], v[80:83]
	v_mfma_i32_16x16x64_i8 v[92:95], v[12:15], v[60:63], v[92:95]
	v_mfma_i32_16x16x64_i8 v[96:99], v[16:19], v[32:35], 0
	v_mfma_i32_16x16x64_i8 v[32:35], v[24:27], v[32:35], 0
	v_mfma_i32_16x16x64_i8 v[96:99], v[20:23], v[36:39], v[96:99]
	v_mfma_i32_16x16x64_i8 v[32:35], v[28:31], v[36:39], v[32:35]
	v_mfma_i32_16x16x64_i8 v[36:39], v[16:19], v[40:43], 0
	v_mfma_i32_16x16x64_i8 v[40:43], v[24:27], v[40:43], 0
	v_mfma_i32_16x16x64_i8 v[36:39], v[20:23], v[44:47], v[36:39]
	v_mfma_i32_16x16x64_i8 v[40:43], v[28:31], v[44:47], v[40:43]
	v_mfma_i32_16x16x64_i8 v[44:47], v[16:19], v[48:51], 0
	v_mfma_i32_16x16x64_i8 v[48:51], v[24:27], v[48:51], 0
	v_mfma_i32_16x16x64_i8 v[44:47], v[20:23], v[52:55], v[44:47]
	v_mfma_i32_16x16x64_i8 v[48:51], v[28:31], v[52:55], v[48:51]
	v_mfma_i32_16x16x64_i8 v[52:55], v[16:19], v[56:59], 0
	v_mfma_i32_16x16x64_i8 v[56:59], v[24:27], v[56:59], 0
	v_mfma_i32_16x16x64_i8 v[52:55], v[20:23], v[60:63], v[52:55]
	v_mfma_i32_16x16x64_i8 v[56:59], v[28:31], v[60:63], v[56:59]
	s_barrier
	ds_read_b128 v[60:63], v221 offset:16384
	ds_read_b128 v[100:103], v221 offset:17408
	ds_read_b128 v[104:107], v221 offset:18432
	ds_read_b128 v[108:111], v221 offset:19456
	ds_read_b128 v[112:115], v221 offset:20480
	ds_read_b128 v[116:119], v221 offset:21504
	ds_read_b128 v[120:123], v221 offset:22528
	ds_read_b128 v[124:127], v221 offset:23552
	s_add_i32 m0, s59, 0x10000
	s_nop 0
	global_load_lds_dwordx4 v216, s[52:53]
	s_nop 0
	s_add_i32 m0, s59, 0x12000
	s_nop 0
	global_load_lds_dwordx4 v218, s[52:53]
	s_add_u32 s52, s8, 0x40100
	s_addc_u32 s53, s9, 0
	s_add_i32 m0, s59, 0x14000
	s_nop 0
	global_load_lds_dwordx4 v216, s[52:53]
	s_nop 0
	s_add_i32 m0, s59, 0x16000
	s_nop 0
	global_load_lds_dwordx4 v218, s[52:53]
	s_nop 0
	s_add_i32 m0, s59, 0
	s_nop 0
	global_load_lds_dwordx4 v215, s[46:47]
	s_nop 0
	s_add_i32 m0, s59, 0x2000
	s_nop 0
	global_load_lds_dwordx4 v217, s[46:47]
	s_waitcnt vmcnt(8) lgkmcnt(0)
	s_barrier
	v_mfma_i32_16x16x64_i8 v[136:139], v[0:3], v[104:107], 0
	v_mfma_i32_16x16x64_i8 v[228:231], v[4:7], v[108:111], v[136:139]
	v_mfma_i32_16x16x64_i8 v[136:139], v[8:11], v[104:107], 0
	v_mfma_i32_16x16x64_i8 v[128:131], v[0:3], v[60:63], 0
	v_mfma_i32_16x16x64_i8 v[132:135], v[8:11], v[60:63], 0
	v_mfma_i32_16x16x64_i8 v[232:235], v[12:15], v[108:111], v[136:139]
	v_mfma_i32_16x16x64_i8 v[136:139], v[0:3], v[112:115], 0
	v_mfma_i32_16x16x64_i8 v[0:3], v[0:3], v[120:123], 0
	v_mfma_i32_16x16x64_i8 v[128:131], v[4:7], v[100:103], v[128:131]
	v_mfma_i32_16x16x64_i8 v[132:135], v[12:15], v[100:103], v[132:135]
	v_mfma_i32_16x16x64_i8 v[236:239], v[4:7], v[116:119], v[136:139]
	v_mfma_i32_16x16x64_i8 v[136:139], v[8:11], v[112:115], 0
	v_mfma_i32_16x16x64_i8 v[0:3], v[4:7], v[124:127], v[0:3]
	v_mfma_i32_16x16x64_i8 v[4:7], v[8:11], v[120:123], 0
	v_mfma_i32_16x16x64_i8 v[240:243], v[12:15], v[116:119], v[136:139]
	v_mfma_i32_16x16x64_i8 v[4:7], v[12:15], v[124:127], v[4:7]
	v_mfma_i32_16x16x64_i8 v[8:11], v[16:19], v[60:63], 0
	v_mfma_i32_16x16x64_i8 v[12:15], v[24:27], v[60:63], 0
	v_mfma_i32_16x16x64_i8 v[8:11], v[20:23], v[100:103], v[8:11]
	v_mfma_i32_16x16x64_i8 v[12:15], v[28:31], v[100:103], v[12:15]
	v_mfma_i32_16x16x64_i8 v[60:63], v[16:19], v[104:107], 0
	v_mfma_i32_16x16x64_i8 v[100:103], v[24:27], v[104:107], 0
	v_mfma_i32_16x16x64_i8 v[104:107], v[16:19], v[112:115], 0
	v_mfma_i32_16x16x64_i8 v[16:19], v[16:19], v[120:123], 0
	v_mfma_i32_16x16x64_i8 v[60:63], v[20:23], v[108:111], v[60:63]
	v_mfma_i32_16x16x64_i8 v[100:103], v[28:31], v[108:111], v[100:103]
	v_mfma_i32_16x16x64_i8 v[244:247], v[20:23], v[116:119], v[104:107]
	v_mfma_i32_16x16x64_i8 v[104:107], v[24:27], v[112:115], 0
	v_mfma_i32_16x16x64_i8 v[16:19], v[20:23], v[124:127], v[16:19]
	v_mfma_i32_16x16x64_i8 v[20:23], v[24:27], v[120:123], 0
	v_mfma_i32_16x16x64_i8 v[248:251], v[28:31], v[116:119], v[104:107]
	v_mfma_i32_16x16x64_i8 v[20:23], v[28:31], v[124:127], v[20:23]
	s_barrier
	ds_read_b128 v[24:27], v222
	ds_read_b128 v[28:31], v222 offset:1024
	ds_read_b128 v[112:115], v222 offset:2048
	ds_read_b128 v[116:119], v222 offset:3072
	ds_read_b128 v[208:211], v223
	ds_read_b128 v[224:227], v223 offset:1024
	ds_read_b128 v[64:67], v223 offset:2048
	ds_read_b128 v[68:71], v223 offset:3072
	ds_read_b128 v[104:107], v221 offset:32768
	ds_read_b128 v[108:111], v221 offset:33792
	ds_read_b128 v[120:123], v221 offset:34816
	ds_read_b128 v[124:127], v221 offset:35840
	ds_read_b128 v[136:139], v221 offset:36864
	ds_read_b128 v[148:151], v221 offset:37888
	ds_read_b128 v[72:75], v221 offset:38912
	ds_read_b128 v[76:79], v221 offset:39936
	s_add_u32 s12, s12, 0x40100
	s_addc_u32 s13, s13, 0
	s_add_i32 m0, s59, 0x4000
	s_nop 0
	global_load_lds_dwordx4 v215, s[12:13]
	s_nop 0
	s_add_i32 m0, s59, 0x6000
	s_nop 0
	global_load_lds_dwordx4 v217, s[12:13]
	s_waitcnt vmcnt(8) lgkmcnt(0)
	s_barrier
	v_mfma_i32_16x16x64_i8 v[140:143], v[24:27], v[104:107], v[140:143]
	v_mfma_i32_16x16x64_i8 v[80:83], v[24:27], v[136:139], v[80:83]
	v_mfma_i32_16x16x64_i8 v[204:207], v[28:31], v[108:111], v[140:143]
	v_mfma_i32_16x16x64_i8 v[140:143], v[112:115], v[104:107], v[144:147]
	v_mfma_i32_16x16x64_i8 v[172:175], v[28:31], v[148:151], v[80:83]
	v_mfma_i32_16x16x64_i8 v[80:83], v[112:115], v[136:139], v[84:87]
	v_mfma_i32_16x16x64_i8 v[200:203], v[116:119], v[108:111], v[140:143]
	v_mfma_i32_16x16x64_i8 v[140:143], v[24:27], v[120:123], v[152:155]
	v_mfma_i32_16x16x64_i8 v[168:171], v[116:119], v[148:151], v[80:83]
	v_mfma_i32_16x16x64_i8 v[80:83], v[24:27], v[72:75], v[88:91]
	v_mfma_i32_16x16x64_i8 v[188:191], v[28:31], v[124:127], v[140:143]
	v_mfma_i32_16x16x64_i8 v[140:143], v[112:115], v[120:123], v[156:159]
	v_mfma_i32_16x16x64_i8 v[156:159], v[28:31], v[76:79], v[80:83]
	v_mfma_i32_16x16x64_i8 v[80:83], v[112:115], v[72:75], v[92:95]
	v_mfma_i32_16x16x64_i8 v[184:187], v[116:119], v[124:127], v[140:143]
	v_mfma_i32_16x16x64_i8 v[152:155], v[116:119], v[76:79], v[80:83]
	v_mfma_i32_16x16x64_i8 v[32:35], v[64:67], v[104:107], v[32:35]
	v_mfma_i32_16x16x64_i8 v[192:195], v[68:71], v[108:111], v[32:35]
	v_mfma_i32_16x16x64_i8 v[32:35], v[208:211], v[120:123], v[36:39]
	v_mfma_i32_16x16x64_i8 v[180:183], v[224:227], v[124:127], v[32:35]
	v_mfma_i32_16x16x64_i8 v[32:35], v[64:67], v[120:123], v[40:43]
	v_mfma_i32_16x16x64_i8 v[176:179], v[68:71], v[124:127], v[32:35]
	v_mfma_i32_16x16x64_i8 v[32:35], v[208:211], v[136:139], v[44:47]
	v_mfma_i32_16x16x64_i8 v[164:167], v[224:227], v[148:151], v[32:35]
	v_mfma_i32_16x16x64_i8 v[32:35], v[64:67], v[136:139], v[48:51]
	v_mfma_i32_16x16x64_i8 v[160:163], v[68:71], v[148:151], v[32:35]
	v_mfma_i32_16x16x64_i8 v[32:35], v[208:211], v[72:75], v[52:55]
	v_mfma_i32_16x16x64_i8 v[80:83], v[208:211], v[104:107], v[96:99]
	v_mfma_i32_16x16x64_i8 v[148:151], v[224:227], v[76:79], v[32:35]
	v_mfma_i32_16x16x64_i8 v[32:35], v[64:67], v[72:75], v[56:59]
	v_mfma_i32_16x16x64_i8 v[196:199], v[224:227], v[108:111], v[80:83]
	v_mfma_i32_16x16x64_i8 v[144:147], v[68:71], v[76:79], v[32:35]
	s_barrier
	s_nop 3
	ds_read_b128 v[32:35], v221 offset:49152
	ds_read_b128 v[36:39], v221 offset:50176
	ds_read_b128 v[40:43], v221 offset:51200
	ds_read_b128 v[44:47], v221 offset:52224
	ds_read_b128 v[48:51], v221 offset:53248
	ds_read_b128 v[52:55], v221 offset:54272
	ds_read_b128 v[56:59], v221 offset:55296
	ds_read_b128 v[76:79], v221 offset:56320
	s_add_i32 m0, s59, 0x18000
	s_nop 0
	global_load_lds_dwordx4 v216, s[50:51]
	s_nop 0
	s_add_i32 m0, s59, 0x1a000
	s_nop 0
	global_load_lds_dwordx4 v218, s[50:51]
	s_add_u32 s12, s8, 0x40180
	s_addc_u32 s13, s9, 0
	s_add_i32 m0, s59, 0x1c000
	s_nop 0
	global_load_lds_dwordx4 v216, s[12:13]
	s_nop 0
	s_add_i32 m0, s59, 0x1e000
	s_nop 0
	global_load_lds_dwordx4 v218, s[12:13]
	s_nop 0
	s_add_i32 m0, s59, 0x8000
	s_nop 0
	global_load_lds_dwordx4 v215, s[48:49]
	s_nop 0
	s_add_i32 m0, s59, 0xa000
	s_nop 0
	global_load_lds_dwordx4 v217, s[48:49]
	s_waitcnt vmcnt(8) lgkmcnt(0)
	s_barrier
	v_mfma_i32_16x16x64_i8 v[72:75], v[24:27], v[32:35], v[128:131]
	v_mfma_i32_16x16x64_i8 v[140:143], v[28:31], v[36:39], v[72:75]
	v_mfma_i32_16x16x64_i8 v[72:75], v[112:115], v[32:35], v[132:135]
	v_mfma_i32_16x16x64_i8 v[136:139], v[116:119], v[36:39], v[72:75]
	v_mfma_i32_16x16x64_i8 v[72:75], v[24:27], v[40:43], v[228:231]
	v_mfma_i32_16x16x64_i8 v[124:127], v[28:31], v[44:47], v[72:75]
	v_mfma_i32_16x16x64_i8 v[72:75], v[112:115], v[40:43], v[232:235]
	v_mfma_i32_16x16x64_i8 v[120:123], v[116:119], v[44:47], v[72:75]
	v_mfma_i32_16x16x64_i8 v[72:75], v[24:27], v[48:51], v[236:239]
	v_mfma_i32_16x16x64_i8 v[0:3], v[24:27], v[56:59], v[0:3]
	v_mfma_i32_16x16x64_i8 v[108:111], v[28:31], v[52:55], v[72:75]
	v_mfma_i32_16x16x64_i8 v[72:75], v[112:115], v[48:51], v[240:243]
	v_mfma_i32_16x16x64_i8 v[88:91], v[28:31], v[76:79], v[0:3]
	v_mfma_i32_16x16x64_i8 v[0:3], v[112:115], v[56:59], v[4:7]
	v_mfma_i32_16x16x64_i8 v[104:107], v[116:119], v[52:55], v[72:75]
	v_mfma_i32_16x16x64_i8 v[84:87], v[116:119], v[76:79], v[0:3]
	v_mfma_i32_16x16x64_i8 v[0:3], v[208:211], v[32:35], v[8:11]
	v_mfma_i32_16x16x64_i8 v[132:135], v[224:227], v[36:39], v[0:3]
	v_mfma_i32_16x16x64_i8 v[0:3], v[64:67], v[32:35], v[12:15]
	v_mfma_i32_16x16x64_i8 v[128:131], v[68:71], v[36:39], v[0:3]
	v_mfma_i32_16x16x64_i8 v[0:3], v[208:211], v[40:43], v[60:63]
	v_mfma_i32_16x16x64_i8 v[116:119], v[224:227], v[44:47], v[0:3]
	v_mfma_i32_16x16x64_i8 v[0:3], v[64:67], v[40:43], v[100:103]
	v_mfma_i32_16x16x64_i8 v[112:115], v[68:71], v[44:47], v[0:3]
	v_mfma_i32_16x16x64_i8 v[0:3], v[208:211], v[48:51], v[244:247]
	v_mfma_i32_16x16x64_i8 v[100:103], v[224:227], v[52:55], v[0:3]
	v_mfma_i32_16x16x64_i8 v[0:3], v[64:67], v[48:51], v[248:251]
	v_mfma_i32_16x16x64_i8 v[96:99], v[68:71], v[52:55], v[0:3]
	v_mfma_i32_16x16x64_i8 v[0:3], v[208:211], v[56:59], v[16:19]
	v_mfma_i32_16x16x64_i8 v[72:75], v[224:227], v[76:79], v[0:3]
	v_mfma_i32_16x16x64_i8 v[0:3], v[64:67], v[56:59], v[20:23]
	v_mfma_i32_16x16x64_i8 v[68:71], v[68:71], v[76:79], v[0:3]
	s_barrier
	s_add_u32 s77, s8, 0x200
	s_addc_u32 s80, s9, 0
.LBB0_261:
	s_nop 2
	ds_read_b128 v[0:3], v219
	ds_read_b128 v[4:7], v219 offset:1024
	ds_read_b128 v[8:11], v219 offset:2048
	ds_read_b128 v[12:15], v219 offset:3072
	ds_read_b128 v[16:19], v220
	ds_read_b128 v[20:23], v220 offset:1024
	ds_read_b128 v[24:27], v220 offset:2048
	ds_read_b128 v[28:31], v220 offset:3072
	ds_read_b128 v[32:35], v221
	ds_read_b128 v[36:39], v221 offset:1024
	ds_read_b128 v[40:43], v221 offset:2048
	ds_read_b128 v[44:47], v221 offset:3072
	ds_read_b128 v[48:51], v221 offset:4096
	ds_read_b128 v[52:55], v221 offset:5120
	ds_read_b128 v[56:59], v221 offset:6144
	ds_read_b128 v[60:63], v221 offset:7168
	s_add_u32 s8, s46, 0x100
	s_addc_u32 s9, s47, 0
	s_cmp_eq_u32 s76, 12
	s_cselect_b32 s52, s11, s8
	s_cselect_b32 s53, s7, s9
	s_cselect_b32 s48, s41, s77
	s_cselect_b32 s49, s39, s80
	s_add_u32 s12, s52, 0x80
	s_addc_u32 s13, s53, 0
	s_add_u32 s50, s48, 0x80
	s_addc_u32 s51, s49, 0
	s_add_u32 s46, s46, 0x40080
	s_addc_u32 s47, s47, 0
	s_add_i32 m0, s59, 0xc000
	s_nop 0
	global_load_lds_dwordx4 v215, s[46:47]
	s_nop 0
	s_add_i32 m0, s59, 0xe000
	s_nop 0
	global_load_lds_dwordx4 v217, s[46:47]
	s_waitcnt vmcnt(8) lgkmcnt(0)
	s_barrier
	v_mfma_i32_16x16x64_i8 v[172:175], v[0:3], v[48:51], v[172:175]
	v_mfma_i32_16x16x64_i8 v[168:171], v[8:11], v[48:51], v[168:171]
	v_mfma_i32_16x16x64_i8 v[152:155], v[8:11], v[56:59], v[152:155]
	v_mfma_i32_16x16x64_i8 v[156:159], v[0:3], v[56:59], v[156:159]
	v_mfma_i32_16x16x64_i8 v[64:67], v[0:3], v[32:35], v[204:207]
	v_mfma_i32_16x16x64_i8 v[76:79], v[8:11], v[32:35], v[200:203]
	v_mfma_i32_16x16x64_i8 v[92:95], v[8:11], v[40:43], v[184:187]
	v_mfma_i32_16x16x64_i8 v[80:83], v[0:3], v[40:43], v[188:191]
	v_mfma_i32_16x16x64_i8 v[172:175], v[4:7], v[52:55], v[172:175]
	v_mfma_i32_16x16x64_i8 v[168:171], v[12:15], v[52:55], v[168:171]
	v_mfma_i32_16x16x64_i8 v[152:155], v[12:15], v[60:63], v[152:155]
	v_mfma_i32_16x16x64_i8 v[156:159], v[4:7], v[60:63], v[156:159]
	v_mfma_i32_16x16x64_i8 v[64:67], v[4:7], v[36:39], v[64:67]
	v_mfma_i32_16x16x64_i8 v[76:79], v[12:15], v[36:39], v[76:79]
	v_mfma_i32_16x16x64_i8 v[92:95], v[12:15], v[44:47], v[92:95]
	v_mfma_i32_16x16x64_i8 v[80:83], v[4:7], v[44:47], v[80:83]
	v_mfma_i32_16x16x64_i8 v[184:187], v[16:19], v[32:35], v[196:199]
	v_mfma_i32_16x16x64_i8 v[32:35], v[24:27], v[32:35], v[192:195]
	v_mfma_i32_16x16x64_i8 v[196:199], v[20:23], v[36:39], v[184:187]
	v_mfma_i32_16x16x64_i8 v[32:35], v[28:31], v[36:39], v[32:35]
	v_mfma_i32_16x16x64_i8 v[36:39], v[16:19], v[40:43], v[180:183]
	v_mfma_i32_16x16x64_i8 v[40:43], v[24:27], v[40:43], v[176:179]
	v_mfma_i32_16x16x64_i8 v[36:39], v[20:23], v[44:47], v[36:39]
	v_mfma_i32_16x16x64_i8 v[40:43], v[28:31], v[44:47], v[40:43]
	v_mfma_i32_16x16x64_i8 v[44:47], v[16:19], v[48:51], v[164:167]
	v_mfma_i32_16x16x64_i8 v[48:51], v[24:27], v[48:51], v[160:163]
	v_mfma_i32_16x16x64_i8 v[44:47], v[20:23], v[52:55], v[44:47]
	v_mfma_i32_16x16x64_i8 v[48:51], v[28:31], v[52:55], v[48:51]
	v_mfma_i32_16x16x64_i8 v[52:55], v[16:19], v[56:59], v[148:151]
	v_mfma_i32_16x16x64_i8 v[56:59], v[24:27], v[56:59], v[144:147]
	v_mfma_i32_16x16x64_i8 v[52:55], v[20:23], v[60:63], v[52:55]
	v_mfma_i32_16x16x64_i8 v[56:59], v[28:31], v[60:63], v[56:59]
	s_barrier
	ds_read_b128 v[60:63], v221 offset:16384
	ds_read_b128 v[144:147], v221 offset:17408
	ds_read_b128 v[148:151], v221 offset:18432
	ds_read_b128 v[160:163], v221 offset:19456
	ds_read_b128 v[164:167], v221 offset:20480
	ds_read_b128 v[176:179], v221 offset:21504
	ds_read_b128 v[180:183], v221 offset:22528
	ds_read_b128 v[184:187], v221 offset:23552
	s_add_i32 m0, s59, 0x10000
	s_nop 0
	global_load_lds_dwordx4 v216, s[48:49]
	s_nop 0
	s_add_i32 m0, s59, 0x12000
	s_nop 0
	global_load_lds_dwordx4 v218, s[48:49]
	s_add_u32 s46, s48, 0x40000
	s_addc_u32 s47, s49, 0
	s_add_i32 m0, s59, 0x14000
	s_nop 0
	global_load_lds_dwordx4 v216, s[46:47]
	s_nop 0
	s_add_i32 m0, s59, 0x16000
	s_nop 0
	global_load_lds_dwordx4 v218, s[46:47]
	s_nop 0
	s_add_i32 m0, s59, 0
	s_nop 0
	global_load_lds_dwordx4 v215, s[52:53]
	s_nop 0
	s_add_i32 m0, s59, 0x2000
	s_nop 0
	global_load_lds_dwordx4 v217, s[52:53]
	s_waitcnt vmcnt(8) lgkmcnt(0)
	s_barrier
	v_mfma_i32_16x16x64_i8 v[140:143], v[0:3], v[60:63], v[140:143]
	v_mfma_i32_16x16x64_i8 v[124:127], v[0:3], v[148:151], v[124:127]
	v_mfma_i32_16x16x64_i8 v[108:111], v[0:3], v[164:167], v[108:111]
	v_mfma_i32_16x16x64_i8 v[0:3], v[0:3], v[180:183], v[88:91]
	v_mfma_i32_16x16x64_i8 v[136:139], v[8:11], v[60:63], v[136:139]
	v_mfma_i32_16x16x64_i8 v[120:123], v[8:11], v[148:151], v[120:123]
	v_mfma_i32_16x16x64_i8 v[104:107], v[8:11], v[164:167], v[104:107]
	v_mfma_i32_16x16x64_i8 v[88:91], v[4:7], v[184:187], v[0:3]
	v_mfma_i32_16x16x64_i8 v[0:3], v[8:11], v[180:183], v[84:87]
	v_mfma_i32_16x16x64_i8 v[140:143], v[4:7], v[144:147], v[140:143]
	v_mfma_i32_16x16x64_i8 v[136:139], v[12:15], v[144:147], v[136:139]
	v_mfma_i32_16x16x64_i8 v[124:127], v[4:7], v[160:163], v[124:127]
	v_mfma_i32_16x16x64_i8 v[120:123], v[12:15], v[160:163], v[120:123]
	v_mfma_i32_16x16x64_i8 v[108:111], v[4:7], v[176:179], v[108:111]
	v_mfma_i32_16x16x64_i8 v[104:107], v[12:15], v[176:179], v[104:107]
	v_mfma_i32_16x16x64_i8 v[84:87], v[12:15], v[184:187], v[0:3]
	v_mfma_i32_16x16x64_i8 v[0:3], v[16:19], v[60:63], v[132:135]
	v_mfma_i32_16x16x64_i8 v[132:135], v[20:23], v[144:147], v[0:3]
	v_mfma_i32_16x16x64_i8 v[0:3], v[24:27], v[60:63], v[128:131]
	v_mfma_i32_16x16x64_i8 v[128:131], v[28:31], v[144:147], v[0:3]
	v_mfma_i32_16x16x64_i8 v[0:3], v[16:19], v[148:151], v[116:119]
	v_mfma_i32_16x16x64_i8 v[116:119], v[20:23], v[160:163], v[0:3]
	v_mfma_i32_16x16x64_i8 v[0:3], v[24:27], v[148:151], v[112:115]
	v_mfma_i32_16x16x64_i8 v[112:115], v[28:31], v[160:163], v[0:3]
	v_mfma_i32_16x16x64_i8 v[0:3], v[16:19], v[164:167], v[100:103]
	v_mfma_i32_16x16x64_i8 v[100:103], v[20:23], v[176:179], v[0:3]
	v_mfma_i32_16x16x64_i8 v[0:3], v[24:27], v[164:167], v[96:99]
	v_mfma_i32_16x16x64_i8 v[96:99], v[28:31], v[176:179], v[0:3]
	v_mfma_i32_16x16x64_i8 v[0:3], v[16:19], v[180:183], v[72:75]
	v_mfma_i32_16x16x64_i8 v[72:75], v[20:23], v[184:187], v[0:3]
	v_mfma_i32_16x16x64_i8 v[0:3], v[24:27], v[180:183], v[68:71]
	v_mfma_i32_16x16x64_i8 v[68:71], v[28:31], v[184:187], v[0:3]
	s_barrier
	ds_read_b128 v[16:19], v222
	ds_read_b128 v[8:11], v222 offset:1024
	ds_read_b128 v[4:7], v222 offset:2048
	s_nop 1
	ds_read_b128 v[0:3], v222 offset:3072
	ds_read_b128 v[28:31], v223
	ds_read_b128 v[24:27], v223 offset:1024
	ds_read_b128 v[20:23], v223 offset:2048
	ds_read_b128 v[12:15], v223 offset:3072
	ds_read_b128 v[60:63], v221 offset:32768
	ds_read_b128 v[144:147], v221 offset:33792
	ds_read_b128 v[148:151], v221 offset:34816
	ds_read_b128 v[160:163], v221 offset:35840
	ds_read_b128 v[208:211], v221 offset:36864
	ds_read_b128 v[224:227], v221 offset:37888
	ds_read_b128 v[228:231], v221 offset:38912
	ds_read_b128 v[232:235], v221 offset:39936
	s_add_u32 s46, s52, 0x40000
	s_addc_u32 s47, s53, 0
	s_add_i32 m0, s59, 0x4000
	s_nop 0
	global_load_lds_dwordx4 v215, s[46:47]
	s_nop 0
	s_add_i32 m0, s59, 0x6000
	s_nop 0
	global_load_lds_dwordx4 v217, s[46:47]
	s_waitcnt vmcnt(8) lgkmcnt(0)
	s_barrier
	v_mfma_i32_16x16x64_i8 v[64:67], v[16:19], v[60:63], v[64:67]
	v_mfma_i32_16x16x64_i8 v[204:207], v[8:11], v[144:147], v[64:67]
	v_mfma_i32_16x16x64_i8 v[64:67], v[4:7], v[60:63], v[76:79]
	v_mfma_i32_16x16x64_i8 v[200:203], v[0:3], v[144:147], v[64:67]
	v_mfma_i32_16x16x64_i8 v[64:67], v[16:19], v[148:151], v[80:83]
	v_mfma_i32_16x16x64_i8 v[188:191], v[8:11], v[160:163], v[64:67]
	v_mfma_i32_16x16x64_i8 v[64:67], v[4:7], v[148:151], v[92:95]
	v_mfma_i32_16x16x64_i8 v[184:187], v[0:3], v[160:163], v[64:67]
	v_mfma_i32_16x16x64_i8 v[64:67], v[16:19], v[208:211], v[172:175]
	v_mfma_i32_16x16x64_i8 v[172:175], v[8:11], v[224:227], v[64:67]
	v_mfma_i32_16x16x64_i8 v[64:67], v[4:7], v[208:211], v[168:171]
	v_mfma_i32_16x16x64_i8 v[168:171], v[0:3], v[224:227], v[64:67]
	v_mfma_i32_16x16x64_i8 v[64:67], v[16:19], v[228:231], v[156:159]
	v_mfma_i32_16x16x64_i8 v[156:159], v[8:11], v[232:235], v[64:67]
	v_mfma_i32_16x16x64_i8 v[64:67], v[4:7], v[228:231], v[152:155]
	v_mfma_i32_16x16x64_i8 v[152:155], v[0:3], v[232:235], v[64:67]
	v_mfma_i32_16x16x64_i8 v[32:35], v[20:23], v[60:63], v[32:35]
	v_mfma_i32_16x16x64_i8 v[192:195], v[12:15], v[144:147], v[32:35]
	v_mfma_i32_16x16x64_i8 v[32:35], v[28:31], v[148:151], v[36:39]
	v_mfma_i32_16x16x64_i8 v[180:183], v[24:27], v[160:163], v[32:35]
	v_mfma_i32_16x16x64_i8 v[32:35], v[20:23], v[148:151], v[40:43]
	v_mfma_i32_16x16x64_i8 v[176:179], v[12:15], v[160:163], v[32:35]
	v_mfma_i32_16x16x64_i8 v[32:35], v[28:31], v[208:211], v[44:47]
	v_mfma_i32_16x16x64_i8 v[164:167], v[24:27], v[224:227], v[32:35]
	v_mfma_i32_16x16x64_i8 v[32:35], v[20:23], v[208:211], v[48:51]
	v_mfma_i32_16x16x64_i8 v[160:163], v[12:15], v[224:227], v[32:35]
	v_mfma_i32_16x16x64_i8 v[32:35], v[28:31], v[228:231], v[52:55]
	v_mfma_i32_16x16x64_i8 v[64:67], v[28:31], v[60:63], v[196:199]
	v_mfma_i32_16x16x64_i8 v[148:151], v[24:27], v[232:235], v[32:35]
	v_mfma_i32_16x16x64_i8 v[32:35], v[20:23], v[228:231], v[56:59]
	v_mfma_i32_16x16x64_i8 v[196:199], v[24:27], v[144:147], v[64:67]
	v_mfma_i32_16x16x64_i8 v[144:147], v[12:15], v[232:235], v[32:35]
	s_barrier
	ds_read_b128 v[60:63], v221 offset:49152
	ds_read_b128 v[56:59], v221 offset:50176
	ds_read_b128 v[52:55], v221 offset:51200
	ds_read_b128 v[48:51], v221 offset:52224
	ds_read_b128 v[44:47], v221 offset:53248
	ds_read_b128 v[40:43], v221 offset:54272
	ds_read_b128 v[36:39], v221 offset:55296
	ds_read_b128 v[32:35], v221 offset:56320
	s_add_i32 m0, s59, 0x18000
	s_nop 0
	global_load_lds_dwordx4 v216, s[50:51]
	s_nop 0
	s_add_i32 m0, s59, 0x1a000
	s_nop 0
	global_load_lds_dwordx4 v218, s[50:51]
	s_add_u32 s46, s48, 0x40080
	s_addc_u32 s47, s49, 0
	s_add_i32 m0, s59, 0x1c000
	s_nop 0
	global_load_lds_dwordx4 v216, s[46:47]
	s_nop 0
	s_add_i32 m0, s59, 0x1e000
	s_nop 0
	global_load_lds_dwordx4 v218, s[46:47]
	s_nop 0
	s_add_i32 m0, s59, 0x8000
	s_nop 0
	global_load_lds_dwordx4 v215, s[12:13]
	s_nop 0
	s_add_i32 m0, s59, 0xa000
	s_nop 0
	global_load_lds_dwordx4 v217, s[12:13]
	s_waitcnt vmcnt(8) lgkmcnt(0)
	s_barrier
	v_mfma_i32_16x16x64_i8 v[64:67], v[16:19], v[60:63], v[140:143]
	v_mfma_i32_16x16x64_i8 v[140:143], v[8:11], v[56:59], v[64:67]
	v_mfma_i32_16x16x64_i8 v[64:67], v[4:7], v[60:63], v[136:139]
	v_mfma_i32_16x16x64_i8 v[136:139], v[0:3], v[56:59], v[64:67]
	v_mfma_i32_16x16x64_i8 v[64:67], v[16:19], v[52:55], v[124:127]
	v_mfma_i32_16x16x64_i8 v[124:127], v[8:11], v[48:51], v[64:67]
	v_mfma_i32_16x16x64_i8 v[64:67], v[4:7], v[52:55], v[120:123]
	v_mfma_i32_16x16x64_i8 v[120:123], v[0:3], v[48:51], v[64:67]
	v_mfma_i32_16x16x64_i8 v[64:67], v[16:19], v[44:47], v[108:111]
	v_mfma_i32_16x16x64_i8 v[108:111], v[8:11], v[40:43], v[64:67]
	v_mfma_i32_16x16x64_i8 v[64:67], v[4:7], v[44:47], v[104:107]
	v_mfma_i32_16x16x64_i8 v[104:107], v[0:3], v[40:43], v[64:67]
	v_mfma_i32_16x16x64_i8 v[64:67], v[16:19], v[36:39], v[88:91]
	v_mfma_i32_16x16x64_i8 v[88:91], v[8:11], v[32:35], v[64:67]
	v_mfma_i32_16x16x64_i8 v[64:67], v[4:7], v[36:39], v[84:87]
	v_mfma_i32_16x16x64_i8 v[84:87], v[0:3], v[32:35], v[64:67]
	v_mfma_i32_16x16x64_i8 v[64:67], v[28:31], v[60:63], v[132:135]
	v_mfma_i32_16x16x64_i8 v[132:135], v[24:27], v[56:59], v[64:67]
	v_mfma_i32_16x16x64_i8 v[64:67], v[20:23], v[60:63], v[128:131]
	v_mfma_i32_16x16x64_i8 v[128:131], v[12:15], v[56:59], v[64:67]
	v_mfma_i32_16x16x64_i8 v[64:67], v[28:31], v[52:55], v[116:119]
	v_mfma_i32_16x16x64_i8 v[116:119], v[24:27], v[48:51], v[64:67]
	v_mfma_i32_16x16x64_i8 v[64:67], v[20:23], v[52:55], v[112:115]
	v_mfma_i32_16x16x64_i8 v[112:115], v[12:15], v[48:51], v[64:67]
	v_mfma_i32_16x16x64_i8 v[64:67], v[28:31], v[44:47], v[100:103]
	v_mfma_i32_16x16x64_i8 v[100:103], v[24:27], v[40:43], v[64:67]
	v_mfma_i32_16x16x64_i8 v[64:67], v[20:23], v[44:47], v[96:99]
	v_mfma_i32_16x16x64_i8 v[96:99], v[12:15], v[40:43], v[64:67]
	v_mfma_i32_16x16x64_i8 v[64:67], v[28:31], v[36:39], v[72:75]
	v_mfma_i32_16x16x64_i8 v[72:75], v[24:27], v[32:35], v[64:67]
	v_mfma_i32_16x16x64_i8 v[64:67], v[20:23], v[36:39], v[68:71]
	v_mfma_i32_16x16x64_i8 v[68:71], v[12:15], v[32:35], v[64:67]
	s_barrier
	s_add_i32 s76, s76, 2
	s_add_u32 s77, s77, 0x100
	s_addc_u32 s80, s80, 0
	s_cmp_gt_u32 s76, 13
	s_mov_b64 s[46:47], s[8:9]
	s_cbranch_scc0 .LBB0_261
	s_and_b64 vcc, exec, s[28:29]
	s_cbranch_vccz .LBB0_264
	s_barrier

.LBB0_602:
	s_ashr_i32 s25, s24, 31
	s_lshl_b64 s[26:27], s[24:25], 20
	s_add_u32 s26, s44, s26
	s_addc_u32 s27, s45, s27
	s_and_b64 s[28:29], s[4:5], exec
	s_waitcnt lgkmcnt(0)
	ds_read_b128 v[0:3], v217
	ds_read_b128 v[4:7], v217 offset:1024
	ds_read_b128 v[8:11], v217 offset:2048
	ds_read_b128 v[12:15], v217 offset:3072
	ds_read_b128 v[16:19], v218
	ds_read_b128 v[20:23], v218 offset:1024
	ds_read_b128 v[24:27], v218 offset:2048
	ds_read_b128 v[28:31], v218 offset:3072
	ds_read_b128 v[32:35], v219
	ds_read_b128 v[36:39], v219 offset:1024
	ds_read_b128 v[40:43], v219 offset:2048
	ds_read_b128 v[44:47], v219 offset:3072
	ds_read_b128 v[48:51], v219 offset:4096
	ds_read_b128 v[52:55], v219 offset:5120
	ds_read_b128 v[56:59], v219 offset:6144
	ds_read_b128 v[60:63], v219 offset:7168
	s_cselect_b32 s7, s27, s35
	s_cselect_b32 s9, s26, s34
	s_ashr_i32 s23, s22, 31
	s_lshl_b64 s[28:29], s[22:23], 20
	s_add_u32 s28, s46, s28
	s_addc_u32 s29, s47, s29
	s_and_b64 s[36:37], s[4:5], exec
	s_cselect_b32 s23, s29, s31
	s_cselect_b32 s25, s28, s30
	s_add_u32 s36, s34, 0x100
	s_addc_u32 s37, s35, 0
	s_add_u32 s42, s30, 0x100
	s_addc_u32 s43, s31, 0
	s_add_u32 s38, s34, 0x180
	s_addc_u32 s39, s35, 0
	s_add_u32 s40, s30, 0x180
	s_addc_u32 s41, s31, 0
	s_add_u32 s60, s34, 0x80080
	s_addc_u32 s61, s35, 0
	s_add_i32 m0, s48, 0xc000
	s_nop 0
	global_load_lds_dwordx4 v213, s[60:61]
	s_nop 0
	s_add_i32 m0, s48, 0xe000
	s_nop 0
	global_load_lds_dwordx4 v214, s[60:61]
	s_waitcnt vmcnt(8) lgkmcnt(0)
	s_barrier
	v_mfma_f32_16x16x32_bf16 v[64:67], v[0:3], v[32:35], 0
	v_mfma_f32_16x16x32_bf16 v[68:71], v[8:11], v[32:35], 0
	v_mfma_f32_16x16x32_bf16 v[72:75], v[0:3], v[40:43], 0
	v_mfma_f32_16x16x32_bf16 v[76:79], v[8:11], v[40:43], 0
	v_mfma_f32_16x16x32_bf16 v[80:83], v[0:3], v[48:51], 0
	v_mfma_f32_16x16x32_bf16 v[84:87], v[8:11], v[48:51], 0
	v_mfma_f32_16x16x32_bf16 v[88:91], v[0:3], v[56:59], 0
	v_mfma_f32_16x16x32_bf16 v[64:67], v[4:7], v[36:39], v[64:67]
	v_mfma_f32_16x16x32_bf16 v[68:71], v[12:15], v[36:39], v[68:71]
	v_mfma_f32_16x16x32_bf16 v[72:75], v[4:7], v[44:47], v[72:75]
	v_mfma_f32_16x16x32_bf16 v[76:79], v[12:15], v[44:47], v[76:79]
	v_mfma_f32_16x16x32_bf16 v[80:83], v[4:7], v[52:55], v[80:83]
	v_mfma_f32_16x16x32_bf16 v[84:87], v[12:15], v[52:55], v[84:87]
	v_mfma_f32_16x16x32_bf16 v[96:99], v[4:7], v[60:63], v[88:91]
	v_mfma_f32_16x16x32_bf16 v[88:91], v[8:11], v[56:59], 0
	v_mfma_f32_16x16x32_bf16 v[100:103], v[12:15], v[60:63], v[88:91]
	v_mfma_f32_16x16x32_bf16 v[88:91], v[16:19], v[32:35], 0
	v_mfma_f32_16x16x32_bf16 v[32:35], v[24:27], v[32:35], 0
	v_mfma_f32_16x16x32_bf16 v[104:107], v[20:23], v[36:39], v[88:91]
	v_mfma_f32_16x16x32_bf16 v[32:35], v[28:31], v[36:39], v[32:35]
	v_mfma_f32_16x16x32_bf16 v[36:39], v[16:19], v[40:43], 0
	v_mfma_f32_16x16x32_bf16 v[40:43], v[24:27], v[40:43], 0
	v_mfma_f32_16x16x32_bf16 v[36:39], v[20:23], v[44:47], v[36:39]
	v_mfma_f32_16x16x32_bf16 v[40:43], v[28:31], v[44:47], v[40:43]
	v_mfma_f32_16x16x32_bf16 v[44:47], v[16:19], v[48:51], 0
	v_mfma_f32_16x16x32_bf16 v[48:51], v[24:27], v[48:51], 0
	v_mfma_f32_16x16x32_bf16 v[44:47], v[20:23], v[52:55], v[44:47]
	v_mfma_f32_16x16x32_bf16 v[48:51], v[28:31], v[52:55], v[48:51]
	v_mfma_f32_16x16x32_bf16 v[52:55], v[16:19], v[56:59], 0
	v_mfma_f32_16x16x32_bf16 v[56:59], v[24:27], v[56:59], 0
	v_mfma_f32_16x16x32_bf16 v[52:55], v[20:23], v[60:63], v[52:55]
	v_mfma_f32_16x16x32_bf16 v[56:59], v[28:31], v[60:63], v[56:59]
	s_barrier
	ds_read_b128 v[60:63], v219 offset:16384
	ds_read_b128 v[88:91], v219 offset:17408
	ds_read_b128 v[92:95], v219 offset:18432
	ds_read_b128 v[108:111], v219 offset:19456
	ds_read_b128 v[112:115], v219 offset:20480
	ds_read_b128 v[116:119], v219 offset:21504
	ds_read_b128 v[120:123], v219 offset:22528
	ds_read_b128 v[124:127], v219 offset:23552
	s_add_i32 m0, s48, 0x10000
	s_nop 0
	global_load_lds_dwordx4 v213, s[42:43]
	s_nop 0
	s_add_i32 m0, s48, 0x12000
	s_nop 0
	global_load_lds_dwordx4 v214, s[42:43]
	s_add_u32 s42, s30, 0x80100
	s_addc_u32 s43, s31, 0
	s_add_i32 m0, s48, 0x14000
	s_nop 0
	global_load_lds_dwordx4 v213, s[42:43]
	s_nop 0
	s_add_i32 m0, s48, 0x16000
	s_nop 0
	global_load_lds_dwordx4 v214, s[42:43]
	s_nop 0
	s_add_i32 m0, s48, 0
	s_nop 0
	global_load_lds_dwordx4 v213, s[36:37]
	s_nop 0
	s_add_i32 m0, s48, 0x2000
	s_nop 0
	global_load_lds_dwordx4 v214, s[36:37]
	s_waitcnt vmcnt(8) lgkmcnt(0)
	s_barrier
	v_mfma_f32_16x16x32_bf16 v[128:131], v[0:3], v[60:63], 0
	v_mfma_f32_16x16x32_bf16 v[132:135], v[4:7], v[88:91], v[128:131]
	v_mfma_f32_16x16x32_bf16 v[128:131], v[8:11], v[60:63], 0
	v_mfma_f32_16x16x32_bf16 v[140:143], v[12:15], v[88:91], v[128:131]
	v_mfma_f32_16x16x32_bf16 v[128:131], v[0:3], v[92:95], 0
	v_mfma_f32_16x16x32_bf16 v[148:151], v[4:7], v[108:111], v[128:131]
	v_mfma_f32_16x16x32_bf16 v[128:131], v[8:11], v[92:95], 0
	v_mfma_f32_16x16x32_bf16 v[156:159], v[12:15], v[108:111], v[128:131]
	v_mfma_f32_16x16x32_bf16 v[128:131], v[0:3], v[112:115], 0
	v_mfma_f32_16x16x32_bf16 v[0:3], v[0:3], v[120:123], 0
	v_mfma_f32_16x16x32_bf16 v[160:163], v[4:7], v[116:119], v[128:131]
	v_mfma_f32_16x16x32_bf16 v[0:3], v[4:7], v[124:127], v[0:3]
	v_mfma_f32_16x16x32_bf16 v[4:7], v[8:11], v[120:123], 0
	v_mfma_f32_16x16x32_bf16 v[128:131], v[8:11], v[112:115], 0
	v_mfma_f32_16x16x32_bf16 v[4:7], v[12:15], v[124:127], v[4:7]
	v_mfma_f32_16x16x32_bf16 v[164:167], v[12:15], v[116:119], v[128:131]
	v_mfma_f32_16x16x32_bf16 v[8:11], v[16:19], v[60:63], 0
	v_mfma_f32_16x16x32_bf16 v[168:171], v[20:23], v[88:91], v[8:11]
	v_mfma_f32_16x16x32_bf16 v[8:11], v[24:27], v[60:63], 0
	v_mfma_f32_16x16x32_bf16 v[172:175], v[28:31], v[88:91], v[8:11]
	v_mfma_f32_16x16x32_bf16 v[8:11], v[16:19], v[92:95], 0
	v_mfma_f32_16x16x32_bf16 v[176:179], v[20:23], v[108:111], v[8:11]
	v_mfma_f32_16x16x32_bf16 v[8:11], v[24:27], v[92:95], 0
	v_mfma_f32_16x16x32_bf16 v[108:111], v[28:31], v[108:111], v[8:11]
	v_mfma_f32_16x16x32_bf16 v[8:11], v[16:19], v[112:115], 0
	v_mfma_f32_16x16x32_bf16 v[180:183], v[20:23], v[116:119], v[8:11]
	v_mfma_f32_16x16x32_bf16 v[8:11], v[24:27], v[112:115], 0
	v_mfma_f32_16x16x32_bf16 v[116:119], v[28:31], v[116:119], v[8:11]
	v_mfma_f32_16x16x32_bf16 v[8:11], v[16:19], v[120:123], 0
	v_mfma_f32_16x16x32_bf16 v[184:187], v[20:23], v[124:127], v[8:11]
	v_mfma_f32_16x16x32_bf16 v[8:11], v[24:27], v[120:123], 0
	v_mfma_f32_16x16x32_bf16 v[124:127], v[28:31], v[124:127], v[8:11]
	s_barrier
	s_nop 4
	ds_read_b128 v[8:11], v220
	ds_read_b128 v[12:15], v220 offset:1024
	ds_read_b128 v[16:19], v220 offset:2048
	ds_read_b128 v[20:23], v220 offset:3072
	ds_read_b128 v[194:197], v221
	ds_read_b128 v[198:201], v221 offset:1024
	ds_read_b128 v[202:205], v221 offset:2048
	ds_read_b128 v[206:209], v221 offset:3072
	ds_read_b128 v[24:27], v219 offset:32768
	ds_read_b128 v[28:31], v219 offset:33792
	ds_read_b128 v[60:63], v219 offset:34816
	ds_read_b128 v[224:227], v219 offset:35840
	ds_read_b128 v[228:231], v219 offset:36864
	ds_read_b128 v[232:235], v219 offset:37888
	ds_read_b128 v[236:239], v219 offset:38912
	ds_read_b128 v[240:243], v219 offset:39936
	s_add_u32 s34, s34, 0x80100
	s_addc_u32 s35, s35, 0
	s_add_i32 m0, s48, 0x4000
	s_nop 0
	global_load_lds_dwordx4 v213, s[34:35]
	s_nop 0
	s_add_i32 m0, s48, 0x6000
	s_nop 0
	global_load_lds_dwordx4 v214, s[34:35]
	s_waitcnt vmcnt(8) lgkmcnt(0)
	s_barrier
	v_mfma_f32_16x16x32_bf16 v[64:67], v[8:11], v[24:27], v[64:67]
	v_mfma_f32_16x16x32_bf16 v[152:155], v[12:15], v[28:31], v[64:67]
	v_mfma_f32_16x16x32_bf16 v[64:67], v[16:19], v[24:27], v[68:71]
	v_mfma_f32_16x16x32_bf16 v[144:147], v[20:23], v[28:31], v[64:67]
	v_mfma_f32_16x16x32_bf16 v[64:67], v[8:11], v[60:63], v[72:75]
	v_mfma_f32_16x16x32_bf16 v[120:123], v[12:15], v[224:227], v[64:67]
	v_mfma_f32_16x16x32_bf16 v[64:67], v[16:19], v[60:63], v[76:79]
	v_mfma_f32_16x16x32_bf16 v[112:115], v[20:23], v[224:227], v[64:67]
	v_mfma_f32_16x16x32_bf16 v[64:67], v[8:11], v[228:231], v[80:83]
	v_mfma_f32_16x16x32_bf16 v[92:95], v[12:15], v[232:235], v[64:67]
	v_mfma_f32_16x16x32_bf16 v[64:67], v[16:19], v[228:231], v[84:87]
	v_mfma_f32_16x16x32_bf16 v[88:91], v[20:23], v[232:235], v[64:67]
	v_mfma_f32_16x16x32_bf16 v[64:67], v[8:11], v[236:239], v[96:99]
	v_mfma_f32_16x16x32_bf16 v[76:79], v[12:15], v[240:243], v[64:67]
	v_mfma_f32_16x16x32_bf16 v[64:67], v[16:19], v[236:239], v[100:103]
	v_mfma_f32_16x16x32_bf16 v[72:75], v[20:23], v[240:243], v[64:67]
	v_mfma_f32_16x16x32_bf16 v[64:67], v[194:197], v[24:27], v[104:107]
	v_mfma_f32_16x16x32_bf16 v[24:27], v[202:205], v[24:27], v[32:35]
	v_mfma_f32_16x16x32_bf16 v[128:131], v[206:209], v[28:31], v[24:27]
	v_mfma_f32_16x16x32_bf16 v[24:27], v[194:197], v[60:63], v[36:39]
	v_mfma_f32_16x16x32_bf16 v[104:107], v[198:201], v[224:227], v[24:27]
	v_mfma_f32_16x16x32_bf16 v[24:27], v[202:205], v[60:63], v[40:43]
	v_mfma_f32_16x16x32_bf16 v[96:99], v[206:209], v[224:227], v[24:27]
	v_mfma_f32_16x16x32_bf16 v[24:27], v[194:197], v[228:231], v[44:47]
	v_mfma_f32_16x16x32_bf16 v[84:87], v[198:201], v[232:235], v[24:27]
	v_mfma_f32_16x16x32_bf16 v[24:27], v[202:205], v[228:231], v[48:51]
	v_mfma_f32_16x16x32_bf16 v[80:83], v[206:209], v[232:235], v[24:27]
	v_mfma_f32_16x16x32_bf16 v[24:27], v[194:197], v[236:239], v[52:55]
	v_mfma_f32_16x16x32_bf16 v[68:71], v[198:201], v[240:243], v[24:27]
	v_mfma_f32_16x16x32_bf16 v[24:27], v[202:205], v[236:239], v[56:59]
	v_mfma_f32_16x16x32_bf16 v[136:139], v[198:201], v[28:31], v[64:67]
	v_mfma_f32_16x16x32_bf16 v[64:67], v[206:209], v[240:243], v[24:27]
	s_barrier
	ds_read_b128 v[32:35], v219 offset:49152
	ds_read_b128 v[36:39], v219 offset:50176
	ds_read_b128 v[100:103], v219 offset:51200
	ds_read_b128 v[224:227], v219 offset:52224
	ds_read_b128 v[228:231], v219 offset:53248
	ds_read_b128 v[232:235], v219 offset:54272
	ds_read_b128 v[236:239], v219 offset:55296
	ds_read_b128 v[240:243], v219 offset:56320
	s_add_i32 m0, s48, 0x18000
	s_nop 0
	global_load_lds_dwordx4 v213, s[40:41]
	s_nop 0
	s_add_i32 m0, s48, 0x1a000
	s_nop 0
	global_load_lds_dwordx4 v214, s[40:41]
	s_add_u32 s34, s30, 0x80180
	s_addc_u32 s35, s31, 0
	s_add_i32 m0, s48, 0x1c000
	s_nop 0
	global_load_lds_dwordx4 v213, s[34:35]
	s_nop 0
	s_add_i32 m0, s48, 0x1e000
	s_nop 0
	global_load_lds_dwordx4 v214, s[34:35]
	s_nop 0
	s_add_i32 m0, s48, 0x8000
	s_nop 0
	global_load_lds_dwordx4 v213, s[38:39]
	s_nop 0
	s_add_i32 m0, s48, 0xa000
	s_nop 0
	global_load_lds_dwordx4 v214, s[38:39]
	s_waitcnt vmcnt(8) lgkmcnt(0)
	s_barrier
	v_mfma_f32_16x16x32_bf16 v[24:27], v[8:11], v[32:35], v[132:135]
	v_mfma_f32_16x16x32_bf16 v[60:63], v[12:15], v[36:39], v[24:27]
	v_mfma_f32_16x16x32_bf16 v[24:27], v[16:19], v[32:35], v[140:143]
	v_mfma_f32_16x16x32_bf16 v[56:59], v[20:23], v[36:39], v[24:27]
	v_mfma_f32_16x16x32_bf16 v[24:27], v[8:11], v[100:103], v[148:151]
	v_mfma_f32_16x16x32_bf16 v[44:47], v[12:15], v[224:227], v[24:27]
	v_mfma_f32_16x16x32_bf16 v[24:27], v[16:19], v[100:103], v[156:159]
	v_mfma_f32_16x16x32_bf16 v[40:43], v[20:23], v[224:227], v[24:27]
	v_mfma_f32_16x16x32_bf16 v[24:27], v[8:11], v[228:231], v[160:163]
	v_mfma_f32_16x16x32_bf16 v[0:3], v[8:11], v[236:239], v[0:3]
	v_mfma_f32_16x16x32_bf16 v[28:31], v[12:15], v[232:235], v[24:27]
	v_mfma_f32_16x16x32_bf16 v[24:27], v[16:19], v[228:231], v[164:167]
	v_mfma_f32_16x16x32_bf16 v[12:15], v[12:15], v[240:243], v[0:3]
	v_mfma_f32_16x16x32_bf16 v[0:3], v[16:19], v[236:239], v[4:7]
	v_mfma_f32_16x16x32_bf16 v[24:27], v[20:23], v[232:235], v[24:27]
	v_mfma_f32_16x16x32_bf16 v[8:11], v[20:23], v[240:243], v[0:3]
	v_mfma_f32_16x16x32_bf16 v[0:3], v[194:197], v[32:35], v[168:171]
	v_mfma_f32_16x16x32_bf16 v[52:55], v[198:201], v[36:39], v[0:3]
	v_mfma_f32_16x16x32_bf16 v[0:3], v[202:205], v[32:35], v[172:175]
	v_mfma_f32_16x16x32_bf16 v[48:51], v[206:209], v[36:39], v[0:3]
	v_mfma_f32_16x16x32_bf16 v[0:3], v[194:197], v[100:103], v[176:179]
	v_mfma_f32_16x16x32_bf16 v[36:39], v[198:201], v[224:227], v[0:3]
	v_mfma_f32_16x16x32_bf16 v[0:3], v[202:205], v[100:103], v[108:111]
	v_mfma_f32_16x16x32_bf16 v[32:35], v[206:209], v[224:227], v[0:3]
	v_mfma_f32_16x16x32_bf16 v[0:3], v[194:197], v[228:231], v[180:183]
	v_mfma_f32_16x16x32_bf16 v[20:23], v[198:201], v[232:235], v[0:3]
	v_mfma_f32_16x16x32_bf16 v[0:3], v[202:205], v[228:231], v[116:119]
	v_mfma_f32_16x16x32_bf16 v[16:19], v[206:209], v[232:235], v[0:3]
	v_mfma_f32_16x16x32_bf16 v[0:3], v[194:197], v[236:239], v[184:187]
	v_mfma_f32_16x16x32_bf16 v[4:7], v[198:201], v[240:243], v[0:3]
	v_mfma_f32_16x16x32_bf16 v[0:3], v[202:205], v[236:239], v[124:127]
	v_mfma_f32_16x16x32_bf16 v[0:3], v[206:209], v[240:243], v[0:3]
	s_barrier
	s_add_u32 s59, s30, 0x200
	s_addc_u32 s60, s31, 0
	s_mov_b32 s61, 0
.LBB0_603:
	ds_read_b128 v[100:103], v217
	ds_read_b128 v[108:111], v217 offset:1024
	ds_read_b128 v[116:119], v217 offset:2048
	ds_read_b128 v[124:127], v217 offset:3072
	ds_read_b128 v[132:135], v218
	ds_read_b128 v[140:143], v218 offset:1024
	ds_read_b128 v[148:151], v218 offset:2048
	ds_read_b128 v[156:159], v218 offset:3072
	ds_read_b128 v[160:163], v219
	ds_read_b128 v[164:167], v219 offset:1024
	ds_read_b128 v[168:171], v219 offset:2048
	ds_read_b128 v[172:175], v219 offset:3072
	ds_read_b128 v[176:179], v219 offset:4096
	ds_read_b128 v[180:183], v219 offset:5120
	ds_read_b128 v[184:187], v219 offset:6144
	ds_read_b128 v[194:197], v219 offset:7168
	s_add_u32 s30, s36, 0x100
	s_addc_u32 s31, s37, 0
	s_cmp_eq_u32 s61, 28
	s_cselect_b32 s42, s9, s30
	s_cselect_b32 s43, s7, s31
	s_cselect_b32 s38, s25, s59
	s_cselect_b32 s39, s23, s60
	s_add_u32 s34, s42, 0x80
	s_addc_u32 s35, s43, 0
	s_add_u32 s40, s38, 0x80
	s_addc_u32 s41, s39, 0
	s_add_u32 s36, s36, 0x80080
	s_addc_u32 s37, s37, 0
	s_add_i32 m0, s48, 0xc000
	s_nop 0
	global_load_lds_dwordx4 v213, s[36:37]
	s_nop 0
	s_add_i32 m0, s48, 0xe000
	s_nop 0
	global_load_lds_dwordx4 v214, s[36:37]
	s_waitcnt vmcnt(8) lgkmcnt(0)
	s_barrier
	v_mfma_f32_16x16x32_bf16 v[152:155], v[100:103], v[160:163], v[152:155]
	v_mfma_f32_16x16x32_bf16 v[144:147], v[116:119], v[160:163], v[144:147]
	v_mfma_f32_16x16x32_bf16 v[112:115], v[116:119], v[168:171], v[112:115]
	v_mfma_f32_16x16x32_bf16 v[120:123], v[100:103], v[168:171], v[120:123]
	v_mfma_f32_16x16x32_bf16 v[92:95], v[100:103], v[176:179], v[92:95]
	v_mfma_f32_16x16x32_bf16 v[88:91], v[116:119], v[176:179], v[88:91]
	v_mfma_f32_16x16x32_bf16 v[72:75], v[116:119], v[184:187], v[72:75]
	v_mfma_f32_16x16x32_bf16 v[76:79], v[100:103], v[184:187], v[76:79]
	v_mfma_f32_16x16x32_bf16 v[152:155], v[108:111], v[164:167], v[152:155]
	v_mfma_f32_16x16x32_bf16 v[144:147], v[124:127], v[164:167], v[144:147]
	v_mfma_f32_16x16x32_bf16 v[112:115], v[124:127], v[172:175], v[112:115]
	v_mfma_f32_16x16x32_bf16 v[120:123], v[108:111], v[172:175], v[120:123]
	v_mfma_f32_16x16x32_bf16 v[92:95], v[108:111], v[180:183], v[92:95]
	v_mfma_f32_16x16x32_bf16 v[88:91], v[124:127], v[180:183], v[88:91]
	v_mfma_f32_16x16x32_bf16 v[72:75], v[124:127], v[194:197], v[72:75]
	v_mfma_f32_16x16x32_bf16 v[76:79], v[108:111], v[194:197], v[76:79]
	v_mfma_f32_16x16x32_bf16 v[136:139], v[132:135], v[160:163], v[136:139]
	v_mfma_f32_16x16x32_bf16 v[128:131], v[148:151], v[160:163], v[128:131]
	v_mfma_f32_16x16x32_bf16 v[96:99], v[148:151], v[168:171], v[96:99]
	v_mfma_f32_16x16x32_bf16 v[104:107], v[132:135], v[168:171], v[104:107]
	v_mfma_f32_16x16x32_bf16 v[84:87], v[132:135], v[176:179], v[84:87]
	v_mfma_f32_16x16x32_bf16 v[80:83], v[148:151], v[176:179], v[80:83]
	v_mfma_f32_16x16x32_bf16 v[64:67], v[148:151], v[184:187], v[64:67]
	v_mfma_f32_16x16x32_bf16 v[68:71], v[132:135], v[184:187], v[68:71]
	v_mfma_f32_16x16x32_bf16 v[136:139], v[140:143], v[164:167], v[136:139]
	v_mfma_f32_16x16x32_bf16 v[128:131], v[156:159], v[164:167], v[128:131]
	v_mfma_f32_16x16x32_bf16 v[96:99], v[156:159], v[172:175], v[96:99]
	v_mfma_f32_16x16x32_bf16 v[104:107], v[140:143], v[172:175], v[104:107]
	v_mfma_f32_16x16x32_bf16 v[84:87], v[140:143], v[180:183], v[84:87]
	v_mfma_f32_16x16x32_bf16 v[80:83], v[156:159], v[180:183], v[80:83]
	v_mfma_f32_16x16x32_bf16 v[64:67], v[156:159], v[194:197], v[64:67]
	v_mfma_f32_16x16x32_bf16 v[68:71], v[140:143], v[194:197], v[68:71]
	s_barrier
	ds_read_b128 v[160:163], v219 offset:16384
	ds_read_b128 v[164:167], v219 offset:17408
	ds_read_b128 v[168:171], v219 offset:18432
	ds_read_b128 v[172:175], v219 offset:19456
	ds_read_b128 v[176:179], v219 offset:20480
	ds_read_b128 v[180:183], v219 offset:21504
	ds_read_b128 v[184:187], v219 offset:22528
	ds_read_b128 v[194:197], v219 offset:23552
	s_add_i32 m0, s48, 0x10000
	s_nop 0
	global_load_lds_dwordx4 v213, s[38:39]
	s_nop 0
	s_add_i32 m0, s48, 0x12000
	s_nop 0
	global_load_lds_dwordx4 v214, s[38:39]
	s_add_u32 s36, s38, 0x80000
	s_addc_u32 s37, s39, 0
	s_add_i32 m0, s48, 0x14000
	s_nop 0
	global_load_lds_dwordx4 v213, s[36:37]
	s_nop 0
	s_add_i32 m0, s48, 0x16000
	s_nop 0
	global_load_lds_dwordx4 v214, s[36:37]
	s_nop 0
	s_add_i32 m0, s48, 0
	s_nop 0
	global_load_lds_dwordx4 v213, s[42:43]
	s_nop 0
	s_add_i32 m0, s48, 0x2000
	s_nop 0
	global_load_lds_dwordx4 v214, s[42:43]
	s_waitcnt vmcnt(8) lgkmcnt(0)
	s_barrier
	v_mfma_f32_16x16x32_bf16 v[60:63], v[100:103], v[160:163], v[60:63]
	v_mfma_f32_16x16x32_bf16 v[56:59], v[116:119], v[160:163], v[56:59]
	v_mfma_f32_16x16x32_bf16 v[40:43], v[116:119], v[168:171], v[40:43]
	v_mfma_f32_16x16x32_bf16 v[44:47], v[100:103], v[168:171], v[44:47]
	v_mfma_f32_16x16x32_bf16 v[28:31], v[100:103], v[176:179], v[28:31]
	v_mfma_f32_16x16x32_bf16 v[24:27], v[116:119], v[176:179], v[24:27]
	v_mfma_f32_16x16x32_bf16 v[8:11], v[116:119], v[184:187], v[8:11]
	v_mfma_f32_16x16x32_bf16 v[12:15], v[100:103], v[184:187], v[12:15]
	v_mfma_f32_16x16x32_bf16 v[60:63], v[108:111], v[164:167], v[60:63]
	v_mfma_f32_16x16x32_bf16 v[56:59], v[124:127], v[164:167], v[56:59]
	v_mfma_f32_16x16x32_bf16 v[40:43], v[124:127], v[172:175], v[40:43]
	v_mfma_f32_16x16x32_bf16 v[44:47], v[108:111], v[172:175], v[44:47]
	v_mfma_f32_16x16x32_bf16 v[28:31], v[108:111], v[180:183], v[28:31]
	v_mfma_f32_16x16x32_bf16 v[24:27], v[124:127], v[180:183], v[24:27]
	v_mfma_f32_16x16x32_bf16 v[8:11], v[124:127], v[194:197], v[8:11]
	v_mfma_f32_16x16x32_bf16 v[12:15], v[108:111], v[194:197], v[12:15]
	v_mfma_f32_16x16x32_bf16 v[52:55], v[132:135], v[160:163], v[52:55]
	v_mfma_f32_16x16x32_bf16 v[48:51], v[148:151], v[160:163], v[48:51]
	v_mfma_f32_16x16x32_bf16 v[32:35], v[148:151], v[168:171], v[32:35]
	v_mfma_f32_16x16x32_bf16 v[36:39], v[132:135], v[168:171], v[36:39]
	v_mfma_f32_16x16x32_bf16 v[20:23], v[132:135], v[176:179], v[20:23]
	v_mfma_f32_16x16x32_bf16 v[16:19], v[148:151], v[176:179], v[16:19]
	v_mfma_f32_16x16x32_bf16 v[0:3], v[148:151], v[184:187], v[0:3]
	v_mfma_f32_16x16x32_bf16 v[4:7], v[132:135], v[184:187], v[4:7]
	v_mfma_f32_16x16x32_bf16 v[52:55], v[140:143], v[164:167], v[52:55]
	v_mfma_f32_16x16x32_bf16 v[48:51], v[156:159], v[164:167], v[48:51]
	v_mfma_f32_16x16x32_bf16 v[32:35], v[156:159], v[172:175], v[32:35]
	v_mfma_f32_16x16x32_bf16 v[36:39], v[140:143], v[172:175], v[36:39]
	v_mfma_f32_16x16x32_bf16 v[20:23], v[140:143], v[180:183], v[20:23]
	v_mfma_f32_16x16x32_bf16 v[16:19], v[156:159], v[180:183], v[16:19]
	v_mfma_f32_16x16x32_bf16 v[0:3], v[156:159], v[194:197], v[0:3]
	v_mfma_f32_16x16x32_bf16 v[4:7], v[140:143], v[194:197], v[4:7]
	s_barrier
	ds_read_b128 v[100:103], v220
	ds_read_b128 v[108:111], v220 offset:1024
	ds_read_b128 v[116:119], v220 offset:2048
	ds_read_b128 v[124:127], v220 offset:3072
	ds_read_b128 v[132:135], v221
	ds_read_b128 v[140:143], v221 offset:1024
	ds_read_b128 v[148:151], v221 offset:2048
	ds_read_b128 v[156:159], v221 offset:3072
	ds_read_b128 v[160:163], v219 offset:32768
	ds_read_b128 v[164:167], v219 offset:33792
	ds_read_b128 v[168:171], v219 offset:34816
	ds_read_b128 v[172:175], v219 offset:35840
	ds_read_b128 v[176:179], v219 offset:36864
	ds_read_b128 v[180:183], v219 offset:37888
	ds_read_b128 v[184:187], v219 offset:38912
	ds_read_b128 v[194:197], v219 offset:39936
	s_add_u32 s36, s42, 0x80000
	s_addc_u32 s37, s43, 0
	s_add_i32 m0, s48, 0x4000
	s_nop 0
	global_load_lds_dwordx4 v213, s[36:37]
	s_nop 0
	s_add_i32 m0, s48, 0x6000
	s_nop 0
	global_load_lds_dwordx4 v214, s[36:37]
	s_waitcnt vmcnt(8) lgkmcnt(0)
	s_barrier
	v_mfma_f32_16x16x32_bf16 v[152:155], v[100:103], v[160:163], v[152:155]
	v_mfma_f32_16x16x32_bf16 v[144:147], v[116:119], v[160:163], v[144:147]
	v_mfma_f32_16x16x32_bf16 v[112:115], v[116:119], v[168:171], v[112:115]
	v_mfma_f32_16x16x32_bf16 v[120:123], v[100:103], v[168:171], v[120:123]
	v_mfma_f32_16x16x32_bf16 v[92:95], v[100:103], v[176:179], v[92:95]
	v_mfma_f32_16x16x32_bf16 v[88:91], v[116:119], v[176:179], v[88:91]
	v_mfma_f32_16x16x32_bf16 v[72:75], v[116:119], v[184:187], v[72:75]
	v_mfma_f32_16x16x32_bf16 v[76:79], v[100:103], v[184:187], v[76:79]
	v_mfma_f32_16x16x32_bf16 v[152:155], v[108:111], v[164:167], v[152:155]
	v_mfma_f32_16x16x32_bf16 v[144:147], v[124:127], v[164:167], v[144:147]
	v_mfma_f32_16x16x32_bf16 v[112:115], v[124:127], v[172:175], v[112:115]
	v_mfma_f32_16x16x32_bf16 v[120:123], v[108:111], v[172:175], v[120:123]
	v_mfma_f32_16x16x32_bf16 v[92:95], v[108:111], v[180:183], v[92:95]
	v_mfma_f32_16x16x32_bf16 v[88:91], v[124:127], v[180:183], v[88:91]
	v_mfma_f32_16x16x32_bf16 v[72:75], v[124:127], v[194:197], v[72:75]
	v_mfma_f32_16x16x32_bf16 v[76:79], v[108:111], v[194:197], v[76:79]
	v_mfma_f32_16x16x32_bf16 v[136:139], v[132:135], v[160:163], v[136:139]
	v_mfma_f32_16x16x32_bf16 v[128:131], v[148:151], v[160:163], v[128:131]
	v_mfma_f32_16x16x32_bf16 v[96:99], v[148:151], v[168:171], v[96:99]
	v_mfma_f32_16x16x32_bf16 v[104:107], v[132:135], v[168:171], v[104:107]
	v_mfma_f32_16x16x32_bf16 v[84:87], v[132:135], v[176:179], v[84:87]
	v_mfma_f32_16x16x32_bf16 v[80:83], v[148:151], v[176:179], v[80:83]
	v_mfma_f32_16x16x32_bf16 v[64:67], v[148:151], v[184:187], v[64:67]
	v_mfma_f32_16x16x32_bf16 v[68:71], v[132:135], v[184:187], v[68:71]
	v_mfma_f32_16x16x32_bf16 v[136:139], v[140:143], v[164:167], v[136:139]
	v_mfma_f32_16x16x32_bf16 v[128:131], v[156:159], v[164:167], v[128:131]
	v_mfma_f32_16x16x32_bf16 v[96:99], v[156:159], v[172:175], v[96:99]
	v_mfma_f32_16x16x32_bf16 v[104:107], v[140:143], v[172:175], v[104:107]
	v_mfma_f32_16x16x32_bf16 v[84:87], v[140:143], v[180:183], v[84:87]
	v_mfma_f32_16x16x32_bf16 v[80:83], v[156:159], v[180:183], v[80:83]
	v_mfma_f32_16x16x32_bf16 v[64:67], v[156:159], v[194:197], v[64:67]
	v_mfma_f32_16x16x32_bf16 v[68:71], v[140:143], v[194:197], v[68:71]
	s_barrier
	ds_read_b128 v[160:163], v219 offset:49152
	ds_read_b128 v[164:167], v219 offset:50176
	ds_read_b128 v[168:171], v219 offset:51200
	ds_read_b128 v[172:175], v219 offset:52224
	ds_read_b128 v[176:179], v219 offset:53248
	ds_read_b128 v[180:183], v219 offset:54272
	ds_read_b128 v[184:187], v219 offset:55296
	ds_read_b128 v[194:197], v219 offset:56320
	s_add_i32 m0, s48, 0x18000
	s_nop 0
	global_load_lds_dwordx4 v213, s[40:41]
	s_nop 0
	s_add_i32 m0, s48, 0x1a000
	s_nop 0
	global_load_lds_dwordx4 v214, s[40:41]
	s_add_u32 s36, s38, 0x80080
	s_addc_u32 s37, s39, 0
	s_add_i32 m0, s48, 0x1c000
	s_nop 0
	global_load_lds_dwordx4 v213, s[36:37]
	s_nop 0
	s_add_i32 m0, s48, 0x1e000
	s_nop 0
	global_load_lds_dwordx4 v214, s[36:37]
	s_nop 0
	s_add_i32 m0, s48, 0x8000
	s_nop 0
	global_load_lds_dwordx4 v213, s[34:35]
	s_nop 0
	s_add_i32 m0, s48, 0xa000
	s_nop 0
	global_load_lds_dwordx4 v214, s[34:35]
	s_waitcnt vmcnt(8) lgkmcnt(0)
	s_barrier
	v_mfma_f32_16x16x32_bf16 v[60:63], v[100:103], v[160:163], v[60:63]
	v_mfma_f32_16x16x32_bf16 v[56:59], v[116:119], v[160:163], v[56:59]
	v_mfma_f32_16x16x32_bf16 v[40:43], v[116:119], v[168:171], v[40:43]
	v_mfma_f32_16x16x32_bf16 v[44:47], v[100:103], v[168:171], v[44:47]
	v_mfma_f32_16x16x32_bf16 v[28:31], v[100:103], v[176:179], v[28:31]
	v_mfma_f32_16x16x32_bf16 v[24:27], v[116:119], v[176:179], v[24:27]
	v_mfma_f32_16x16x32_bf16 v[8:11], v[116:119], v[184:187], v[8:11]
	v_mfma_f32_16x16x32_bf16 v[12:15], v[100:103], v[184:187], v[12:15]
	v_mfma_f32_16x16x32_bf16 v[60:63], v[108:111], v[164:167], v[60:63]
	v_mfma_f32_16x16x32_bf16 v[56:59], v[124:127], v[164:167], v[56:59]
	v_mfma_f32_16x16x32_bf16 v[40:43], v[124:127], v[172:175], v[40:43]
	v_mfma_f32_16x16x32_bf16 v[44:47], v[108:111], v[172:175], v[44:47]
	v_mfma_f32_16x16x32_bf16 v[28:31], v[108:111], v[180:183], v[28:31]
	v_mfma_f32_16x16x32_bf16 v[24:27], v[124:127], v[180:183], v[24:27]
	v_mfma_f32_16x16x32_bf16 v[8:11], v[124:127], v[194:197], v[8:11]
	v_mfma_f32_16x16x32_bf16 v[12:15], v[108:111], v[194:197], v[12:15]
	v_mfma_f32_16x16x32_bf16 v[52:55], v[132:135], v[160:163], v[52:55]
	v_mfma_f32_16x16x32_bf16 v[48:51], v[148:151], v[160:163], v[48:51]
	v_mfma_f32_16x16x32_bf16 v[32:35], v[148:151], v[168:171], v[32:35]
	v_mfma_f32_16x16x32_bf16 v[36:39], v[132:135], v[168:171], v[36:39]
	v_mfma_f32_16x16x32_bf16 v[20:23], v[132:135], v[176:179], v[20:23]
	v_mfma_f32_16x16x32_bf16 v[16:19], v[148:151], v[176:179], v[16:19]
	v_mfma_f32_16x16x32_bf16 v[0:3], v[148:151], v[184:187], v[0:3]
	v_mfma_f32_16x16x32_bf16 v[4:7], v[132:135], v[184:187], v[4:7]
	v_mfma_f32_16x16x32_bf16 v[52:55], v[140:143], v[164:167], v[52:55]
	v_mfma_f32_16x16x32_bf16 v[48:51], v[156:159], v[164:167], v[48:51]
	v_mfma_f32_16x16x32_bf16 v[32:35], v[156:159], v[172:175], v[32:35]
	v_mfma_f32_16x16x32_bf16 v[36:39], v[140:143], v[172:175], v[36:39]
	v_mfma_f32_16x16x32_bf16 v[20:23], v[140:143], v[180:183], v[20:23]
	v_mfma_f32_16x16x32_bf16 v[16:19], v[156:159], v[180:183], v[16:19]
	v_mfma_f32_16x16x32_bf16 v[0:3], v[156:159], v[194:197], v[0:3]
	v_mfma_f32_16x16x32_bf16 v[4:7], v[140:143], v[194:197], v[4:7]
	s_barrier
	s_add_i32 s61, s61, 2
	s_add_u32 s59, s59, 0x100
	s_addc_u32 s60, s60, 0
	s_cmp_gt_u32 s61, 29
	s_mov_b64 s[36:37], s[30:31]
	s_cbranch_scc0 .LBB0_603
	s_and_b64 vcc, exec, s[20:21]
	s_cbranch_vccz .LBB0_606
	s_barrier

.LBB0_690:
	s_waitcnt vmcnt(0) lgkmcnt(0)
	s_barrier
	s_and_saveexec_b64 s[4:5], s[72:73]
	s_cbranch_execz .LBB0_742
	s_add_u32 s6, s70, 0x4200
	s_addc_u32 s7, s71, 0
	s_add_i32 s8, 0, 0x23f20
	v_mov_b32_e32 v0, s8
	s_waitcnt vmcnt(0) expcnt(0) lgkmcnt(0)
	ds_read_b32 v2, v0
	s_add_i32 s8, 0, 0x23f24
	v_mov_b32_e32 v0, s8
	ds_read_b32 v0, v0
	s_waitcnt lgkmcnt(1)
	v_cmp_ne_u32_e32 vcc, 0, v2
	s_cbranch_vccnz .LBB0_706
	s_add_u32 s8, s70, 0x4400
	s_addc_u32 s9, s71, 0
	s_add_u32 s10, s70, 0x4500
	s_addc_u32 s11, s71, 0
	s_add_u32 s14, s70, 0x4600
	s_addc_u32 s15, s71, 0
	s_add_u32 s16, s70, 0x4700
	s_addc_u32 s17, s71, 0
	s_add_u32 s18, s70, 0x4800
	s_addc_u32 s19, s71, 0
	s_add_u32 s20, s70, 0x4900
	s_addc_u32 s21, s71, 0
	s_add_u32 s22, s70, 0x4a00
	s_addc_u32 s23, s71, 0
	s_add_u32 s24, s70, 0x4b00
	s_addc_u32 s25, s71, 0
	s_add_u32 s26, s70, 0x4c00
	s_addc_u32 s27, s71, 0
	s_add_u32 s28, s70, 0x4d00
	s_addc_u32 s29, s71, 0
	s_add_u32 s30, s70, 0x4e00
	s_addc_u32 s31, s71, 0
	s_add_u32 s34, s70, 0x4f00
	s_addc_u32 s35, s71, 0
	s_add_u32 s36, s70, 0x5000
	s_addc_u32 s37, s71, 0
	s_load_dwordx2 s[44:45], s[90:91], 0x4
	s_add_u32 s38, s70, 0x5100
	s_addc_u32 s39, s71, 0
	s_add_u32 s40, s70, 0x5200
	s_addc_u32 s41, s71, 0
	s_add_u32 s42, s70, 0x5300
	s_waitcnt lgkmcnt(0)
	s_mul_i32 s50, s44, s33
	s_addc_u32 s43, s71, 0
	s_mul_i32 s50, s50, s45
	s_mov_b32 s51, 1
	v_mov_b32_e32 v16, 0
	s_branch .LBB0_694

.LBB0_752:
	s_ashr_i32 s17, s16, 31
	s_lshl_b64 s[18:19], s[16:17], 19
	s_add_u32 s18, s40, s18
	s_addc_u32 s19, s41, s19
	s_and_b64 s[20:21], s[4:5], exec
	s_cselect_b32 s58, s19, s29
	s_cselect_b32 s59, s18, s28
	s_ashr_i32 s15, s14, 31
	s_lshl_b64 s[20:21], s[14:15], 19
	s_add_u32 s20, s42, s20
	s_addc_u32 s21, s43, s21
	s_and_b64 s[26:27], s[4:5], exec
	ds_read_b128 v[0:3], v204 offset:3072
	ds_read_b128 v[4:7], v204 offset:2048
	ds_read_b128 v[8:11], v204 offset:1024
	ds_read_b128 v[12:15], v204
	ds_read_b128 v[16:19], v205 offset:3072
	ds_read_b128 v[20:23], v205 offset:2048
	ds_read_b128 v[24:27], v205 offset:1024
	ds_read_b128 v[28:31], v205
	ds_read_b128 v[32:35], v206
	ds_read_b128 v[36:39], v206 offset:1024
	ds_read_b128 v[40:43], v206 offset:2048
	ds_read_b128 v[44:47], v206 offset:3072
	ds_read_b128 v[48:51], v206 offset:4096
	ds_read_b128 v[52:55], v206 offset:5120
	ds_read_b128 v[56:59], v206 offset:6144
	ds_read_b128 v[60:63], v206 offset:7168
	s_cselect_b32 s15, s21, s25
	s_cselect_b32 s60, s20, s24
	s_lshl_b32 s26, s55, 11
	s_and_b32 s26, s26, 0x800
	s_or_b32 s38, s26, s49
	s_lshl_b64 s[30:31], s[16:17], 11
	s_add_u32 s26, s28, 0x100
	s_addc_u32 s27, s29, 0
	s_add_u32 s62, s24, 0x100
	s_addc_u32 s63, s25, 0
	s_add_u32 s34, s28, 0x180
	s_addc_u32 s35, s29, 0
	s_add_u32 s36, s24, 0x180
	s_addc_u32 s37, s25, 0
	s_add_u32 s66, s28, 0x40080
	s_addc_u32 s67, s29, 0
	s_add_i32 m0, s46, 0xc000
	s_nop 0
	global_load_lds_dwordx4 v199, s[66:67]
	s_nop 0
	s_add_i32 m0, s46, 0xe000
	s_nop 0
	global_load_lds_dwordx4 v201, s[66:67]
	s_waitcnt vmcnt(8) lgkmcnt(0)
	s_barrier
	s_waitcnt lgkmcnt(7)
	v_mfma_i32_16x16x64_i8 v[64:67], v[28:31], v[32:35], 0
	s_mov_b32 s17, 0
	v_mfma_i32_16x16x64_i8 v[68:71], v[20:23], v[32:35], 0
	s_waitcnt lgkmcnt(5)
	v_mfma_i32_16x16x64_i8 v[72:75], v[28:31], v[40:43], 0
	v_mfma_i32_16x16x64_i8 v[132:135], v[24:27], v[36:39], v[64:67]
	v_mfma_i32_16x16x64_i8 v[136:139], v[16:19], v[36:39], v[68:71]
	s_waitcnt lgkmcnt(4)
	v_mfma_i32_16x16x64_i8 v[144:147], v[24:27], v[44:47], v[72:75]
	v_mfma_i32_16x16x64_i8 v[76:79], v[20:23], v[40:43], 0
	s_waitcnt lgkmcnt(3)
	v_mfma_i32_16x16x64_i8 v[80:83], v[28:31], v[48:51], 0
	v_mfma_i32_16x16x64_i8 v[84:87], v[20:23], v[48:51], 0
	s_waitcnt lgkmcnt(1)
	v_mfma_i32_16x16x64_i8 v[88:91], v[28:31], v[56:59], 0
	v_mfma_i32_16x16x64_i8 v[92:95], v[20:23], v[56:59], 0
	v_mfma_i32_16x16x64_i8 v[76:79], v[16:19], v[44:47], v[76:79]
	v_mfma_i32_16x16x64_i8 v[80:83], v[24:27], v[52:55], v[80:83]
	v_mfma_i32_16x16x64_i8 v[84:87], v[16:19], v[52:55], v[84:87]
	s_waitcnt lgkmcnt(0)
	v_mfma_i32_16x16x64_i8 v[88:91], v[24:27], v[60:63], v[88:91]
	v_mfma_i32_16x16x64_i8 v[92:95], v[16:19], v[60:63], v[92:95]
	v_mfma_i32_16x16x64_i8 v[96:99], v[12:15], v[32:35], 0
	v_mfma_i32_16x16x64_i8 v[32:35], v[4:7], v[32:35], 0
	v_mfma_i32_16x16x64_i8 v[96:99], v[8:11], v[36:39], v[96:99]
	v_mfma_i32_16x16x64_i8 v[32:35], v[0:3], v[36:39], v[32:35]
	v_mfma_i32_16x16x64_i8 v[36:39], v[12:15], v[40:43], 0
	v_mfma_i32_16x16x64_i8 v[40:43], v[4:7], v[40:43], 0
	v_mfma_i32_16x16x64_i8 v[36:39], v[8:11], v[44:47], v[36:39]
	v_mfma_i32_16x16x64_i8 v[40:43], v[0:3], v[44:47], v[40:43]
	v_mfma_i32_16x16x64_i8 v[44:47], v[12:15], v[48:51], 0
	v_mfma_i32_16x16x64_i8 v[48:51], v[4:7], v[48:51], 0
	v_mfma_i32_16x16x64_i8 v[44:47], v[8:11], v[52:55], v[44:47]
	v_mfma_i32_16x16x64_i8 v[48:51], v[0:3], v[52:55], v[48:51]
	v_mfma_i32_16x16x64_i8 v[52:55], v[12:15], v[56:59], 0
	v_mfma_i32_16x16x64_i8 v[56:59], v[4:7], v[56:59], 0
	v_mfma_i32_16x16x64_i8 v[52:55], v[8:11], v[60:63], v[52:55]
	v_mfma_i32_16x16x64_i8 v[56:59], v[0:3], v[60:63], v[56:59]
	s_barrier
	ds_read_b128 v[60:63], v206 offset:16384
	ds_read_b128 v[100:103], v206 offset:17408
	ds_read_b128 v[104:107], v206 offset:18432
	ds_read_b128 v[108:111], v206 offset:19456
	ds_read_b128 v[112:115], v206 offset:20480
	ds_read_b128 v[116:119], v206 offset:21504
	ds_read_b128 v[120:123], v206 offset:22528
	ds_read_b128 v[124:127], v206 offset:23552
	s_add_i32 m0, s46, 0x10000
	s_nop 0
	global_load_lds_dwordx4 v200, s[62:63]
	s_nop 0
	s_add_i32 m0, s46, 0x12000
	s_nop 0
	global_load_lds_dwordx4 v202, s[62:63]
	s_add_u32 s62, s24, 0x40100
	s_addc_u32 s63, s25, 0
	s_add_i32 m0, s46, 0x14000
	s_nop 0
	global_load_lds_dwordx4 v200, s[62:63]
	s_nop 0
	s_add_i32 m0, s46, 0x16000
	s_nop 0
	global_load_lds_dwordx4 v202, s[62:63]
	s_nop 0
	s_add_i32 m0, s46, 0
	s_nop 0
	global_load_lds_dwordx4 v199, s[26:27]
	s_nop 0
	s_add_i32 m0, s46, 0x2000
	s_nop 0
	global_load_lds_dwordx4 v201, s[26:27]
	s_waitcnt vmcnt(8) lgkmcnt(0)
	s_barrier
	v_mfma_i32_16x16x64_i8 v[128:131], v[28:31], v[60:63], 0
	v_mfma_i32_16x16x64_i8 v[210:213], v[24:27], v[100:103], v[128:131]
	v_mfma_i32_16x16x64_i8 v[128:131], v[20:23], v[60:63], 0
	v_mfma_i32_16x16x64_i8 v[214:217], v[16:19], v[100:103], v[128:131]
	v_mfma_i32_16x16x64_i8 v[128:131], v[28:31], v[104:107], 0
	v_mfma_i32_16x16x64_i8 v[218:221], v[24:27], v[108:111], v[128:131]
	v_mfma_i32_16x16x64_i8 v[128:131], v[20:23], v[104:107], 0
	v_mfma_i32_16x16x64_i8 v[222:225], v[16:19], v[108:111], v[128:131]
	v_mfma_i32_16x16x64_i8 v[128:131], v[28:31], v[112:115], 0
	v_mfma_i32_16x16x64_i8 v[226:229], v[24:27], v[116:119], v[128:131]
	v_mfma_i32_16x16x64_i8 v[128:131], v[20:23], v[112:115], 0
	v_mfma_i32_16x16x64_i8 v[28:31], v[28:31], v[120:123], 0
	v_mfma_i32_16x16x64_i8 v[20:23], v[20:23], v[120:123], 0
	v_mfma_i32_16x16x64_i8 v[230:233], v[16:19], v[116:119], v[128:131]
	v_mfma_i32_16x16x64_i8 v[24:27], v[24:27], v[124:127], v[28:31]
	v_mfma_i32_16x16x64_i8 v[20:23], v[16:19], v[124:127], v[20:23]
	v_mfma_i32_16x16x64_i8 v[16:19], v[12:15], v[60:63], 0
	v_mfma_i32_16x16x64_i8 v[28:31], v[8:11], v[100:103], v[16:19]
	v_mfma_i32_16x16x64_i8 v[16:19], v[4:7], v[60:63], 0
	v_mfma_i32_16x16x64_i8 v[60:63], v[0:3], v[100:103], v[16:19]
	v_mfma_i32_16x16x64_i8 v[16:19], v[12:15], v[104:107], 0
	v_mfma_i32_16x16x64_i8 v[100:103], v[8:11], v[108:111], v[16:19]
	v_mfma_i32_16x16x64_i8 v[16:19], v[4:7], v[104:107], 0
	v_mfma_i32_16x16x64_i8 v[234:237], v[0:3], v[108:111], v[16:19]
	v_mfma_i32_16x16x64_i8 v[16:19], v[12:15], v[112:115], 0
	v_mfma_i32_16x16x64_i8 v[238:241], v[8:11], v[116:119], v[16:19]
	v_mfma_i32_16x16x64_i8 v[16:19], v[4:7], v[112:115], 0
	v_mfma_i32_16x16x64_i8 v[12:15], v[12:15], v[120:123], 0
	v_mfma_i32_16x16x64_i8 v[4:7], v[4:7], v[120:123], 0
	v_mfma_i32_16x16x64_i8 v[12:15], v[8:11], v[124:127], v[12:15]
	v_mfma_i32_16x16x64_i8 v[4:7], v[0:3], v[124:127], v[4:7]
	v_mfma_i32_16x16x64_i8 v[242:245], v[0:3], v[116:119], v[16:19]
	s_barrier
	ds_read_b128 v[0:3], v207
	ds_read_b128 v[8:11], v207 offset:1024
	ds_read_b128 v[108:111], v207 offset:2048
	ds_read_b128 v[116:119], v207 offset:3072
	ds_read_b128 v[246:249], v208
	ds_read_b128 v[250:253], v208 offset:1024
	ds_read_b128 v[192:195], v208 offset:2048
	ds_read_b128 v[64:67], v208 offset:3072
	ds_read_b128 v[16:19], v206 offset:32768
	ds_read_b128 v[104:107], v206 offset:33792
	ds_read_b128 v[112:115], v206 offset:34816
	ds_read_b128 v[120:123], v206 offset:35840
	ds_read_b128 v[124:127], v206 offset:36864
	ds_read_b128 v[140:143], v206 offset:37888
	ds_read_b128 v[68:71], v206 offset:38912
	ds_read_b128 v[72:75], v206 offset:39936
	s_add_u32 s28, s28, 0x40100
	s_addc_u32 s29, s29, 0
	s_add_i32 m0, s46, 0x4000
	s_nop 0
	global_load_lds_dwordx4 v199, s[28:29]
	s_nop 0
	s_add_i32 m0, s46, 0x6000
	s_nop 0
	global_load_lds_dwordx4 v201, s[28:29]
	s_waitcnt vmcnt(8) lgkmcnt(0)
	s_barrier
	v_mfma_i32_16x16x64_i8 v[76:79], v[108:111], v[112:115], v[76:79]
	v_mfma_i32_16x16x64_i8 v[128:131], v[0:3], v[16:19], v[132:135]
	v_mfma_i32_16x16x64_i8 v[160:163], v[116:119], v[120:123], v[76:79]
	v_mfma_i32_16x16x64_i8 v[76:79], v[0:3], v[124:127], v[80:83]
	v_mfma_i32_16x16x64_i8 v[184:187], v[8:11], v[104:107], v[128:131]
	v_mfma_i32_16x16x64_i8 v[128:131], v[108:111], v[16:19], v[136:139]
	v_mfma_i32_16x16x64_i8 v[152:155], v[8:11], v[140:143], v[76:79]
	v_mfma_i32_16x16x64_i8 v[76:79], v[108:111], v[124:127], v[84:87]
	v_mfma_i32_16x16x64_i8 v[176:179], v[116:119], v[104:107], v[128:131]
	v_mfma_i32_16x16x64_i8 v[128:131], v[0:3], v[112:115], v[144:147]
	v_mfma_i32_16x16x64_i8 v[144:147], v[116:119], v[140:143], v[76:79]
	v_mfma_i32_16x16x64_i8 v[76:79], v[0:3], v[68:71], v[88:91]
	v_mfma_i32_16x16x64_i8 v[136:139], v[8:11], v[72:75], v[76:79]
	v_mfma_i32_16x16x64_i8 v[76:79], v[108:111], v[68:71], v[92:95]
	v_mfma_i32_16x16x64_i8 v[168:171], v[8:11], v[120:123], v[128:131]
	v_mfma_i32_16x16x64_i8 v[128:131], v[116:119], v[72:75], v[76:79]
	v_mfma_i32_16x16x64_i8 v[76:79], v[246:249], v[16:19], v[96:99]
	v_mfma_i32_16x16x64_i8 v[16:19], v[192:195], v[16:19], v[32:35]
	v_mfma_i32_16x16x64_i8 v[180:183], v[64:67], v[104:107], v[16:19]
	v_mfma_i32_16x16x64_i8 v[16:19], v[246:249], v[112:115], v[36:39]
	v_mfma_i32_16x16x64_i8 v[172:175], v[250:253], v[120:123], v[16:19]
	v_mfma_i32_16x16x64_i8 v[16:19], v[192:195], v[112:115], v[40:43]
	v_mfma_i32_16x16x64_i8 v[164:167], v[64:67], v[120:123], v[16:19]
	v_mfma_i32_16x16x64_i8 v[16:19], v[246:249], v[124:127], v[44:47]
	v_mfma_i32_16x16x64_i8 v[156:159], v[250:253], v[140:143], v[16:19]
	v_mfma_i32_16x16x64_i8 v[16:19], v[192:195], v[124:127], v[48:51]
	v_mfma_i32_16x16x64_i8 v[148:151], v[64:67], v[140:143], v[16:19]
	v_mfma_i32_16x16x64_i8 v[16:19], v[246:249], v[68:71], v[52:55]
	v_mfma_i32_16x16x64_i8 v[140:143], v[250:253], v[72:75], v[16:19]
	v_mfma_i32_16x16x64_i8 v[16:19], v[192:195], v[68:71], v[56:59]
	v_mfma_i32_16x16x64_i8 v[188:191], v[250:253], v[104:107], v[76:79]
	v_mfma_i32_16x16x64_i8 v[132:135], v[64:67], v[72:75], v[16:19]
	s_barrier
	ds_read_b128 v[32:35], v206 offset:49152
	ds_read_b128 v[36:39], v206 offset:50176
	ds_read_b128 v[40:43], v206 offset:51200
	ds_read_b128 v[44:47], v206 offset:52224
	ds_read_b128 v[52:55], v206 offset:53248
	ds_read_b128 v[56:59], v206 offset:54272
	ds_read_b128 v[68:71], v206 offset:55296
	ds_read_b128 v[72:75], v206 offset:56320
	s_add_i32 m0, s46, 0x18000
	s_nop 0
	global_load_lds_dwordx4 v200, s[36:37]
	s_nop 0
	s_add_i32 m0, s46, 0x1a000
	s_nop 0
	global_load_lds_dwordx4 v202, s[36:37]
	s_add_u32 s28, s24, 0x40180
	s_addc_u32 s29, s25, 0
	s_add_i32 m0, s46, 0x1c000
	s_nop 0
	global_load_lds_dwordx4 v200, s[28:29]
	s_nop 0
	s_add_i32 m0, s46, 0x1e000
	s_nop 0
	global_load_lds_dwordx4 v202, s[28:29]
	s_nop 0
	s_add_i32 m0, s46, 0x8000
	s_nop 0
	global_load_lds_dwordx4 v199, s[34:35]
	s_nop 0
	s_add_i32 m0, s46, 0xa000
	s_nop 0
	global_load_lds_dwordx4 v201, s[34:35]
	s_waitcnt vmcnt(8) lgkmcnt(0)
	s_barrier
	v_mfma_i32_16x16x64_i8 v[16:19], v[0:3], v[32:35], v[210:213]
	v_mfma_i32_16x16x64_i8 v[120:123], v[8:11], v[36:39], v[16:19]
	v_mfma_i32_16x16x64_i8 v[16:19], v[108:111], v[32:35], v[214:217]
	v_mfma_i32_16x16x64_i8 v[112:115], v[116:119], v[36:39], v[16:19]
	v_mfma_i32_16x16x64_i8 v[16:19], v[0:3], v[40:43], v[218:221]
	v_mfma_i32_16x16x64_i8 v[104:107], v[8:11], v[44:47], v[16:19]
	v_mfma_i32_16x16x64_i8 v[16:19], v[108:111], v[40:43], v[222:225]
	v_mfma_i32_16x16x64_i8 v[96:99], v[116:119], v[44:47], v[16:19]
	v_mfma_i32_16x16x64_i8 v[16:19], v[0:3], v[52:55], v[226:229]
	v_mfma_i32_16x16x64_i8 v[0:3], v[0:3], v[68:71], v[24:27]
	v_mfma_i32_16x16x64_i8 v[48:51], v[8:11], v[56:59], v[16:19]
	v_mfma_i32_16x16x64_i8 v[16:19], v[108:111], v[52:55], v[230:233]
	v_mfma_i32_16x16x64_i8 v[8:11], v[8:11], v[72:75], v[0:3]
	v_mfma_i32_16x16x64_i8 v[0:3], v[108:111], v[68:71], v[20:23]
	v_mfma_i32_16x16x64_i8 v[16:19], v[116:119], v[56:59], v[16:19]
	v_mfma_i32_16x16x64_i8 v[0:3], v[116:119], v[72:75], v[0:3]
	v_mfma_i32_16x16x64_i8 v[20:23], v[246:249], v[32:35], v[28:31]
	v_mfma_i32_16x16x64_i8 v[124:127], v[250:253], v[36:39], v[20:23]
	v_mfma_i32_16x16x64_i8 v[20:23], v[192:195], v[32:35], v[60:63]
	v_mfma_i32_16x16x64_i8 v[116:119], v[64:67], v[36:39], v[20:23]
	v_mfma_i32_16x16x64_i8 v[20:23], v[246:249], v[40:43], v[100:103]
	v_mfma_i32_16x16x64_i8 v[108:111], v[250:253], v[44:47], v[20:23]
	v_mfma_i32_16x16x64_i8 v[20:23], v[192:195], v[40:43], v[234:237]
	v_mfma_i32_16x16x64_i8 v[100:103], v[64:67], v[44:47], v[20:23]
	v_mfma_i32_16x16x64_i8 v[20:23], v[246:249], v[52:55], v[238:241]
	v_mfma_i32_16x16x64_i8 v[60:63], v[250:253], v[56:59], v[20:23]
	v_mfma_i32_16x16x64_i8 v[20:23], v[192:195], v[52:55], v[242:245]
	v_mfma_i32_16x16x64_i8 v[12:15], v[246:249], v[68:71], v[12:15]
	v_mfma_i32_16x16x64_i8 v[4:7], v[192:195], v[68:71], v[4:7]
	v_mfma_i32_16x16x64_i8 v[44:47], v[64:67], v[56:59], v[20:23]
	v_mfma_i32_16x16x64_i8 v[12:15], v[250:253], v[72:75], v[12:15]
	v_mfma_i32_16x16x64_i8 v[4:7], v[64:67], v[72:75], v[4:7]
	s_barrier
	s_add_u32 s28, s44, s30
	s_addc_u32 s29, s45, s31
	s_add_u32 s61, s24, 0x200
	s_addc_u32 s62, s25, 0
	s_add_i32 s63, s38, 0
	s_add_i32 s63, s63, 0x20000

.LBB0_755:
	ds_read_b128 v[20:23], v205
	ds_read_b128 v[24:27], v205 offset:1024
	ds_read_b128 v[28:31], v205 offset:2048
	ds_read_b128 v[32:35], v205 offset:3072
	ds_read_b128 v[36:39], v204
	ds_read_b128 v[40:43], v204 offset:1024
	ds_read_b128 v[52:55], v204 offset:2048
	ds_read_b128 v[56:59], v204 offset:3072
	ds_read_b128 v[64:67], v206
	ds_read_b128 v[68:71], v206 offset:1024
	ds_read_b128 v[72:75], v206 offset:2048
	ds_read_b128 v[76:79], v206 offset:3072
	ds_read_b128 v[80:83], v206 offset:4096
	ds_read_b128 v[84:87], v206 offset:5120
	ds_read_b128 v[88:91], v206 offset:6144
	ds_read_b128 v[92:95], v206 offset:7168
	s_add_u32 s24, s26, 0x100
	s_addc_u32 s25, s27, 0
	s_and_b64 s[30:31], s[30:31], exec
	s_cselect_b32 s38, s59, s24
	s_cselect_b32 s39, s58, s25
	s_cselect_b32 s35, s15, s62
	s_cselect_b32 s34, s60, s61
	s_add_u32 s30, s38, 0x80
	s_addc_u32 s31, s39, 0
	s_add_u32 s36, s34, 0x80
	s_addc_u32 s37, s35, 0
	s_add_u32 s26, s26, 0x40080
	s_addc_u32 s27, s27, 0
	s_add_i32 m0, s46, 0xc000
	s_nop 0
	global_load_lds_dwordx4 v199, s[26:27]
	s_nop 0
	s_add_i32 m0, s46, 0xe000
	s_nop 0
	global_load_lds_dwordx4 v201, s[26:27]
	s_waitcnt vmcnt(8) lgkmcnt(0)
	s_barrier
	v_mfma_i32_16x16x64_i8 v[184:187], v[20:23], v[64:67], v[184:187]
	v_mfma_i32_16x16x64_i8 v[176:179], v[28:31], v[64:67], v[176:179]
	v_mfma_i32_16x16x64_i8 v[160:163], v[28:31], v[72:75], v[160:163]
	v_mfma_i32_16x16x64_i8 v[168:171], v[20:23], v[72:75], v[168:171]
	v_mfma_i32_16x16x64_i8 v[152:155], v[20:23], v[80:83], v[152:155]
	v_mfma_i32_16x16x64_i8 v[144:147], v[28:31], v[80:83], v[144:147]
	v_mfma_i32_16x16x64_i8 v[128:131], v[28:31], v[88:91], v[128:131]
	v_mfma_i32_16x16x64_i8 v[136:139], v[20:23], v[88:91], v[136:139]
	v_mfma_i32_16x16x64_i8 v[184:187], v[24:27], v[68:71], v[184:187]
	v_mfma_i32_16x16x64_i8 v[176:179], v[32:35], v[68:71], v[176:179]
	v_mfma_i32_16x16x64_i8 v[160:163], v[32:35], v[76:79], v[160:163]
	v_mfma_i32_16x16x64_i8 v[168:171], v[24:27], v[76:79], v[168:171]
	v_mfma_i32_16x16x64_i8 v[152:155], v[24:27], v[84:87], v[152:155]
	v_mfma_i32_16x16x64_i8 v[144:147], v[32:35], v[84:87], v[144:147]
	v_mfma_i32_16x16x64_i8 v[128:131], v[32:35], v[92:95], v[128:131]
	v_mfma_i32_16x16x64_i8 v[136:139], v[24:27], v[92:95], v[136:139]
	v_mfma_i32_16x16x64_i8 v[188:191], v[36:39], v[64:67], v[188:191]
	v_mfma_i32_16x16x64_i8 v[64:67], v[52:55], v[64:67], v[180:183]
	v_mfma_i32_16x16x64_i8 v[188:191], v[40:43], v[68:71], v[188:191]
	v_mfma_i32_16x16x64_i8 v[64:67], v[56:59], v[68:71], v[64:67]
	v_mfma_i32_16x16x64_i8 v[68:71], v[36:39], v[72:75], v[172:175]
	v_mfma_i32_16x16x64_i8 v[72:75], v[52:55], v[72:75], v[164:167]
	v_mfma_i32_16x16x64_i8 v[68:71], v[40:43], v[76:79], v[68:71]
	v_mfma_i32_16x16x64_i8 v[72:75], v[56:59], v[76:79], v[72:75]
	v_mfma_i32_16x16x64_i8 v[76:79], v[36:39], v[80:83], v[156:159]
	v_mfma_i32_16x16x64_i8 v[80:83], v[52:55], v[80:83], v[148:151]
	v_mfma_i32_16x16x64_i8 v[76:79], v[40:43], v[84:87], v[76:79]
	v_mfma_i32_16x16x64_i8 v[80:83], v[56:59], v[84:87], v[80:83]
	v_mfma_i32_16x16x64_i8 v[84:87], v[36:39], v[88:91], v[140:143]
	v_mfma_i32_16x16x64_i8 v[88:91], v[52:55], v[88:91], v[132:135]
	v_mfma_i32_16x16x64_i8 v[84:87], v[40:43], v[92:95], v[84:87]
	v_mfma_i32_16x16x64_i8 v[88:91], v[56:59], v[92:95], v[88:91]
	s_barrier
	ds_read_b128 v[92:95], v206 offset:16384
	ds_read_b128 v[132:135], v206 offset:17408
	ds_read_b128 v[140:143], v206 offset:18432
	ds_read_b128 v[148:151], v206 offset:19456
	ds_read_b128 v[156:159], v206 offset:20480
	ds_read_b128 v[164:167], v206 offset:21504
	ds_read_b128 v[172:175], v206 offset:22528
	ds_read_b128 v[180:183], v206 offset:23552
	s_add_i32 m0, s46, 0x10000
	s_nop 0
	global_load_lds_dwordx4 v200, s[34:35]
	s_nop 0
	s_add_i32 m0, s46, 0x12000
	s_nop 0
	global_load_lds_dwordx4 v202, s[34:35]
	s_add_u32 s26, s34, 0x40000
	s_addc_u32 s27, s35, 0
	s_add_i32 m0, s46, 0x14000
	s_nop 0
	global_load_lds_dwordx4 v200, s[26:27]
	s_nop 0
	s_add_i32 m0, s46, 0x16000
	s_nop 0
	global_load_lds_dwordx4 v202, s[26:27]
	s_nop 0
	s_add_i32 m0, s46, 0
	s_nop 0
	global_load_lds_dwordx4 v199, s[38:39]
	s_nop 0
	s_add_i32 m0, s46, 0x2000
	s_nop 0
	global_load_lds_dwordx4 v201, s[38:39]
	s_waitcnt vmcnt(8) lgkmcnt(0)
	s_barrier
	v_mfma_i32_16x16x64_i8 v[120:123], v[20:23], v[92:95], v[120:123]
	v_mfma_i32_16x16x64_i8 v[112:115], v[28:31], v[92:95], v[112:115]
	v_mfma_i32_16x16x64_i8 v[96:99], v[28:31], v[140:143], v[96:99]
	v_mfma_i32_16x16x64_i8 v[104:107], v[20:23], v[140:143], v[104:107]
	v_mfma_i32_16x16x64_i8 v[48:51], v[20:23], v[156:159], v[48:51]
	v_mfma_i32_16x16x64_i8 v[16:19], v[28:31], v[156:159], v[16:19]
	v_mfma_i32_16x16x64_i8 v[0:3], v[28:31], v[172:175], v[0:3]
	v_mfma_i32_16x16x64_i8 v[8:11], v[20:23], v[172:175], v[8:11]
	v_mfma_i32_16x16x64_i8 v[120:123], v[24:27], v[132:135], v[120:123]
	v_mfma_i32_16x16x64_i8 v[112:115], v[32:35], v[132:135], v[112:115]
	v_mfma_i32_16x16x64_i8 v[96:99], v[32:35], v[148:151], v[96:99]
	v_mfma_i32_16x16x64_i8 v[104:107], v[24:27], v[148:151], v[104:107]
	v_mfma_i32_16x16x64_i8 v[48:51], v[24:27], v[164:167], v[48:51]
	v_mfma_i32_16x16x64_i8 v[16:19], v[32:35], v[164:167], v[16:19]
	v_mfma_i32_16x16x64_i8 v[0:3], v[32:35], v[180:183], v[0:3]
	v_mfma_i32_16x16x64_i8 v[8:11], v[24:27], v[180:183], v[8:11]
	v_mfma_i32_16x16x64_i8 v[20:23], v[36:39], v[92:95], v[124:127]
	v_mfma_i32_16x16x64_i8 v[124:127], v[40:43], v[132:135], v[20:23]
	v_mfma_i32_16x16x64_i8 v[20:23], v[52:55], v[92:95], v[116:119]
	v_mfma_i32_16x16x64_i8 v[116:119], v[56:59], v[132:135], v[20:23]
	v_mfma_i32_16x16x64_i8 v[20:23], v[36:39], v[140:143], v[108:111]
	v_mfma_i32_16x16x64_i8 v[108:111], v[40:43], v[148:151], v[20:23]
	v_mfma_i32_16x16x64_i8 v[20:23], v[52:55], v[140:143], v[100:103]
	v_mfma_i32_16x16x64_i8 v[100:103], v[56:59], v[148:151], v[20:23]
	v_mfma_i32_16x16x64_i8 v[20:23], v[36:39], v[156:159], v[60:63]
	v_mfma_i32_16x16x64_i8 v[60:63], v[40:43], v[164:167], v[20:23]
	v_mfma_i32_16x16x64_i8 v[20:23], v[52:55], v[156:159], v[44:47]
	v_mfma_i32_16x16x64_i8 v[12:15], v[36:39], v[172:175], v[12:15]
	v_mfma_i32_16x16x64_i8 v[4:7], v[52:55], v[172:175], v[4:7]
	v_mfma_i32_16x16x64_i8 v[44:47], v[56:59], v[164:167], v[20:23]
	v_mfma_i32_16x16x64_i8 v[12:15], v[40:43], v[180:183], v[12:15]
	v_mfma_i32_16x16x64_i8 v[4:7], v[56:59], v[180:183], v[4:7]
	s_barrier
	ds_read_b128 v[36:39], v207
	ds_read_b128 v[28:31], v207 offset:1024
	ds_read_b128 v[24:27], v207 offset:2048
	ds_read_b128 v[20:23], v207 offset:3072
	ds_read_b128 v[56:59], v208
	ds_read_b128 v[52:55], v208 offset:1024
	ds_read_b128 v[40:43], v208 offset:2048
	ds_read_b128 v[32:35], v208 offset:3072
	ds_read_b128 v[92:95], v206 offset:32768
	ds_read_b128 v[132:135], v206 offset:33792
	ds_read_b128 v[140:143], v206 offset:34816
	ds_read_b128 v[148:151], v206 offset:35840
	ds_read_b128 v[192:195], v206 offset:36864
	ds_read_b128 v[210:213], v206 offset:37888
	ds_read_b128 v[214:217], v206 offset:38912
	ds_read_b128 v[218:221], v206 offset:39936
	s_add_u32 s26, s38, 0x40000
	s_addc_u32 s27, s39, 0
	s_add_i32 m0, s46, 0x4000
	s_nop 0
	global_load_lds_dwordx4 v199, s[26:27]
	s_nop 0
	s_add_i32 m0, s46, 0x6000
	s_nop 0
	global_load_lds_dwordx4 v201, s[26:27]
	s_waitcnt vmcnt(8) lgkmcnt(0)
	s_barrier
	v_mfma_i32_16x16x64_i8 v[156:159], v[36:39], v[92:95], v[184:187]
	v_mfma_i32_16x16x64_i8 v[184:187], v[28:31], v[132:135], v[156:159]
	v_mfma_i32_16x16x64_i8 v[156:159], v[24:27], v[92:95], v[176:179]
	v_mfma_i32_16x16x64_i8 v[176:179], v[20:23], v[132:135], v[156:159]
	v_mfma_i32_16x16x64_i8 v[156:159], v[36:39], v[140:143], v[168:171]
	v_mfma_i32_16x16x64_i8 v[168:171], v[28:31], v[148:151], v[156:159]
	v_mfma_i32_16x16x64_i8 v[156:159], v[24:27], v[140:143], v[160:163]
	v_mfma_i32_16x16x64_i8 v[152:155], v[36:39], v[192:195], v[152:155]
	v_mfma_i32_16x16x64_i8 v[144:147], v[24:27], v[192:195], v[144:147]
	v_mfma_i32_16x16x64_i8 v[136:139], v[36:39], v[214:217], v[136:139]
	v_mfma_i32_16x16x64_i8 v[128:131], v[24:27], v[214:217], v[128:131]
	v_mfma_i32_16x16x64_i8 v[160:163], v[20:23], v[148:151], v[156:159]
	v_mfma_i32_16x16x64_i8 v[152:155], v[28:31], v[210:213], v[152:155]
	v_mfma_i32_16x16x64_i8 v[144:147], v[20:23], v[210:213], v[144:147]
	v_mfma_i32_16x16x64_i8 v[136:139], v[28:31], v[218:221], v[136:139]
	v_mfma_i32_16x16x64_i8 v[128:131], v[20:23], v[218:221], v[128:131]
	v_mfma_i32_16x16x64_i8 v[64:67], v[40:43], v[92:95], v[64:67]
	v_mfma_i32_16x16x64_i8 v[180:183], v[32:35], v[132:135], v[64:67]
	v_mfma_i32_16x16x64_i8 v[64:67], v[56:59], v[140:143], v[68:71]
	v_mfma_i32_16x16x64_i8 v[172:175], v[52:55], v[148:151], v[64:67]
	v_mfma_i32_16x16x64_i8 v[64:67], v[40:43], v[140:143], v[72:75]
	v_mfma_i32_16x16x64_i8 v[156:159], v[56:59], v[92:95], v[188:191]
	v_mfma_i32_16x16x64_i8 v[164:167], v[32:35], v[148:151], v[64:67]
	v_mfma_i32_16x16x64_i8 v[64:67], v[56:59], v[192:195], v[76:79]
	v_mfma_i32_16x16x64_i8 v[188:191], v[52:55], v[132:135], v[156:159]
	v_mfma_i32_16x16x64_i8 v[156:159], v[52:55], v[210:213], v[64:67]
	v_mfma_i32_16x16x64_i8 v[64:67], v[40:43], v[192:195], v[80:83]
	v_mfma_i32_16x16x64_i8 v[148:151], v[32:35], v[210:213], v[64:67]
	v_mfma_i32_16x16x64_i8 v[64:67], v[56:59], v[214:217], v[84:87]
	v_mfma_i32_16x16x64_i8 v[140:143], v[52:55], v[218:221], v[64:67]
	v_mfma_i32_16x16x64_i8 v[64:67], v[40:43], v[214:217], v[88:91]
	v_mfma_i32_16x16x64_i8 v[132:135], v[32:35], v[218:221], v[64:67]
	s_barrier
	ds_read_b128 v[92:95], v206 offset:49152
	ds_read_b128 v[88:91], v206 offset:50176
	ds_read_b128 v[84:87], v206 offset:51200
	ds_read_b128 v[80:83], v206 offset:52224
	ds_read_b128 v[76:79], v206 offset:53248
	ds_read_b128 v[72:75], v206 offset:54272
	ds_read_b128 v[68:71], v206 offset:55296
	ds_read_b128 v[64:67], v206 offset:56320
	s_add_i32 m0, s46, 0x18000
	s_nop 0
	global_load_lds_dwordx4 v200, s[36:37]
	s_nop 0
	s_add_i32 m0, s46, 0x1a000
	s_nop 0
	global_load_lds_dwordx4 v202, s[36:37]
	s_add_u32 s26, s34, 0x40080
	s_addc_u32 s27, s35, 0
	s_add_i32 m0, s46, 0x1c000
	s_nop 0
	global_load_lds_dwordx4 v200, s[26:27]
	s_nop 0
	s_add_i32 m0, s46, 0x1e000
	s_nop 0
	global_load_lds_dwordx4 v202, s[26:27]
	s_nop 0
	s_add_i32 m0, s46, 0x8000
	s_nop 0
	global_load_lds_dwordx4 v199, s[30:31]
	s_nop 0
	s_add_i32 m0, s46, 0xa000
	s_nop 0
	global_load_lds_dwordx4 v201, s[30:31]
	s_waitcnt vmcnt(8) lgkmcnt(0)
	s_barrier
	v_mfma_i32_16x16x64_i8 v[120:123], v[36:39], v[92:95], v[120:123]
	v_mfma_i32_16x16x64_i8 v[112:115], v[24:27], v[92:95], v[112:115]
	v_mfma_i32_16x16x64_i8 v[96:99], v[24:27], v[84:87], v[96:99]
	v_mfma_i32_16x16x64_i8 v[104:107], v[36:39], v[84:87], v[104:107]
	v_mfma_i32_16x16x64_i8 v[48:51], v[36:39], v[76:79], v[48:51]
	v_mfma_i32_16x16x64_i8 v[16:19], v[24:27], v[76:79], v[16:19]
	v_mfma_i32_16x16x64_i8 v[0:3], v[24:27], v[68:71], v[0:3]
	v_mfma_i32_16x16x64_i8 v[8:11], v[36:39], v[68:71], v[8:11]
	v_mfma_i32_16x16x64_i8 v[120:123], v[28:31], v[88:91], v[120:123]
	v_mfma_i32_16x16x64_i8 v[112:115], v[20:23], v[88:91], v[112:115]
	v_mfma_i32_16x16x64_i8 v[96:99], v[20:23], v[80:83], v[96:99]
	v_mfma_i32_16x16x64_i8 v[104:107], v[28:31], v[80:83], v[104:107]
	v_mfma_i32_16x16x64_i8 v[48:51], v[28:31], v[72:75], v[48:51]
	v_mfma_i32_16x16x64_i8 v[16:19], v[20:23], v[72:75], v[16:19]
	v_mfma_i32_16x16x64_i8 v[0:3], v[20:23], v[64:67], v[0:3]
	v_mfma_i32_16x16x64_i8 v[8:11], v[28:31], v[64:67], v[8:11]
	v_mfma_i32_16x16x64_i8 v[124:127], v[56:59], v[92:95], v[124:127]
	v_mfma_i32_16x16x64_i8 v[116:119], v[40:43], v[92:95], v[116:119]
	v_mfma_i32_16x16x64_i8 v[100:103], v[40:43], v[84:87], v[100:103]
	v_mfma_i32_16x16x64_i8 v[108:111], v[56:59], v[84:87], v[108:111]
	v_mfma_i32_16x16x64_i8 v[60:63], v[56:59], v[76:79], v[60:63]
	v_mfma_i32_16x16x64_i8 v[44:47], v[40:43], v[76:79], v[44:47]
	v_mfma_i32_16x16x64_i8 v[4:7], v[40:43], v[68:71], v[4:7]
	v_mfma_i32_16x16x64_i8 v[12:15], v[56:59], v[68:71], v[12:15]
	v_mfma_i32_16x16x64_i8 v[124:127], v[52:55], v[88:91], v[124:127]
	v_mfma_i32_16x16x64_i8 v[116:119], v[32:35], v[88:91], v[116:119]
	v_mfma_i32_16x16x64_i8 v[100:103], v[32:35], v[80:83], v[100:103]
	v_mfma_i32_16x16x64_i8 v[108:111], v[52:55], v[80:83], v[108:111]
	v_mfma_i32_16x16x64_i8 v[60:63], v[52:55], v[72:75], v[60:63]
	v_mfma_i32_16x16x64_i8 v[44:47], v[32:35], v[72:75], v[44:47]
	v_mfma_i32_16x16x64_i8 v[4:7], v[32:35], v[64:67], v[4:7]
	v_mfma_i32_16x16x64_i8 v[12:15], v[52:55], v[64:67], v[12:15]
	s_barrier
	s_add_i32 s17, s17, 2
	s_add_u32 s61, s61, 0x100
	s_addc_u32 s62, s62, 0
	s_cmp_gt_u32 s17, 13
	s_cbranch_scc1 .LBB0_757
	s_mov_b64 s[26:27], s[24:25]
	s_branch .LBB0_753

.LBB0_763:
	s_cmp_lt_u32 s93, 6
	s_cbranch_scc1 .LBB0_817
	s_waitcnt vmcnt(0) lgkmcnt(0)
	s_barrier
	s_and_saveexec_b64 s[4:5], s[72:73]
	s_cbranch_execz .LBB0_816
	s_add_u32 s6, s70, 0x4200
	s_addc_u32 s7, s71, 0
	s_add_i32 s8, 0, 0x23f20
	v_mov_b32_e32 v0, s8
	s_waitcnt vmcnt(0) expcnt(0) lgkmcnt(0)
	ds_read_b32 v2, v0
	s_add_i32 s8, 0, 0x23f24
	v_mov_b32_e32 v0, s8
	ds_read_b32 v0, v0
	s_waitcnt lgkmcnt(1)
	v_cmp_ne_u32_e32 vcc, 0, v2
	s_cbranch_vccnz .LBB0_780
	s_add_u32 s8, s70, 0x4400
	s_addc_u32 s9, s71, 0
	s_add_u32 s10, s70, 0x4500
	s_addc_u32 s11, s71, 0
	s_add_u32 s14, s70, 0x4600
	s_addc_u32 s15, s71, 0
	s_add_u32 s16, s70, 0x4700
	s_addc_u32 s17, s71, 0
	s_add_u32 s18, s70, 0x4800
	s_addc_u32 s19, s71, 0
	s_add_u32 s20, s70, 0x4900
	s_addc_u32 s21, s71, 0
	s_add_u32 s22, s70, 0x4a00
	s_addc_u32 s23, s71, 0
	s_add_u32 s24, s70, 0x4b00
	s_addc_u32 s25, s71, 0
	s_add_u32 s26, s70, 0x4c00
	s_addc_u32 s27, s71, 0
	s_add_u32 s28, s70, 0x4d00
	s_addc_u32 s29, s71, 0
	s_add_u32 s30, s70, 0x4e00
	s_addc_u32 s31, s71, 0
	s_add_u32 s34, s70, 0x4f00
	s_addc_u32 s35, s71, 0
	s_add_u32 s36, s70, 0x5000
	s_addc_u32 s37, s71, 0
	s_load_dwordx2 s[44:45], s[90:91], 0x4
	s_add_u32 s38, s70, 0x5100
	s_addc_u32 s39, s71, 0
	s_add_u32 s40, s70, 0x5200
	s_addc_u32 s41, s71, 0
	s_add_u32 s42, s70, 0x5300
	s_waitcnt lgkmcnt(0)
	s_mul_i32 s50, s44, s33
	s_addc_u32 s43, s71, 0
	s_mul_i32 s50, s50, s45
	s_mov_b32 s51, 1
	v_mov_b32_e32 v16, 0
	s_branch .LBB0_768

.LBB0_837:
	s_waitcnt lgkmcnt(0)
	ds_read_b128 v[0:3], v181
	ds_read_b128 v[4:7], v181 offset:1024
	ds_read_b128 v[8:11], v181 offset:2048
	ds_read_b128 v[12:15], v181 offset:3072
	ds_read_b128 v[16:19], v182
	ds_read_b128 v[20:23], v182 offset:1024
	ds_read_b128 v[24:27], v182 offset:2048
	ds_read_b128 v[28:31], v182 offset:3072
	ds_read_b128 v[32:35], v183
	ds_read_b128 v[36:39], v183 offset:1024
	ds_read_b128 v[40:43], v183 offset:2048
	ds_read_b128 v[44:47], v183 offset:3072
	ds_read_b128 v[48:51], v183 offset:4096
	ds_read_b128 v[52:55], v183 offset:5120
	ds_read_b128 v[56:59], v183 offset:6144
	ds_read_b128 v[60:63], v183 offset:7168
	s_add_u32 s28, s22, 0x100
	s_addc_u32 s29, s23, 0
	s_add_u32 s52, s24, 0x100
	s_addc_u32 s53, s25, 0
	s_add_u32 s6, s22, 0x180
	s_addc_u32 s7, s23, 0
	s_add_u32 s26, s24, 0x180
	s_addc_u32 s27, s25, 0
	s_add_u32 s54, s22, 0x160080
	s_addc_u32 s55, s23, 0
	s_add_i32 m0, s36, 0xc000
	s_nop 0
	global_load_lds_dwordx4 v175, s[54:55]
	s_nop 0
	s_add_i32 m0, s36, 0xe000
	s_nop 0
	global_load_lds_dwordx4 v177, s[54:55]
	s_waitcnt vmcnt(8) lgkmcnt(0)
	s_barrier
	v_mfma_f32_16x16x32_bf16 v[88:91], v[0:3], v[56:59], 0
	v_mfma_f32_16x16x32_bf16 v[64:67], v[0:3], v[32:35], 0
	v_mfma_f32_16x16x32_bf16 v[68:71], v[8:11], v[32:35], 0
	v_mfma_f32_16x16x32_bf16 v[72:75], v[0:3], v[40:43], 0
	v_mfma_f32_16x16x32_bf16 v[76:79], v[8:11], v[40:43], 0
	v_mfma_f32_16x16x32_bf16 v[80:83], v[0:3], v[48:51], 0
	v_mfma_f32_16x16x32_bf16 v[84:87], v[8:11], v[48:51], 0
	v_mfma_f32_16x16x32_bf16 v[96:99], v[4:7], v[60:63], v[88:91]
	v_mfma_f32_16x16x32_bf16 v[88:91], v[8:11], v[56:59], 0
	v_mfma_f32_16x16x32_bf16 v[64:67], v[4:7], v[36:39], v[64:67]
	v_mfma_f32_16x16x32_bf16 v[68:71], v[12:15], v[36:39], v[68:71]
	v_mfma_f32_16x16x32_bf16 v[72:75], v[4:7], v[44:47], v[72:75]
	v_mfma_f32_16x16x32_bf16 v[76:79], v[12:15], v[44:47], v[76:79]
	v_mfma_f32_16x16x32_bf16 v[80:83], v[4:7], v[52:55], v[80:83]
	v_mfma_f32_16x16x32_bf16 v[84:87], v[12:15], v[52:55], v[84:87]
	v_mfma_f32_16x16x32_bf16 v[100:103], v[12:15], v[60:63], v[88:91]
	v_mfma_f32_16x16x32_bf16 v[88:91], v[16:19], v[32:35], 0
	v_mfma_f32_16x16x32_bf16 v[32:35], v[24:27], v[32:35], 0
	v_mfma_f32_16x16x32_bf16 v[112:115], v[20:23], v[36:39], v[88:91]
	v_mfma_f32_16x16x32_bf16 v[32:35], v[28:31], v[36:39], v[32:35]
	v_mfma_f32_16x16x32_bf16 v[36:39], v[16:19], v[40:43], 0
	v_mfma_f32_16x16x32_bf16 v[40:43], v[24:27], v[40:43], 0
	v_mfma_f32_16x16x32_bf16 v[36:39], v[20:23], v[44:47], v[36:39]
	v_mfma_f32_16x16x32_bf16 v[40:43], v[28:31], v[44:47], v[40:43]
	v_mfma_f32_16x16x32_bf16 v[44:47], v[16:19], v[48:51], 0
	v_mfma_f32_16x16x32_bf16 v[48:51], v[24:27], v[48:51], 0
	v_mfma_f32_16x16x32_bf16 v[44:47], v[20:23], v[52:55], v[44:47]
	v_mfma_f32_16x16x32_bf16 v[48:51], v[28:31], v[52:55], v[48:51]
	v_mfma_f32_16x16x32_bf16 v[52:55], v[16:19], v[56:59], 0
	v_mfma_f32_16x16x32_bf16 v[56:59], v[24:27], v[56:59], 0
	v_mfma_f32_16x16x32_bf16 v[52:55], v[20:23], v[60:63], v[52:55]
	v_mfma_f32_16x16x32_bf16 v[56:59], v[28:31], v[60:63], v[56:59]
	s_barrier
	ds_read_b128 v[60:63], v183 offset:16384
	ds_read_b128 v[88:91], v183 offset:17408
	ds_read_b128 v[92:95], v183 offset:18432
	ds_read_b128 v[104:107], v183 offset:19456
	ds_read_b128 v[108:111], v183 offset:20480
	ds_read_b128 v[116:119], v183 offset:21504
	ds_read_b128 v[120:123], v183 offset:22528
	ds_read_b128 v[124:127], v183 offset:23552
	s_add_i32 m0, s36, 0x10000
	s_nop 0
	global_load_lds_dwordx4 v176, s[52:53]
	s_nop 0
	s_add_i32 m0, s36, 0x12000
	s_nop 0
	global_load_lds_dwordx4 v178, s[52:53]
	s_add_u32 s52, s24, 0x160100
	s_addc_u32 s53, s25, 0
	s_add_i32 m0, s36, 0x14000
	s_nop 0
	global_load_lds_dwordx4 v176, s[52:53]
	s_nop 0
	s_add_i32 m0, s36, 0x16000
	s_nop 0
	global_load_lds_dwordx4 v178, s[52:53]
	s_nop 0
	s_add_i32 m0, s36, 0
	s_nop 0
	global_load_lds_dwordx4 v175, s[28:29]
	s_nop 0
	s_add_i32 m0, s36, 0x2000
	s_nop 0
	global_load_lds_dwordx4 v177, s[28:29]
	s_waitcnt vmcnt(8) lgkmcnt(0)
	s_barrier
	v_mfma_f32_16x16x32_bf16 v[128:131], v[0:3], v[60:63], 0
	v_mfma_f32_16x16x32_bf16 v[136:139], v[4:7], v[88:91], v[128:131]
	v_mfma_f32_16x16x32_bf16 v[128:131], v[8:11], v[60:63], 0
	v_mfma_f32_16x16x32_bf16 v[140:143], v[12:15], v[88:91], v[128:131]
	v_mfma_f32_16x16x32_bf16 v[128:131], v[0:3], v[92:95], 0
	v_mfma_f32_16x16x32_bf16 v[144:147], v[4:7], v[104:107], v[128:131]
	v_mfma_f32_16x16x32_bf16 v[128:131], v[8:11], v[92:95], 0
	v_mfma_f32_16x16x32_bf16 v[148:151], v[12:15], v[104:107], v[128:131]
	v_mfma_f32_16x16x32_bf16 v[128:131], v[0:3], v[108:111], 0
	v_mfma_f32_16x16x32_bf16 v[0:3], v[0:3], v[120:123], 0
	v_mfma_f32_16x16x32_bf16 v[156:159], v[4:7], v[116:119], v[128:131]
	v_mfma_f32_16x16x32_bf16 v[0:3], v[4:7], v[124:127], v[0:3]
	v_mfma_f32_16x16x32_bf16 v[4:7], v[8:11], v[120:123], 0
	v_mfma_f32_16x16x32_bf16 v[128:131], v[8:11], v[108:111], 0
	v_mfma_f32_16x16x32_bf16 v[4:7], v[12:15], v[124:127], v[4:7]
	v_mfma_f32_16x16x32_bf16 v[160:163], v[12:15], v[116:119], v[128:131]
	v_mfma_f32_16x16x32_bf16 v[8:11], v[16:19], v[60:63], 0
	v_mfma_f32_16x16x32_bf16 v[164:167], v[20:23], v[88:91], v[8:11]
	v_mfma_f32_16x16x32_bf16 v[8:11], v[24:27], v[60:63], 0
	v_mfma_f32_16x16x32_bf16 v[168:171], v[28:31], v[88:91], v[8:11]
	v_mfma_f32_16x16x32_bf16 v[8:11], v[16:19], v[92:95], 0
	v_mfma_f32_16x16x32_bf16 v[188:191], v[20:23], v[104:107], v[8:11]
	v_mfma_f32_16x16x32_bf16 v[8:11], v[24:27], v[92:95], 0
	v_mfma_f32_16x16x32_bf16 v[192:195], v[28:31], v[104:107], v[8:11]
	v_mfma_f32_16x16x32_bf16 v[8:11], v[16:19], v[108:111], 0
	v_mfma_f32_16x16x32_bf16 v[196:199], v[20:23], v[116:119], v[8:11]
	v_mfma_f32_16x16x32_bf16 v[8:11], v[24:27], v[108:111], 0
	v_mfma_f32_16x16x32_bf16 v[116:119], v[28:31], v[116:119], v[8:11]
	v_mfma_f32_16x16x32_bf16 v[8:11], v[16:19], v[120:123], 0
	v_mfma_f32_16x16x32_bf16 v[200:203], v[20:23], v[124:127], v[8:11]
	v_mfma_f32_16x16x32_bf16 v[8:11], v[24:27], v[120:123], 0
	v_mfma_f32_16x16x32_bf16 v[204:207], v[28:31], v[124:127], v[8:11]
	s_barrier
	s_nop 4
	ds_read_b128 v[8:11], v184
	ds_read_b128 v[12:15], v184 offset:1024
	ds_read_b128 v[16:19], v184 offset:2048
	ds_read_b128 v[20:23], v184 offset:3072
	ds_read_b128 v[208:211], v185
	ds_read_b128 v[212:215], v185 offset:1024
	ds_read_b128 v[216:219], v185 offset:2048
	ds_read_b128 v[220:223], v185 offset:3072
	ds_read_b128 v[24:27], v183 offset:32768
	ds_read_b128 v[28:31], v183 offset:33792
	ds_read_b128 v[60:63], v183 offset:34816
	ds_read_b128 v[224:227], v183 offset:35840
	ds_read_b128 v[228:231], v183 offset:36864
	ds_read_b128 v[232:235], v183 offset:37888
	ds_read_b128 v[236:239], v183 offset:38912
	ds_read_b128 v[240:243], v183 offset:39936
	s_add_u32 s28, s22, 0x160100
	s_addc_u32 s29, s23, 0
	s_add_i32 m0, s36, 0x4000
	s_nop 0
	global_load_lds_dwordx4 v175, s[28:29]
	s_nop 0
	s_add_i32 m0, s36, 0x6000
	s_nop 0
	global_load_lds_dwordx4 v177, s[28:29]
	s_waitcnt vmcnt(8) lgkmcnt(0)
	s_barrier
	v_mfma_f32_16x16x32_bf16 v[64:67], v[8:11], v[24:27], v[64:67]
	v_mfma_f32_16x16x32_bf16 v[132:135], v[12:15], v[28:31], v[64:67]
	v_mfma_f32_16x16x32_bf16 v[64:67], v[16:19], v[24:27], v[68:71]
	v_mfma_f32_16x16x32_bf16 v[128:131], v[20:23], v[28:31], v[64:67]
	v_mfma_f32_16x16x32_bf16 v[64:67], v[8:11], v[60:63], v[72:75]
	v_mfma_f32_16x16x32_bf16 v[108:111], v[12:15], v[224:227], v[64:67]
	v_mfma_f32_16x16x32_bf16 v[64:67], v[16:19], v[60:63], v[76:79]
	v_mfma_f32_16x16x32_bf16 v[104:107], v[20:23], v[224:227], v[64:67]
	v_mfma_f32_16x16x32_bf16 v[64:67], v[8:11], v[228:231], v[80:83]
	v_mfma_f32_16x16x32_bf16 v[92:95], v[12:15], v[232:235], v[64:67]
	v_mfma_f32_16x16x32_bf16 v[64:67], v[16:19], v[228:231], v[84:87]
	v_mfma_f32_16x16x32_bf16 v[88:91], v[20:23], v[232:235], v[64:67]
	v_mfma_f32_16x16x32_bf16 v[64:67], v[8:11], v[236:239], v[96:99]
	v_mfma_f32_16x16x32_bf16 v[76:79], v[12:15], v[240:243], v[64:67]
	v_mfma_f32_16x16x32_bf16 v[64:67], v[16:19], v[236:239], v[100:103]
	v_mfma_f32_16x16x32_bf16 v[72:75], v[20:23], v[240:243], v[64:67]
	v_mfma_f32_16x16x32_bf16 v[64:67], v[208:211], v[24:27], v[112:115]
	v_mfma_f32_16x16x32_bf16 v[24:27], v[216:219], v[24:27], v[32:35]
	v_mfma_f32_16x16x32_bf16 v[120:123], v[220:223], v[28:31], v[24:27]
	v_mfma_f32_16x16x32_bf16 v[24:27], v[208:211], v[60:63], v[36:39]
	v_mfma_f32_16x16x32_bf16 v[100:103], v[212:215], v[224:227], v[24:27]
	v_mfma_f32_16x16x32_bf16 v[24:27], v[216:219], v[60:63], v[40:43]
	v_mfma_f32_16x16x32_bf16 v[96:99], v[220:223], v[224:227], v[24:27]
	v_mfma_f32_16x16x32_bf16 v[24:27], v[208:211], v[228:231], v[44:47]
	v_mfma_f32_16x16x32_bf16 v[84:87], v[212:215], v[232:235], v[24:27]
	v_mfma_f32_16x16x32_bf16 v[24:27], v[216:219], v[228:231], v[48:51]
	v_mfma_f32_16x16x32_bf16 v[80:83], v[220:223], v[232:235], v[24:27]
	v_mfma_f32_16x16x32_bf16 v[24:27], v[208:211], v[236:239], v[52:55]
	v_mfma_f32_16x16x32_bf16 v[68:71], v[212:215], v[240:243], v[24:27]
	v_mfma_f32_16x16x32_bf16 v[24:27], v[216:219], v[236:239], v[56:59]
	v_mfma_f32_16x16x32_bf16 v[124:127], v[212:215], v[28:31], v[64:67]
	v_mfma_f32_16x16x32_bf16 v[64:67], v[220:223], v[240:243], v[24:27]
	s_barrier
	ds_read_b128 v[32:35], v183 offset:49152
	ds_read_b128 v[36:39], v183 offset:50176
	ds_read_b128 v[112:115], v183 offset:51200
	ds_read_b128 v[224:227], v183 offset:52224
	ds_read_b128 v[228:231], v183 offset:53248
	ds_read_b128 v[232:235], v183 offset:54272
	ds_read_b128 v[236:239], v183 offset:55296
	ds_read_b128 v[240:243], v183 offset:56320
	s_add_i32 m0, s36, 0x18000
	s_nop 0
	global_load_lds_dwordx4 v176, s[26:27]
	s_nop 0
	s_add_i32 m0, s36, 0x1a000
	s_nop 0
	global_load_lds_dwordx4 v178, s[26:27]
	s_add_u32 s26, s24, 0x160180
	s_addc_u32 s27, s25, 0
	s_add_i32 m0, s36, 0x1c000
	s_nop 0
	global_load_lds_dwordx4 v176, s[26:27]
	s_nop 0
	s_add_i32 m0, s36, 0x1e000
	s_nop 0
	global_load_lds_dwordx4 v178, s[26:27]
	s_nop 0
	s_add_i32 m0, s36, 0x8000
	s_nop 0
	global_load_lds_dwordx4 v175, s[6:7]
	s_nop 0
	s_add_i32 m0, s36, 0xa000
	s_nop 0
	global_load_lds_dwordx4 v177, s[6:7]
	s_waitcnt vmcnt(8) lgkmcnt(0)
	s_barrier
	v_mfma_f32_16x16x32_bf16 v[24:27], v[8:11], v[32:35], v[136:139]
	v_mfma_f32_16x16x32_bf16 v[60:63], v[12:15], v[36:39], v[24:27]
	v_mfma_f32_16x16x32_bf16 v[24:27], v[16:19], v[32:35], v[140:143]
	v_mfma_f32_16x16x32_bf16 v[56:59], v[20:23], v[36:39], v[24:27]
	v_mfma_f32_16x16x32_bf16 v[24:27], v[8:11], v[112:115], v[144:147]
	v_mfma_f32_16x16x32_bf16 v[44:47], v[12:15], v[224:227], v[24:27]
	v_mfma_f32_16x16x32_bf16 v[24:27], v[16:19], v[112:115], v[148:151]
	v_mfma_f32_16x16x32_bf16 v[40:43], v[20:23], v[224:227], v[24:27]
	v_mfma_f32_16x16x32_bf16 v[24:27], v[8:11], v[228:231], v[156:159]
	v_mfma_f32_16x16x32_bf16 v[0:3], v[8:11], v[236:239], v[0:3]
	v_mfma_f32_16x16x32_bf16 v[28:31], v[12:15], v[232:235], v[24:27]
	v_mfma_f32_16x16x32_bf16 v[24:27], v[16:19], v[228:231], v[160:163]
	v_mfma_f32_16x16x32_bf16 v[12:15], v[12:15], v[240:243], v[0:3]
	v_mfma_f32_16x16x32_bf16 v[0:3], v[16:19], v[236:239], v[4:7]
	v_mfma_f32_16x16x32_bf16 v[24:27], v[20:23], v[232:235], v[24:27]
	v_mfma_f32_16x16x32_bf16 v[8:11], v[20:23], v[240:243], v[0:3]
	v_mfma_f32_16x16x32_bf16 v[0:3], v[208:211], v[32:35], v[164:167]
	v_mfma_f32_16x16x32_bf16 v[52:55], v[212:215], v[36:39], v[0:3]
	v_mfma_f32_16x16x32_bf16 v[0:3], v[216:219], v[32:35], v[168:171]
	v_mfma_f32_16x16x32_bf16 v[48:51], v[220:223], v[36:39], v[0:3]
	v_mfma_f32_16x16x32_bf16 v[0:3], v[208:211], v[112:115], v[188:191]
	v_mfma_f32_16x16x32_bf16 v[36:39], v[212:215], v[224:227], v[0:3]
	v_mfma_f32_16x16x32_bf16 v[0:3], v[216:219], v[112:115], v[192:195]
	v_mfma_f32_16x16x32_bf16 v[32:35], v[220:223], v[224:227], v[0:3]
	v_mfma_f32_16x16x32_bf16 v[0:3], v[208:211], v[228:231], v[196:199]
	v_mfma_f32_16x16x32_bf16 v[20:23], v[212:215], v[232:235], v[0:3]
	v_mfma_f32_16x16x32_bf16 v[0:3], v[216:219], v[228:231], v[116:119]
	v_mfma_f32_16x16x32_bf16 v[16:19], v[220:223], v[232:235], v[0:3]
	v_mfma_f32_16x16x32_bf16 v[0:3], v[208:211], v[236:239], v[200:203]
	v_mfma_f32_16x16x32_bf16 v[4:7], v[212:215], v[240:243], v[0:3]
	v_mfma_f32_16x16x32_bf16 v[0:3], v[216:219], v[236:239], v[204:207]
	v_mfma_f32_16x16x32_bf16 v[0:3], v[220:223], v[240:243], v[0:3]
	s_barrier
	s_add_u32 s51, s22, 0x200
	s_addc_u32 s52, s23, 0
	s_add_u32 s53, s24, 0x200
	s_addc_u32 s54, s25, 0
	s_add_u32 s6, s22, 0x160180
	s_addc_u32 s7, s23, 0
	s_mov_b32 s55, 0
.LBB0_838:
	ds_read_b128 v[112:115], v181
	ds_read_b128 v[116:119], v181 offset:1024
	ds_read_b128 v[136:139], v181 offset:2048
	ds_read_b128 v[140:143], v181 offset:3072
	ds_read_b128 v[144:147], v182
	ds_read_b128 v[148:151], v182 offset:1024
	ds_read_b128 v[156:159], v182 offset:2048
	ds_read_b128 v[160:163], v182 offset:3072
	ds_read_b128 v[164:167], v183
	ds_read_b128 v[168:171], v183 offset:1024
	ds_read_b128 v[188:191], v183 offset:2048
	ds_read_b128 v[192:195], v183 offset:3072
	ds_read_b128 v[196:199], v183 offset:4096
	ds_read_b128 v[200:203], v183 offset:5120
	ds_read_b128 v[204:207], v183 offset:6144
	ds_read_b128 v[208:211], v183 offset:7168
	s_cmpk_eq_i32 s55, 0x54
	s_cselect_b32 s28, s18, s51
	s_cselect_b32 s29, s19, s52
	s_cselect_b32 s24, s20, s53
	s_cselect_b32 s25, s21, s54
	s_add_u32 s22, s28, 0x80
	s_addc_u32 s23, s29, 0
	s_add_u32 s26, s24, 0x80
	s_addc_u32 s27, s25, 0
	s_add_i32 m0, s36, 0xc000
	s_nop 0
	global_load_lds_dwordx4 v175, s[6:7]
	s_nop 0
	s_add_i32 m0, s36, 0xe000
	s_nop 0
	global_load_lds_dwordx4 v177, s[6:7]
	s_waitcnt vmcnt(8) lgkmcnt(0)
	s_barrier
	v_mfma_f32_16x16x32_bf16 v[132:135], v[112:115], v[164:167], v[132:135]
	v_mfma_f32_16x16x32_bf16 v[128:131], v[136:139], v[164:167], v[128:131]
	v_mfma_f32_16x16x32_bf16 v[104:107], v[136:139], v[188:191], v[104:107]
	v_mfma_f32_16x16x32_bf16 v[108:111], v[112:115], v[188:191], v[108:111]
	v_mfma_f32_16x16x32_bf16 v[92:95], v[112:115], v[196:199], v[92:95]
	v_mfma_f32_16x16x32_bf16 v[88:91], v[136:139], v[196:199], v[88:91]
	v_mfma_f32_16x16x32_bf16 v[72:75], v[136:139], v[204:207], v[72:75]
	v_mfma_f32_16x16x32_bf16 v[76:79], v[112:115], v[204:207], v[76:79]
	v_mfma_f32_16x16x32_bf16 v[132:135], v[116:119], v[168:171], v[132:135]
	v_mfma_f32_16x16x32_bf16 v[128:131], v[140:143], v[168:171], v[128:131]
	v_mfma_f32_16x16x32_bf16 v[104:107], v[140:143], v[192:195], v[104:107]
	v_mfma_f32_16x16x32_bf16 v[108:111], v[116:119], v[192:195], v[108:111]
	v_mfma_f32_16x16x32_bf16 v[92:95], v[116:119], v[200:203], v[92:95]
	v_mfma_f32_16x16x32_bf16 v[88:91], v[140:143], v[200:203], v[88:91]
	v_mfma_f32_16x16x32_bf16 v[72:75], v[140:143], v[208:211], v[72:75]
	v_mfma_f32_16x16x32_bf16 v[76:79], v[116:119], v[208:211], v[76:79]
	v_mfma_f32_16x16x32_bf16 v[124:127], v[144:147], v[164:167], v[124:127]
	v_mfma_f32_16x16x32_bf16 v[120:123], v[156:159], v[164:167], v[120:123]
	v_mfma_f32_16x16x32_bf16 v[96:99], v[156:159], v[188:191], v[96:99]
	v_mfma_f32_16x16x32_bf16 v[100:103], v[144:147], v[188:191], v[100:103]
	v_mfma_f32_16x16x32_bf16 v[84:87], v[144:147], v[196:199], v[84:87]
	v_mfma_f32_16x16x32_bf16 v[80:83], v[156:159], v[196:199], v[80:83]
	v_mfma_f32_16x16x32_bf16 v[64:67], v[156:159], v[204:207], v[64:67]
	v_mfma_f32_16x16x32_bf16 v[68:71], v[144:147], v[204:207], v[68:71]
	v_mfma_f32_16x16x32_bf16 v[124:127], v[148:151], v[168:171], v[124:127]
	v_mfma_f32_16x16x32_bf16 v[120:123], v[160:163], v[168:171], v[120:123]
	v_mfma_f32_16x16x32_bf16 v[96:99], v[160:163], v[192:195], v[96:99]
	v_mfma_f32_16x16x32_bf16 v[100:103], v[148:151], v[192:195], v[100:103]
	v_mfma_f32_16x16x32_bf16 v[84:87], v[148:151], v[200:203], v[84:87]
	v_mfma_f32_16x16x32_bf16 v[80:83], v[160:163], v[200:203], v[80:83]
	v_mfma_f32_16x16x32_bf16 v[64:67], v[160:163], v[208:211], v[64:67]
	v_mfma_f32_16x16x32_bf16 v[68:71], v[148:151], v[208:211], v[68:71]
	s_barrier
	ds_read_b128 v[164:167], v183 offset:16384
	ds_read_b128 v[168:171], v183 offset:17408
	ds_read_b128 v[188:191], v183 offset:18432
	ds_read_b128 v[192:195], v183 offset:19456
	ds_read_b128 v[196:199], v183 offset:20480
	ds_read_b128 v[200:203], v183 offset:21504
	ds_read_b128 v[204:207], v183 offset:22528
	ds_read_b128 v[208:211], v183 offset:23552
	s_add_i32 m0, s36, 0x10000
	s_nop 0
	global_load_lds_dwordx4 v176, s[24:25]
	s_nop 0
	s_add_i32 m0, s36, 0x12000
	s_nop 0
	global_load_lds_dwordx4 v178, s[24:25]
	s_add_u32 s56, s24, 0x160000
	s_addc_u32 s57, s25, 0
	s_add_i32 m0, s36, 0x14000
	s_nop 0
	global_load_lds_dwordx4 v176, s[56:57]
	s_nop 0
	s_add_i32 m0, s36, 0x16000
	s_nop 0
	global_load_lds_dwordx4 v178, s[56:57]
	s_nop 0
	s_add_i32 m0, s36, 0
	s_nop 0
	global_load_lds_dwordx4 v175, s[28:29]
	s_nop 0
	s_add_i32 m0, s36, 0x2000
	s_nop 0
	global_load_lds_dwordx4 v177, s[28:29]
	s_waitcnt vmcnt(8) lgkmcnt(0)
	s_barrier
	v_mfma_f32_16x16x32_bf16 v[60:63], v[112:115], v[164:167], v[60:63]
	v_mfma_f32_16x16x32_bf16 v[56:59], v[136:139], v[164:167], v[56:59]
	v_mfma_f32_16x16x32_bf16 v[40:43], v[136:139], v[188:191], v[40:43]
	v_mfma_f32_16x16x32_bf16 v[44:47], v[112:115], v[188:191], v[44:47]
	v_mfma_f32_16x16x32_bf16 v[28:31], v[112:115], v[196:199], v[28:31]
	v_mfma_f32_16x16x32_bf16 v[24:27], v[136:139], v[196:199], v[24:27]
	v_mfma_f32_16x16x32_bf16 v[8:11], v[136:139], v[204:207], v[8:11]
	v_mfma_f32_16x16x32_bf16 v[12:15], v[112:115], v[204:207], v[12:15]
	v_mfma_f32_16x16x32_bf16 v[60:63], v[116:119], v[168:171], v[60:63]
	v_mfma_f32_16x16x32_bf16 v[56:59], v[140:143], v[168:171], v[56:59]
	v_mfma_f32_16x16x32_bf16 v[40:43], v[140:143], v[192:195], v[40:43]
	v_mfma_f32_16x16x32_bf16 v[44:47], v[116:119], v[192:195], v[44:47]
	v_mfma_f32_16x16x32_bf16 v[28:31], v[116:119], v[200:203], v[28:31]
	v_mfma_f32_16x16x32_bf16 v[24:27], v[140:143], v[200:203], v[24:27]
	v_mfma_f32_16x16x32_bf16 v[8:11], v[140:143], v[208:211], v[8:11]
	v_mfma_f32_16x16x32_bf16 v[12:15], v[116:119], v[208:211], v[12:15]
	v_mfma_f32_16x16x32_bf16 v[52:55], v[144:147], v[164:167], v[52:55]
	v_mfma_f32_16x16x32_bf16 v[48:51], v[156:159], v[164:167], v[48:51]
	v_mfma_f32_16x16x32_bf16 v[32:35], v[156:159], v[188:191], v[32:35]
	v_mfma_f32_16x16x32_bf16 v[36:39], v[144:147], v[188:191], v[36:39]
	v_mfma_f32_16x16x32_bf16 v[20:23], v[144:147], v[196:199], v[20:23]
	v_mfma_f32_16x16x32_bf16 v[16:19], v[156:159], v[196:199], v[16:19]
	v_mfma_f32_16x16x32_bf16 v[0:3], v[156:159], v[204:207], v[0:3]
	v_mfma_f32_16x16x32_bf16 v[4:7], v[144:147], v[204:207], v[4:7]
	v_mfma_f32_16x16x32_bf16 v[52:55], v[148:151], v[168:171], v[52:55]
	v_mfma_f32_16x16x32_bf16 v[48:51], v[160:163], v[168:171], v[48:51]
	v_mfma_f32_16x16x32_bf16 v[32:35], v[160:163], v[192:195], v[32:35]
	v_mfma_f32_16x16x32_bf16 v[36:39], v[148:151], v[192:195], v[36:39]
	v_mfma_f32_16x16x32_bf16 v[20:23], v[148:151], v[200:203], v[20:23]
	v_mfma_f32_16x16x32_bf16 v[16:19], v[160:163], v[200:203], v[16:19]
	v_mfma_f32_16x16x32_bf16 v[0:3], v[160:163], v[208:211], v[0:3]
	v_mfma_f32_16x16x32_bf16 v[4:7], v[148:151], v[208:211], v[4:7]
	s_barrier
	ds_read_b128 v[112:115], v184
	ds_read_b128 v[116:119], v184 offset:1024
	ds_read_b128 v[136:139], v184 offset:2048
	ds_read_b128 v[140:143], v184 offset:3072
	ds_read_b128 v[144:147], v185
	ds_read_b128 v[148:151], v185 offset:1024
	ds_read_b128 v[156:159], v185 offset:2048
	ds_read_b128 v[160:163], v185 offset:3072
	ds_read_b128 v[164:167], v183 offset:32768
	ds_read_b128 v[168:171], v183 offset:33792
	ds_read_b128 v[188:191], v183 offset:34816
	ds_read_b128 v[192:195], v183 offset:35840
	ds_read_b128 v[196:199], v183 offset:36864
	ds_read_b128 v[200:203], v183 offset:37888
	ds_read_b128 v[204:207], v183 offset:38912
	ds_read_b128 v[208:211], v183 offset:39936
	s_add_u32 s28, s28, 0x160000
	s_addc_u32 s29, s29, 0
	s_add_i32 m0, s36, 0x4000
	s_nop 0
	global_load_lds_dwordx4 v175, s[28:29]
	s_nop 0
	s_add_i32 m0, s36, 0x6000
	s_nop 0
	global_load_lds_dwordx4 v177, s[28:29]
	s_waitcnt vmcnt(8) lgkmcnt(0)
	s_barrier
	v_mfma_f32_16x16x32_bf16 v[132:135], v[112:115], v[164:167], v[132:135]
	v_mfma_f32_16x16x32_bf16 v[128:131], v[136:139], v[164:167], v[128:131]
	v_mfma_f32_16x16x32_bf16 v[104:107], v[136:139], v[188:191], v[104:107]
	v_mfma_f32_16x16x32_bf16 v[108:111], v[112:115], v[188:191], v[108:111]
	v_mfma_f32_16x16x32_bf16 v[92:95], v[112:115], v[196:199], v[92:95]
	v_mfma_f32_16x16x32_bf16 v[88:91], v[136:139], v[196:199], v[88:91]
	v_mfma_f32_16x16x32_bf16 v[72:75], v[136:139], v[204:207], v[72:75]
	v_mfma_f32_16x16x32_bf16 v[76:79], v[112:115], v[204:207], v[76:79]
	v_mfma_f32_16x16x32_bf16 v[132:135], v[116:119], v[168:171], v[132:135]
	v_mfma_f32_16x16x32_bf16 v[128:131], v[140:143], v[168:171], v[128:131]
	v_mfma_f32_16x16x32_bf16 v[104:107], v[140:143], v[192:195], v[104:107]
	v_mfma_f32_16x16x32_bf16 v[108:111], v[116:119], v[192:195], v[108:111]
	v_mfma_f32_16x16x32_bf16 v[92:95], v[116:119], v[200:203], v[92:95]
	v_mfma_f32_16x16x32_bf16 v[88:91], v[140:143], v[200:203], v[88:91]
	v_mfma_f32_16x16x32_bf16 v[72:75], v[140:143], v[208:211], v[72:75]
	v_mfma_f32_16x16x32_bf16 v[76:79], v[116:119], v[208:211], v[76:79]
	v_mfma_f32_16x16x32_bf16 v[124:127], v[144:147], v[164:167], v[124:127]
	v_mfma_f32_16x16x32_bf16 v[120:123], v[156:159], v[164:167], v[120:123]
	v_mfma_f32_16x16x32_bf16 v[96:99], v[156:159], v[188:191], v[96:99]
	v_mfma_f32_16x16x32_bf16 v[100:103], v[144:147], v[188:191], v[100:103]
	v_mfma_f32_16x16x32_bf16 v[84:87], v[144:147], v[196:199], v[84:87]
	v_mfma_f32_16x16x32_bf16 v[80:83], v[156:159], v[196:199], v[80:83]
	v_mfma_f32_16x16x32_bf16 v[64:67], v[156:159], v[204:207], v[64:67]
	v_mfma_f32_16x16x32_bf16 v[68:71], v[144:147], v[204:207], v[68:71]
	v_mfma_f32_16x16x32_bf16 v[124:127], v[148:151], v[168:171], v[124:127]
	v_mfma_f32_16x16x32_bf16 v[120:123], v[160:163], v[168:171], v[120:123]
	v_mfma_f32_16x16x32_bf16 v[96:99], v[160:163], v[192:195], v[96:99]
	v_mfma_f32_16x16x32_bf16 v[100:103], v[148:151], v[192:195], v[100:103]
	v_mfma_f32_16x16x32_bf16 v[84:87], v[148:151], v[200:203], v[84:87]
	v_mfma_f32_16x16x32_bf16 v[80:83], v[160:163], v[200:203], v[80:83]
	v_mfma_f32_16x16x32_bf16 v[64:67], v[160:163], v[208:211], v[64:67]
	v_mfma_f32_16x16x32_bf16 v[68:71], v[148:151], v[208:211], v[68:71]
	s_barrier
	ds_read_b128 v[164:167], v183 offset:49152
	ds_read_b128 v[168:171], v183 offset:50176
	ds_read_b128 v[188:191], v183 offset:51200
	ds_read_b128 v[192:195], v183 offset:52224
	ds_read_b128 v[196:199], v183 offset:53248
	ds_read_b128 v[200:203], v183 offset:54272
	ds_read_b128 v[204:207], v183 offset:55296
	ds_read_b128 v[208:211], v183 offset:56320
	s_add_i32 m0, s36, 0x18000
	s_nop 0
	global_load_lds_dwordx4 v176, s[26:27]
	s_nop 0
	s_add_i32 m0, s36, 0x1a000
	s_nop 0
	global_load_lds_dwordx4 v178, s[26:27]
	s_add_u32 s24, s24, 0x160080
	s_addc_u32 s25, s25, 0
	s_add_i32 m0, s36, 0x1c000
	s_nop 0
	global_load_lds_dwordx4 v176, s[24:25]
	s_nop 0
	s_add_i32 m0, s36, 0x1e000
	s_nop 0
	global_load_lds_dwordx4 v178, s[24:25]
	s_nop 0
	s_add_i32 m0, s36, 0x8000
	s_nop 0
	global_load_lds_dwordx4 v175, s[22:23]
	s_nop 0
	s_add_i32 m0, s36, 0xa000
	s_nop 0
	global_load_lds_dwordx4 v177, s[22:23]
	s_waitcnt vmcnt(8) lgkmcnt(0)
	s_barrier
	v_mfma_f32_16x16x32_bf16 v[60:63], v[112:115], v[164:167], v[60:63]
	v_mfma_f32_16x16x32_bf16 v[56:59], v[136:139], v[164:167], v[56:59]
	v_mfma_f32_16x16x32_bf16 v[40:43], v[136:139], v[188:191], v[40:43]
	v_mfma_f32_16x16x32_bf16 v[44:47], v[112:115], v[188:191], v[44:47]
	v_mfma_f32_16x16x32_bf16 v[28:31], v[112:115], v[196:199], v[28:31]
	v_mfma_f32_16x16x32_bf16 v[24:27], v[136:139], v[196:199], v[24:27]
	v_mfma_f32_16x16x32_bf16 v[8:11], v[136:139], v[204:207], v[8:11]
	v_mfma_f32_16x16x32_bf16 v[12:15], v[112:115], v[204:207], v[12:15]
	v_mfma_f32_16x16x32_bf16 v[60:63], v[116:119], v[168:171], v[60:63]
	v_mfma_f32_16x16x32_bf16 v[56:59], v[140:143], v[168:171], v[56:59]
	v_mfma_f32_16x16x32_bf16 v[40:43], v[140:143], v[192:195], v[40:43]
	v_mfma_f32_16x16x32_bf16 v[44:47], v[116:119], v[192:195], v[44:47]
	v_mfma_f32_16x16x32_bf16 v[28:31], v[116:119], v[200:203], v[28:31]
	v_mfma_f32_16x16x32_bf16 v[24:27], v[140:143], v[200:203], v[24:27]
	v_mfma_f32_16x16x32_bf16 v[8:11], v[140:143], v[208:211], v[8:11]
	v_mfma_f32_16x16x32_bf16 v[12:15], v[116:119], v[208:211], v[12:15]
	v_mfma_f32_16x16x32_bf16 v[52:55], v[144:147], v[164:167], v[52:55]
	v_mfma_f32_16x16x32_bf16 v[48:51], v[156:159], v[164:167], v[48:51]
	v_mfma_f32_16x16x32_bf16 v[32:35], v[156:159], v[188:191], v[32:35]
	v_mfma_f32_16x16x32_bf16 v[36:39], v[144:147], v[188:191], v[36:39]
	v_mfma_f32_16x16x32_bf16 v[20:23], v[144:147], v[196:199], v[20:23]
	v_mfma_f32_16x16x32_bf16 v[16:19], v[156:159], v[196:199], v[16:19]
	v_mfma_f32_16x16x32_bf16 v[0:3], v[156:159], v[204:207], v[0:3]
	v_mfma_f32_16x16x32_bf16 v[4:7], v[144:147], v[204:207], v[4:7]
	v_mfma_f32_16x16x32_bf16 v[52:55], v[148:151], v[168:171], v[52:55]
	v_mfma_f32_16x16x32_bf16 v[48:51], v[160:163], v[168:171], v[48:51]
	v_mfma_f32_16x16x32_bf16 v[32:35], v[160:163], v[192:195], v[32:35]
	v_mfma_f32_16x16x32_bf16 v[36:39], v[148:151], v[192:195], v[36:39]
	v_mfma_f32_16x16x32_bf16 v[20:23], v[148:151], v[200:203], v[20:23]
	v_mfma_f32_16x16x32_bf16 v[16:19], v[160:163], v[200:203], v[16:19]
	v_mfma_f32_16x16x32_bf16 v[0:3], v[160:163], v[208:211], v[0:3]
	v_mfma_f32_16x16x32_bf16 v[4:7], v[148:151], v[208:211], v[4:7]
	s_barrier
	s_add_i32 s55, s55, 2
	s_add_u32 s51, s51, 0x100
	s_addc_u32 s52, s52, 0
	s_add_u32 s53, s53, 0x100
	s_addc_u32 s54, s54, 0
	s_add_u32 s6, s6, 0x100
	s_addc_u32 s7, s7, 0
	s_cmpk_gt_u32 s55, 0x55
	s_cbranch_scc0 .LBB0_838
	s_and_b64 vcc, exec, s[16:17]
	s_cbranch_vccz .LBB0_841
	s_barrier

.LBB0_930:
	s_ashr_i32 s37, s36, 31
	s_lshl_b64 s[38:39], s[36:37], 19
	s_add_u32 s38, s19, s38
	s_addc_u32 s39, s21, s39
	s_and_b64 s[40:41], s[4:5], exec
	s_cselect_b32 s9, s39, s45
	s_cselect_b32 s76, s38, s44
	s_ashr_i32 s35, s34, 31
	s_lshl_b64 s[40:41], s[34:35], 19
	s_add_u32 s40, s23, s40
	s_addc_u32 s41, s25, s41
	s_and_b64 s[46:47], s[4:5], exec
	ds_read_b128 v[0:3], v226 offset:3072
	ds_read_b128 v[4:7], v226 offset:2048
	ds_read_b128 v[8:11], v226 offset:1024
	ds_read_b128 v[12:15], v226
	ds_read_b128 v[16:19], v227 offset:3072
	ds_read_b128 v[20:23], v227 offset:2048
	ds_read_b128 v[24:27], v227 offset:1024
	ds_read_b128 v[28:31], v227
	ds_read_b128 v[32:35], v228
	ds_read_b128 v[36:39], v228 offset:1024
	ds_read_b128 v[40:43], v228 offset:2048
	ds_read_b128 v[44:47], v228 offset:3072
	ds_read_b128 v[48:51], v228 offset:4096
	ds_read_b128 v[52:55], v228 offset:5120
	ds_read_b128 v[56:59], v228 offset:6144
	ds_read_b128 v[60:63], v228 offset:7168
	s_cselect_b32 s35, s41, s43
	s_cselect_b32 s77, s40, s42
	s_lshl_b32 s46, s78, 11
	s_and_b32 s46, s46, 0x800
	s_or_b32 s54, s46, s56
	s_lshl_b64 s[48:49], s[36:37], 11
	s_add_u32 s46, s44, 0x100
	s_addc_u32 s47, s45, 0
	s_add_u32 s80, s42, 0x100
	s_addc_u32 s81, s43, 0
	s_add_u32 s50, s44, 0x180
	s_addc_u32 s51, s45, 0
	s_add_u32 s52, s42, 0x180
	s_addc_u32 s53, s43, 0
	s_add_u32 s82, s44, 0x40080
	s_addc_u32 s83, s45, 0
	s_add_i32 m0, s31, 0xc000
	s_nop 0
	global_load_lds_dwordx4 v219, s[82:83]
	s_nop 0
	s_add_i32 m0, s31, 0xe000
	s_nop 0
	global_load_lds_dwordx4 v221, s[82:83]
	s_waitcnt vmcnt(8) lgkmcnt(0)
	s_barrier
	s_waitcnt lgkmcnt(7)
	v_mfma_i32_16x16x64_i8 v[64:67], v[28:31], v[32:35], 0
	s_mov_b32 s37, 0
	v_mfma_i32_16x16x64_i8 v[68:71], v[20:23], v[32:35], 0
	s_waitcnt lgkmcnt(5)
	v_mfma_i32_16x16x64_i8 v[72:75], v[28:31], v[40:43], 0
	v_mfma_i32_16x16x64_i8 v[76:79], v[20:23], v[40:43], 0
	s_waitcnt lgkmcnt(3)
	v_mfma_i32_16x16x64_i8 v[80:83], v[28:31], v[48:51], 0
	v_mfma_i32_16x16x64_i8 v[84:87], v[20:23], v[48:51], 0
	s_waitcnt lgkmcnt(1)
	v_mfma_i32_16x16x64_i8 v[92:95], v[20:23], v[56:59], 0
	v_mfma_i32_16x16x64_i8 v[136:139], v[24:27], v[36:39], v[64:67]
	v_mfma_i32_16x16x64_i8 v[148:151], v[24:27], v[44:47], v[72:75]
	v_mfma_i32_16x16x64_i8 v[144:147], v[16:19], v[36:39], v[68:71]
	v_mfma_i32_16x16x64_i8 v[76:79], v[16:19], v[44:47], v[76:79]
	v_mfma_i32_16x16x64_i8 v[80:83], v[24:27], v[52:55], v[80:83]
	v_mfma_i32_16x16x64_i8 v[88:91], v[28:31], v[56:59], 0
	v_mfma_i32_16x16x64_i8 v[84:87], v[16:19], v[52:55], v[84:87]
	s_waitcnt lgkmcnt(0)
	v_mfma_i32_16x16x64_i8 v[92:95], v[16:19], v[60:63], v[92:95]
	v_mfma_i32_16x16x64_i8 v[88:91], v[24:27], v[60:63], v[88:91]
	v_mfma_i32_16x16x64_i8 v[96:99], v[12:15], v[32:35], 0
	v_mfma_i32_16x16x64_i8 v[32:35], v[4:7], v[32:35], 0
	v_mfma_i32_16x16x64_i8 v[96:99], v[8:11], v[36:39], v[96:99]
	v_mfma_i32_16x16x64_i8 v[32:35], v[0:3], v[36:39], v[32:35]
	v_mfma_i32_16x16x64_i8 v[36:39], v[12:15], v[40:43], 0
	v_mfma_i32_16x16x64_i8 v[40:43], v[4:7], v[40:43], 0
	v_mfma_i32_16x16x64_i8 v[36:39], v[8:11], v[44:47], v[36:39]
	v_mfma_i32_16x16x64_i8 v[40:43], v[0:3], v[44:47], v[40:43]
	v_mfma_i32_16x16x64_i8 v[44:47], v[12:15], v[48:51], 0
	v_mfma_i32_16x16x64_i8 v[48:51], v[4:7], v[48:51], 0
	v_mfma_i32_16x16x64_i8 v[44:47], v[8:11], v[52:55], v[44:47]
	v_mfma_i32_16x16x64_i8 v[48:51], v[0:3], v[52:55], v[48:51]
	v_mfma_i32_16x16x64_i8 v[52:55], v[12:15], v[56:59], 0
	v_mfma_i32_16x16x64_i8 v[56:59], v[4:7], v[56:59], 0
	v_mfma_i32_16x16x64_i8 v[52:55], v[8:11], v[60:63], v[52:55]
	v_mfma_i32_16x16x64_i8 v[56:59], v[0:3], v[60:63], v[56:59]
	s_barrier
	ds_read_b128 v[60:63], v228 offset:16384
	ds_read_b128 v[100:103], v228 offset:17408
	ds_read_b128 v[104:107], v228 offset:18432
	ds_read_b128 v[108:111], v228 offset:19456
	ds_read_b128 v[112:115], v228 offset:20480
	ds_read_b128 v[116:119], v228 offset:21504
	ds_read_b128 v[120:123], v228 offset:22528
	ds_read_b128 v[124:127], v228 offset:23552
	s_add_i32 m0, s31, 0x10000
	s_nop 0
	global_load_lds_dwordx4 v220, s[80:81]
	s_nop 0
	s_add_i32 m0, s31, 0x12000
	s_nop 0
	global_load_lds_dwordx4 v222, s[80:81]
	s_add_u32 s80, s42, 0x40100
	s_addc_u32 s81, s43, 0
	s_add_i32 m0, s31, 0x14000
	s_nop 0
	global_load_lds_dwordx4 v220, s[80:81]
	s_nop 0
	s_add_i32 m0, s31, 0x16000
	s_nop 0
	global_load_lds_dwordx4 v222, s[80:81]
	s_nop 0
	s_add_i32 m0, s31, 0
	s_nop 0
	global_load_lds_dwordx4 v219, s[46:47]
	s_nop 0
	s_add_i32 m0, s31, 0x2000
	s_nop 0
	global_load_lds_dwordx4 v221, s[46:47]
	s_waitcnt vmcnt(8) lgkmcnt(0)
	s_barrier
	v_mfma_i32_16x16x64_i8 v[132:135], v[20:23], v[60:63], 0
	v_mfma_i32_16x16x64_i8 v[168:171], v[16:19], v[100:103], v[132:135]
	v_mfma_i32_16x16x64_i8 v[132:135], v[28:31], v[104:107], 0
	v_mfma_i32_16x16x64_i8 v[204:207], v[24:27], v[108:111], v[132:135]
	v_mfma_i32_16x16x64_i8 v[132:135], v[20:23], v[104:107], 0
	v_mfma_i32_16x16x64_i8 v[128:131], v[28:31], v[60:63], 0
	v_mfma_i32_16x16x64_i8 v[214:217], v[16:19], v[108:111], v[132:135]
	v_mfma_i32_16x16x64_i8 v[132:135], v[28:31], v[112:115], 0
	v_mfma_i32_16x16x64_i8 v[128:131], v[24:27], v[100:103], v[128:131]
	v_mfma_i32_16x16x64_i8 v[232:235], v[24:27], v[116:119], v[132:135]
	v_mfma_i32_16x16x64_i8 v[132:135], v[20:23], v[112:115], 0
	v_mfma_i32_16x16x64_i8 v[28:31], v[28:31], v[120:123], 0
	v_mfma_i32_16x16x64_i8 v[20:23], v[20:23], v[120:123], 0
	v_mfma_i32_16x16x64_i8 v[236:239], v[16:19], v[116:119], v[132:135]
	v_mfma_i32_16x16x64_i8 v[24:27], v[24:27], v[124:127], v[28:31]
	v_mfma_i32_16x16x64_i8 v[16:19], v[16:19], v[124:127], v[20:23]
	v_mfma_i32_16x16x64_i8 v[20:23], v[12:15], v[60:63], 0
	v_mfma_i32_16x16x64_i8 v[28:31], v[4:7], v[60:63], 0
	v_mfma_i32_16x16x64_i8 v[20:23], v[8:11], v[100:103], v[20:23]
	v_mfma_i32_16x16x64_i8 v[28:31], v[0:3], v[100:103], v[28:31]
	v_mfma_i32_16x16x64_i8 v[60:63], v[12:15], v[104:107], 0
	v_mfma_i32_16x16x64_i8 v[100:103], v[4:7], v[104:107], 0
	v_mfma_i32_16x16x64_i8 v[104:107], v[12:15], v[112:115], 0
	v_mfma_i32_16x16x64_i8 v[100:103], v[0:3], v[108:111], v[100:103]
	v_mfma_i32_16x16x64_i8 v[240:243], v[8:11], v[116:119], v[104:107]
	v_mfma_i32_16x16x64_i8 v[104:107], v[4:7], v[112:115], 0
	v_mfma_i32_16x16x64_i8 v[12:15], v[12:15], v[120:123], 0
	v_mfma_i32_16x16x64_i8 v[4:7], v[4:7], v[120:123], 0
	v_mfma_i32_16x16x64_i8 v[60:63], v[8:11], v[108:111], v[60:63]
	v_mfma_i32_16x16x64_i8 v[244:247], v[0:3], v[116:119], v[104:107]
	v_mfma_i32_16x16x64_i8 v[8:11], v[8:11], v[124:127], v[12:15]
	v_mfma_i32_16x16x64_i8 v[0:3], v[0:3], v[124:127], v[4:7]
	s_barrier
	s_nop 1
	ds_read_b128 v[4:7], v229
	ds_read_b128 v[12:15], v229 offset:1024
	ds_read_b128 v[104:107], v229 offset:2048
	ds_read_b128 v[116:119], v229 offset:3072
	ds_read_b128 v[124:127], v230
	ds_read_b128 v[248:251], v230 offset:1024
	ds_read_b128 v[208:211], v230 offset:2048
	ds_read_b128 v[64:67], v230 offset:3072
	ds_read_b128 v[108:111], v228 offset:32768
	ds_read_b128 v[112:115], v228 offset:33792
	ds_read_b128 v[120:123], v228 offset:34816
	ds_read_b128 v[132:135], v228 offset:35840
	ds_read_b128 v[140:143], v228 offset:36864
	ds_read_b128 v[152:155], v228 offset:37888
	ds_read_b128 v[68:71], v228 offset:38912
	ds_read_b128 v[72:75], v228 offset:39936
	s_add_u32 s44, s44, 0x40100
	s_addc_u32 s45, s45, 0
	s_add_i32 m0, s31, 0x4000
	s_nop 0
	global_load_lds_dwordx4 v219, s[44:45]
	s_nop 0
	s_add_i32 m0, s31, 0x6000
	s_nop 0
	global_load_lds_dwordx4 v221, s[44:45]
	s_waitcnt vmcnt(8) lgkmcnt(0)
	s_barrier
	v_mfma_i32_16x16x64_i8 v[76:79], v[104:107], v[120:123], v[76:79]
	v_mfma_i32_16x16x64_i8 v[180:183], v[116:119], v[132:135], v[76:79]
	v_mfma_i32_16x16x64_i8 v[76:79], v[4:7], v[140:143], v[80:83]
	v_mfma_i32_16x16x64_i8 v[136:139], v[4:7], v[108:111], v[136:139]
	v_mfma_i32_16x16x64_i8 v[164:167], v[12:15], v[152:155], v[76:79]
	v_mfma_i32_16x16x64_i8 v[76:79], v[104:107], v[140:143], v[84:87]
	v_mfma_i32_16x16x64_i8 v[200:203], v[12:15], v[112:115], v[136:139]
	v_mfma_i32_16x16x64_i8 v[136:139], v[104:107], v[108:111], v[144:147]
	v_mfma_i32_16x16x64_i8 v[160:163], v[116:119], v[152:155], v[76:79]
	v_mfma_i32_16x16x64_i8 v[76:79], v[4:7], v[68:71], v[88:91]
	v_mfma_i32_16x16x64_i8 v[196:199], v[116:119], v[112:115], v[136:139]
	v_mfma_i32_16x16x64_i8 v[136:139], v[4:7], v[120:123], v[148:151]
	v_mfma_i32_16x16x64_i8 v[148:151], v[12:15], v[72:75], v[76:79]
	v_mfma_i32_16x16x64_i8 v[76:79], v[104:107], v[68:71], v[92:95]
	v_mfma_i32_16x16x64_i8 v[184:187], v[12:15], v[132:135], v[136:139]
	v_mfma_i32_16x16x64_i8 v[144:147], v[116:119], v[72:75], v[76:79]
	v_mfma_i32_16x16x64_i8 v[32:35], v[208:211], v[108:111], v[32:35]
	v_mfma_i32_16x16x64_i8 v[188:191], v[64:67], v[112:115], v[32:35]
	v_mfma_i32_16x16x64_i8 v[32:35], v[124:127], v[120:123], v[36:39]
	v_mfma_i32_16x16x64_i8 v[176:179], v[248:251], v[132:135], v[32:35]
	v_mfma_i32_16x16x64_i8 v[32:35], v[208:211], v[120:123], v[40:43]
	v_mfma_i32_16x16x64_i8 v[172:175], v[64:67], v[132:135], v[32:35]
	v_mfma_i32_16x16x64_i8 v[32:35], v[124:127], v[140:143], v[44:47]
	v_mfma_i32_16x16x64_i8 v[156:159], v[248:251], v[152:155], v[32:35]
	v_mfma_i32_16x16x64_i8 v[32:35], v[208:211], v[140:143], v[48:51]
	v_mfma_i32_16x16x64_i8 v[152:155], v[64:67], v[152:155], v[32:35]
	v_mfma_i32_16x16x64_i8 v[32:35], v[124:127], v[68:71], v[52:55]
	v_mfma_i32_16x16x64_i8 v[76:79], v[124:127], v[108:111], v[96:99]
	v_mfma_i32_16x16x64_i8 v[140:143], v[248:251], v[72:75], v[32:35]
	v_mfma_i32_16x16x64_i8 v[32:35], v[208:211], v[68:71], v[56:59]
	v_mfma_i32_16x16x64_i8 v[192:195], v[248:251], v[112:115], v[76:79]
	v_mfma_i32_16x16x64_i8 v[136:139], v[64:67], v[72:75], v[32:35]
	s_barrier
	s_nop 3
	ds_read_b128 v[32:35], v228 offset:49152
	ds_read_b128 v[36:39], v228 offset:50176
	ds_read_b128 v[40:43], v228 offset:51200
	ds_read_b128 v[44:47], v228 offset:52224
	ds_read_b128 v[48:51], v228 offset:53248
	ds_read_b128 v[52:55], v228 offset:54272
	ds_read_b128 v[56:59], v228 offset:55296
	ds_read_b128 v[88:91], v228 offset:56320
	s_add_i32 m0, s31, 0x18000
	s_nop 0
	global_load_lds_dwordx4 v220, s[52:53]
	s_nop 0
	s_add_i32 m0, s31, 0x1a000
	s_nop 0
	global_load_lds_dwordx4 v222, s[52:53]
	s_add_u32 s44, s42, 0x40180
	s_addc_u32 s45, s43, 0
	s_add_i32 m0, s31, 0x1c000
	s_nop 0
	global_load_lds_dwordx4 v220, s[44:45]
	s_nop 0
	s_add_i32 m0, s31, 0x1e000
	s_nop 0
	global_load_lds_dwordx4 v222, s[44:45]
	s_nop 0
	s_add_i32 m0, s31, 0x8000
	s_nop 0
	global_load_lds_dwordx4 v219, s[50:51]
	s_nop 0
	s_add_i32 m0, s31, 0xa000
	s_nop 0
	global_load_lds_dwordx4 v221, s[50:51]
	s_waitcnt vmcnt(8) lgkmcnt(0)
	s_barrier
	v_mfma_i32_16x16x64_i8 v[68:71], v[4:7], v[32:35], v[128:131]
	v_mfma_i32_16x16x64_i8 v[132:135], v[12:15], v[36:39], v[68:71]
	v_mfma_i32_16x16x64_i8 v[68:71], v[104:107], v[32:35], v[168:171]
	v_mfma_i32_16x16x64_i8 v[128:131], v[116:119], v[36:39], v[68:71]
	v_mfma_i32_16x16x64_i8 v[68:71], v[4:7], v[40:43], v[204:207]
	v_mfma_i32_16x16x64_i8 v[112:115], v[12:15], v[44:47], v[68:71]
	v_mfma_i32_16x16x64_i8 v[68:71], v[104:107], v[40:43], v[214:217]
	v_mfma_i32_16x16x64_i8 v[108:111], v[116:119], v[44:47], v[68:71]
	v_mfma_i32_16x16x64_i8 v[68:71], v[4:7], v[48:51], v[232:235]
	v_mfma_i32_16x16x64_i8 v[4:7], v[4:7], v[56:59], v[24:27]
	v_mfma_i32_16x16x64_i8 v[96:99], v[12:15], v[52:55], v[68:71]
	v_mfma_i32_16x16x64_i8 v[68:71], v[104:107], v[48:51], v[236:239]
	v_mfma_i32_16x16x64_i8 v[76:79], v[12:15], v[88:91], v[4:7]
	v_mfma_i32_16x16x64_i8 v[4:7], v[104:107], v[56:59], v[16:19]
	v_mfma_i32_16x16x64_i8 v[92:95], v[116:119], v[52:55], v[68:71]
	v_mfma_i32_16x16x64_i8 v[72:75], v[116:119], v[88:91], v[4:7]
	v_mfma_i32_16x16x64_i8 v[4:7], v[124:127], v[32:35], v[20:23]
	v_mfma_i32_16x16x64_i8 v[120:123], v[248:251], v[36:39], v[4:7]
	v_mfma_i32_16x16x64_i8 v[4:7], v[208:211], v[32:35], v[28:31]
	v_mfma_i32_16x16x64_i8 v[116:119], v[64:67], v[36:39], v[4:7]
	v_mfma_i32_16x16x64_i8 v[4:7], v[124:127], v[40:43], v[60:63]
	v_mfma_i32_16x16x64_i8 v[104:107], v[248:251], v[44:47], v[4:7]
	v_mfma_i32_16x16x64_i8 v[4:7], v[208:211], v[40:43], v[100:103]
	v_mfma_i32_16x16x64_i8 v[100:103], v[64:67], v[44:47], v[4:7]
	v_mfma_i32_16x16x64_i8 v[4:7], v[124:127], v[48:51], v[240:243]
	v_mfma_i32_16x16x64_i8 v[84:87], v[248:251], v[52:55], v[4:7]
	v_mfma_i32_16x16x64_i8 v[4:7], v[208:211], v[48:51], v[244:247]
	v_mfma_i32_16x16x64_i8 v[80:83], v[64:67], v[52:55], v[4:7]
	v_mfma_i32_16x16x64_i8 v[4:7], v[124:127], v[56:59], v[8:11]
	v_mfma_i32_16x16x64_i8 v[0:3], v[208:211], v[56:59], v[0:3]
	v_mfma_i32_16x16x64_i8 v[68:71], v[248:251], v[88:91], v[4:7]
	v_mfma_i32_16x16x64_i8 v[64:67], v[64:67], v[88:91], v[0:3]
	s_barrier
	s_add_u32 s44, s27, s48
	s_addc_u32 s45, s29, s49
	s_add_u32 s79, s42, 0x200
	s_addc_u32 s80, s43, 0
	s_add_i32 s81, s54, 0
	s_add_i32 s81, s81, 0x20000

.LBB0_933:
	ds_read_b128 v[0:3], v227
	ds_read_b128 v[4:7], v227 offset:1024
	ds_read_b128 v[8:11], v227 offset:2048
	ds_read_b128 v[12:15], v227 offset:3072
	ds_read_b128 v[16:19], v226
	ds_read_b128 v[20:23], v226 offset:1024
	ds_read_b128 v[24:27], v226 offset:2048
	ds_read_b128 v[28:31], v226 offset:3072
	ds_read_b128 v[32:35], v228
	ds_read_b128 v[36:39], v228 offset:1024
	ds_read_b128 v[40:43], v228 offset:2048
	ds_read_b128 v[44:47], v228 offset:3072
	ds_read_b128 v[48:51], v228 offset:4096
	ds_read_b128 v[52:55], v228 offset:5120
	ds_read_b128 v[56:59], v228 offset:6144
	ds_read_b128 v[60:63], v228 offset:7168
	s_add_u32 s42, s46, 0x100
	s_addc_u32 s43, s47, 0
	s_and_b64 s[48:49], s[48:49], exec
	s_cselect_b32 s54, s76, s42
	s_cselect_b32 s55, s9, s43
	s_cselect_b32 s51, s35, s80
	s_cselect_b32 s50, s77, s79
	s_add_u32 s48, s54, 0x80
	s_addc_u32 s49, s55, 0
	s_add_u32 s52, s50, 0x80
	s_addc_u32 s53, s51, 0
	s_add_u32 s46, s46, 0x40080
	s_addc_u32 s47, s47, 0
	s_add_i32 m0, s31, 0xc000
	s_nop 0
	global_load_lds_dwordx4 v219, s[46:47]
	s_nop 0
	s_add_i32 m0, s31, 0xe000
	s_nop 0
	global_load_lds_dwordx4 v221, s[46:47]
	s_waitcnt vmcnt(8) lgkmcnt(0)
	s_barrier
	v_mfma_i32_16x16x64_i8 v[180:183], v[8:11], v[40:43], v[180:183]
	v_mfma_i32_16x16x64_i8 v[164:167], v[0:3], v[48:51], v[164:167]
	v_mfma_i32_16x16x64_i8 v[148:151], v[0:3], v[56:59], v[148:151]
	v_mfma_i32_16x16x64_i8 v[160:163], v[8:11], v[48:51], v[160:163]
	v_mfma_i32_16x16x64_i8 v[144:147], v[8:11], v[56:59], v[144:147]
	v_mfma_i32_16x16x64_i8 v[88:91], v[0:3], v[32:35], v[200:203]
	v_mfma_i32_16x16x64_i8 v[168:171], v[0:3], v[40:43], v[184:187]
	v_mfma_i32_16x16x64_i8 v[124:127], v[8:11], v[32:35], v[196:199]
	v_mfma_i32_16x16x64_i8 v[180:183], v[12:15], v[44:47], v[180:183]
	v_mfma_i32_16x16x64_i8 v[164:167], v[4:7], v[52:55], v[164:167]
	v_mfma_i32_16x16x64_i8 v[148:151], v[4:7], v[60:63], v[148:151]
	v_mfma_i32_16x16x64_i8 v[160:163], v[12:15], v[52:55], v[160:163]
	v_mfma_i32_16x16x64_i8 v[144:147], v[12:15], v[60:63], v[144:147]
	v_mfma_i32_16x16x64_i8 v[88:91], v[4:7], v[36:39], v[88:91]
	v_mfma_i32_16x16x64_i8 v[168:171], v[4:7], v[44:47], v[168:171]
	v_mfma_i32_16x16x64_i8 v[124:127], v[12:15], v[36:39], v[124:127]
	v_mfma_i32_16x16x64_i8 v[184:187], v[16:19], v[32:35], v[192:195]
	v_mfma_i32_16x16x64_i8 v[32:35], v[24:27], v[32:35], v[188:191]
	v_mfma_i32_16x16x64_i8 v[192:195], v[20:23], v[36:39], v[184:187]
	v_mfma_i32_16x16x64_i8 v[32:35], v[28:31], v[36:39], v[32:35]
	v_mfma_i32_16x16x64_i8 v[36:39], v[16:19], v[40:43], v[176:179]
	v_mfma_i32_16x16x64_i8 v[40:43], v[24:27], v[40:43], v[172:175]
	v_mfma_i32_16x16x64_i8 v[36:39], v[20:23], v[44:47], v[36:39]
	v_mfma_i32_16x16x64_i8 v[40:43], v[28:31], v[44:47], v[40:43]
	v_mfma_i32_16x16x64_i8 v[44:47], v[16:19], v[48:51], v[156:159]
	v_mfma_i32_16x16x64_i8 v[48:51], v[24:27], v[48:51], v[152:155]
	v_mfma_i32_16x16x64_i8 v[44:47], v[20:23], v[52:55], v[44:47]
	v_mfma_i32_16x16x64_i8 v[48:51], v[28:31], v[52:55], v[48:51]
	v_mfma_i32_16x16x64_i8 v[52:55], v[16:19], v[56:59], v[140:143]
	v_mfma_i32_16x16x64_i8 v[56:59], v[24:27], v[56:59], v[136:139]
	v_mfma_i32_16x16x64_i8 v[52:55], v[20:23], v[60:63], v[52:55]
	v_mfma_i32_16x16x64_i8 v[56:59], v[28:31], v[60:63], v[56:59]
	s_barrier
	ds_read_b128 v[60:63], v228 offset:16384
	ds_read_b128 v[136:139], v228 offset:17408
	ds_read_b128 v[140:143], v228 offset:18432
	ds_read_b128 v[152:155], v228 offset:19456
	ds_read_b128 v[156:159], v228 offset:20480
	ds_read_b128 v[172:175], v228 offset:21504
	ds_read_b128 v[176:179], v228 offset:22528
	ds_read_b128 v[184:187], v228 offset:23552
	s_add_i32 m0, s31, 0x10000
	s_nop 0
	global_load_lds_dwordx4 v220, s[50:51]
	s_nop 0
	s_add_i32 m0, s31, 0x12000
	s_nop 0
	global_load_lds_dwordx4 v222, s[50:51]
	s_add_u32 s46, s50, 0x40000
	s_addc_u32 s47, s51, 0
	s_add_i32 m0, s31, 0x14000
	s_nop 0
	global_load_lds_dwordx4 v220, s[46:47]
	s_nop 0
	s_add_i32 m0, s31, 0x16000
	s_nop 0
	global_load_lds_dwordx4 v222, s[46:47]
	s_nop 0
	s_add_i32 m0, s31, 0
	s_nop 0
	global_load_lds_dwordx4 v219, s[54:55]
	s_nop 0
	s_add_i32 m0, s31, 0x2000
	s_nop 0
	global_load_lds_dwordx4 v221, s[54:55]
	s_waitcnt vmcnt(8) lgkmcnt(0)
	s_barrier
	v_mfma_i32_16x16x64_i8 v[132:135], v[0:3], v[60:63], v[132:135]
	v_mfma_i32_16x16x64_i8 v[112:115], v[0:3], v[140:143], v[112:115]
	v_mfma_i32_16x16x64_i8 v[96:99], v[0:3], v[156:159], v[96:99]
	v_mfma_i32_16x16x64_i8 v[0:3], v[0:3], v[176:179], v[76:79]
	v_mfma_i32_16x16x64_i8 v[128:131], v[8:11], v[60:63], v[128:131]
	v_mfma_i32_16x16x64_i8 v[108:111], v[8:11], v[140:143], v[108:111]
	v_mfma_i32_16x16x64_i8 v[92:95], v[8:11], v[156:159], v[92:95]
	v_mfma_i32_16x16x64_i8 v[76:79], v[4:7], v[184:187], v[0:3]
	v_mfma_i32_16x16x64_i8 v[0:3], v[8:11], v[176:179], v[72:75]
	v_mfma_i32_16x16x64_i8 v[132:135], v[4:7], v[136:139], v[132:135]
	v_mfma_i32_16x16x64_i8 v[128:131], v[12:15], v[136:139], v[128:131]
	v_mfma_i32_16x16x64_i8 v[112:115], v[4:7], v[152:155], v[112:115]
	v_mfma_i32_16x16x64_i8 v[108:111], v[12:15], v[152:155], v[108:111]
	v_mfma_i32_16x16x64_i8 v[96:99], v[4:7], v[172:175], v[96:99]
	v_mfma_i32_16x16x64_i8 v[92:95], v[12:15], v[172:175], v[92:95]
	v_mfma_i32_16x16x64_i8 v[72:75], v[12:15], v[184:187], v[0:3]
	v_mfma_i32_16x16x64_i8 v[0:3], v[16:19], v[60:63], v[120:123]
	v_mfma_i32_16x16x64_i8 v[120:123], v[20:23], v[136:139], v[0:3]
	v_mfma_i32_16x16x64_i8 v[0:3], v[24:27], v[60:63], v[116:119]
	v_mfma_i32_16x16x64_i8 v[116:119], v[28:31], v[136:139], v[0:3]
	v_mfma_i32_16x16x64_i8 v[0:3], v[16:19], v[140:143], v[104:107]
	v_mfma_i32_16x16x64_i8 v[104:107], v[20:23], v[152:155], v[0:3]
	v_mfma_i32_16x16x64_i8 v[0:3], v[24:27], v[140:143], v[100:103]
	v_mfma_i32_16x16x64_i8 v[100:103], v[28:31], v[152:155], v[0:3]
	v_mfma_i32_16x16x64_i8 v[0:3], v[16:19], v[156:159], v[84:87]
	v_mfma_i32_16x16x64_i8 v[84:87], v[20:23], v[172:175], v[0:3]
	v_mfma_i32_16x16x64_i8 v[0:3], v[24:27], v[156:159], v[80:83]
	v_mfma_i32_16x16x64_i8 v[80:83], v[28:31], v[172:175], v[0:3]
	v_mfma_i32_16x16x64_i8 v[0:3], v[16:19], v[176:179], v[68:71]
	v_mfma_i32_16x16x64_i8 v[68:71], v[20:23], v[184:187], v[0:3]
	v_mfma_i32_16x16x64_i8 v[0:3], v[24:27], v[176:179], v[64:67]
	v_mfma_i32_16x16x64_i8 v[64:67], v[28:31], v[184:187], v[0:3]
	s_barrier
	ds_read_b128 v[16:19], v229
	ds_read_b128 v[8:11], v229 offset:1024
	ds_read_b128 v[4:7], v229 offset:2048
	s_nop 1
	ds_read_b128 v[0:3], v229 offset:3072
	ds_read_b128 v[28:31], v230
	ds_read_b128 v[24:27], v230 offset:1024
	ds_read_b128 v[20:23], v230 offset:2048
	ds_read_b128 v[12:15], v230 offset:3072
	ds_read_b128 v[60:63], v228 offset:32768
	ds_read_b128 v[136:139], v228 offset:33792
	ds_read_b128 v[140:143], v228 offset:34816
	ds_read_b128 v[152:155], v228 offset:35840
	ds_read_b128 v[204:207], v228 offset:36864
	ds_read_b128 v[208:211], v228 offset:37888
	ds_read_b128 v[214:217], v228 offset:38912
	ds_read_b128 v[232:235], v228 offset:39936
	s_add_u32 s46, s54, 0x40000
	s_addc_u32 s47, s55, 0
	s_add_i32 m0, s31, 0x4000
	s_nop 0
	global_load_lds_dwordx4 v219, s[46:47]
	s_nop 0
	s_add_i32 m0, s31, 0x6000
	s_nop 0
	global_load_lds_dwordx4 v221, s[46:47]
	s_waitcnt vmcnt(8) lgkmcnt(0)
	s_barrier
	v_mfma_i32_16x16x64_i8 v[88:91], v[16:19], v[60:63], v[88:91]
	v_mfma_i32_16x16x64_i8 v[200:203], v[8:11], v[136:139], v[88:91]
	v_mfma_i32_16x16x64_i8 v[88:91], v[4:7], v[60:63], v[124:127]
	v_mfma_i32_16x16x64_i8 v[196:199], v[0:3], v[136:139], v[88:91]
	v_mfma_i32_16x16x64_i8 v[88:91], v[16:19], v[140:143], v[168:171]
	v_mfma_i32_16x16x64_i8 v[184:187], v[8:11], v[152:155], v[88:91]
	v_mfma_i32_16x16x64_i8 v[88:91], v[4:7], v[140:143], v[180:183]
	v_mfma_i32_16x16x64_i8 v[180:183], v[0:3], v[152:155], v[88:91]
	v_mfma_i32_16x16x64_i8 v[88:91], v[16:19], v[204:207], v[164:167]
	v_mfma_i32_16x16x64_i8 v[164:167], v[8:11], v[208:211], v[88:91]
	v_mfma_i32_16x16x64_i8 v[88:91], v[4:7], v[204:207], v[160:163]
	v_mfma_i32_16x16x64_i8 v[160:163], v[0:3], v[208:211], v[88:91]
	v_mfma_i32_16x16x64_i8 v[88:91], v[16:19], v[214:217], v[148:151]
	v_mfma_i32_16x16x64_i8 v[148:151], v[8:11], v[232:235], v[88:91]
	v_mfma_i32_16x16x64_i8 v[88:91], v[4:7], v[214:217], v[144:147]
	v_mfma_i32_16x16x64_i8 v[144:147], v[0:3], v[232:235], v[88:91]
	v_mfma_i32_16x16x64_i8 v[32:35], v[20:23], v[60:63], v[32:35]
	v_mfma_i32_16x16x64_i8 v[188:191], v[12:15], v[136:139], v[32:35]
	v_mfma_i32_16x16x64_i8 v[32:35], v[28:31], v[140:143], v[36:39]
	v_mfma_i32_16x16x64_i8 v[176:179], v[24:27], v[152:155], v[32:35]
	v_mfma_i32_16x16x64_i8 v[32:35], v[20:23], v[140:143], v[40:43]
	v_mfma_i32_16x16x64_i8 v[172:175], v[12:15], v[152:155], v[32:35]
	v_mfma_i32_16x16x64_i8 v[32:35], v[28:31], v[204:207], v[44:47]
	v_mfma_i32_16x16x64_i8 v[156:159], v[24:27], v[208:211], v[32:35]
	v_mfma_i32_16x16x64_i8 v[32:35], v[20:23], v[204:207], v[48:51]
	v_mfma_i32_16x16x64_i8 v[152:155], v[12:15], v[208:211], v[32:35]
	v_mfma_i32_16x16x64_i8 v[32:35], v[28:31], v[214:217], v[52:55]
	v_mfma_i32_16x16x64_i8 v[88:91], v[28:31], v[60:63], v[192:195]
	v_mfma_i32_16x16x64_i8 v[140:143], v[24:27], v[232:235], v[32:35]
	v_mfma_i32_16x16x64_i8 v[32:35], v[20:23], v[214:217], v[56:59]
	v_mfma_i32_16x16x64_i8 v[192:195], v[24:27], v[136:139], v[88:91]
	v_mfma_i32_16x16x64_i8 v[136:139], v[12:15], v[232:235], v[32:35]
	s_barrier
	ds_read_b128 v[60:63], v228 offset:49152
	ds_read_b128 v[56:59], v228 offset:50176
	ds_read_b128 v[52:55], v228 offset:51200
	ds_read_b128 v[48:51], v228 offset:52224
	ds_read_b128 v[44:47], v228 offset:53248
	ds_read_b128 v[40:43], v228 offset:54272
	ds_read_b128 v[36:39], v228 offset:55296
	ds_read_b128 v[32:35], v228 offset:56320
	s_add_i32 m0, s31, 0x18000
	s_nop 0
	global_load_lds_dwordx4 v220, s[52:53]
	s_nop 0
	s_add_i32 m0, s31, 0x1a000
	s_nop 0
	global_load_lds_dwordx4 v222, s[52:53]
	s_add_u32 s46, s50, 0x40080
	s_addc_u32 s47, s51, 0
	s_add_i32 m0, s31, 0x1c000
	s_nop 0
	global_load_lds_dwordx4 v220, s[46:47]
	s_nop 0
	s_add_i32 m0, s31, 0x1e000
	s_nop 0
	global_load_lds_dwordx4 v222, s[46:47]
	s_nop 0
	s_add_i32 m0, s31, 0x8000
	s_nop 0
	global_load_lds_dwordx4 v219, s[48:49]
	s_nop 0
	s_add_i32 m0, s31, 0xa000
	s_nop 0
	global_load_lds_dwordx4 v221, s[48:49]
	s_waitcnt vmcnt(8) lgkmcnt(0)
	s_barrier
	v_mfma_i32_16x16x64_i8 v[88:91], v[16:19], v[60:63], v[132:135]
	v_mfma_i32_16x16x64_i8 v[132:135], v[8:11], v[56:59], v[88:91]
	v_mfma_i32_16x16x64_i8 v[88:91], v[4:7], v[60:63], v[128:131]
	v_mfma_i32_16x16x64_i8 v[128:131], v[0:3], v[56:59], v[88:91]
	v_mfma_i32_16x16x64_i8 v[88:91], v[16:19], v[52:55], v[112:115]
	v_mfma_i32_16x16x64_i8 v[112:115], v[8:11], v[48:51], v[88:91]
	v_mfma_i32_16x16x64_i8 v[88:91], v[4:7], v[52:55], v[108:111]
	v_mfma_i32_16x16x64_i8 v[108:111], v[0:3], v[48:51], v[88:91]
	v_mfma_i32_16x16x64_i8 v[88:91], v[16:19], v[44:47], v[96:99]
	v_mfma_i32_16x16x64_i8 v[96:99], v[8:11], v[40:43], v[88:91]
	v_mfma_i32_16x16x64_i8 v[88:91], v[4:7], v[44:47], v[92:95]
	v_mfma_i32_16x16x64_i8 v[76:79], v[16:19], v[36:39], v[76:79]
	v_mfma_i32_16x16x64_i8 v[72:75], v[4:7], v[36:39], v[72:75]
	v_mfma_i32_16x16x64_i8 v[92:95], v[0:3], v[40:43], v[88:91]
	v_mfma_i32_16x16x64_i8 v[76:79], v[8:11], v[32:35], v[76:79]
	v_mfma_i32_16x16x64_i8 v[72:75], v[0:3], v[32:35], v[72:75]
	v_mfma_i32_16x16x64_i8 v[88:91], v[28:31], v[60:63], v[120:123]
	v_mfma_i32_16x16x64_i8 v[120:123], v[24:27], v[56:59], v[88:91]
	v_mfma_i32_16x16x64_i8 v[88:91], v[20:23], v[60:63], v[116:119]
	v_mfma_i32_16x16x64_i8 v[116:119], v[12:15], v[56:59], v[88:91]
	v_mfma_i32_16x16x64_i8 v[88:91], v[28:31], v[52:55], v[104:107]
	v_mfma_i32_16x16x64_i8 v[104:107], v[24:27], v[48:51], v[88:91]
	v_mfma_i32_16x16x64_i8 v[88:91], v[20:23], v[52:55], v[100:103]
	v_mfma_i32_16x16x64_i8 v[84:87], v[28:31], v[44:47], v[84:87]
	v_mfma_i32_16x16x64_i8 v[80:83], v[20:23], v[44:47], v[80:83]
	v_mfma_i32_16x16x64_i8 v[68:71], v[28:31], v[36:39], v[68:71]
	v_mfma_i32_16x16x64_i8 v[64:67], v[20:23], v[36:39], v[64:67]
	v_mfma_i32_16x16x64_i8 v[100:103], v[12:15], v[48:51], v[88:91]
	v_mfma_i32_16x16x64_i8 v[84:87], v[24:27], v[40:43], v[84:87]
	v_mfma_i32_16x16x64_i8 v[80:83], v[12:15], v[40:43], v[80:83]
	v_mfma_i32_16x16x64_i8 v[68:71], v[24:27], v[32:35], v[68:71]
	v_mfma_i32_16x16x64_i8 v[64:67], v[12:15], v[32:35], v[64:67]
	s_barrier
	s_add_i32 s37, s37, 2
	s_add_u32 s79, s79, 0x100
	s_addc_u32 s80, s80, 0
	s_cmp_gt_u32 s37, 13
	s_cbranch_scc1 .LBB0_935
	s_mov_b64 s[46:47], s[42:43]
	s_branch .LBB0_931

.LBB0_1041:
	s_cmp_gt_u32 s93, 8
	s_cbranch_scc0 .LBB0_1095
	s_waitcnt vmcnt(0) lgkmcnt(0)
	s_barrier
	s_and_saveexec_b64 s[4:5], s[72:73]
	s_cbranch_execz .LBB0_1094
	s_add_u32 s6, s70, 0x4200
	s_addc_u32 s7, s71, 0
	s_add_i32 s2, 0, 0x23f20
	v_mov_b32_e32 v0, s2
	s_waitcnt vmcnt(0) expcnt(0) lgkmcnt(0)
	ds_read_b32 v2, v0
	s_add_i32 s2, 0, 0x23f24
	v_mov_b32_e32 v0, s2
	ds_read_b32 v0, v0
	s_waitcnt lgkmcnt(1)
	v_cmp_ne_u32_e32 vcc, 0, v2
	s_cbranch_vccnz .LBB0_1058
	s_add_u32 s8, s70, 0x4400
	s_addc_u32 s9, s71, 0
	s_add_u32 s10, s70, 0x4500
	s_addc_u32 s11, s71, 0
	s_add_u32 s14, s70, 0x4600
	s_addc_u32 s15, s71, 0
	s_add_u32 s16, s70, 0x4700
	s_addc_u32 s17, s71, 0
	s_add_u32 s18, s70, 0x4800
	s_addc_u32 s19, s71, 0
	s_add_u32 s20, s70, 0x4900
	s_addc_u32 s21, s71, 0
	s_add_u32 s22, s70, 0x4a00
	s_addc_u32 s23, s71, 0
	s_add_u32 s24, s70, 0x4b00
	s_addc_u32 s25, s71, 0
	s_add_u32 s26, s70, 0x4c00
	s_addc_u32 s27, s71, 0
	s_add_u32 s28, s70, 0x4d00
	s_addc_u32 s29, s71, 0
	s_add_u32 s30, s70, 0x4e00
	s_addc_u32 s31, s71, 0
	s_add_u32 s34, s70, 0x4f00
	s_addc_u32 s35, s71, 0
	s_add_u32 s36, s70, 0x5000
	s_addc_u32 s37, s71, 0
	s_load_dwordx2 s[44:45], s[90:91], 0x4
	s_add_u32 s38, s70, 0x5100
	s_addc_u32 s39, s71, 0
	s_add_u32 s40, s70, 0x5200
	s_addc_u32 s41, s71, 0
	s_add_u32 s42, s70, 0x5300
	s_waitcnt lgkmcnt(0)
	s_mul_i32 s2, s44, s33
	s_addc_u32 s43, s71, 0
	s_mul_i32 s2, s2, s45
	s_mov_b32 s50, 1
	v_mov_b32_e32 v16, 0
	s_branch .LBB0_1046

.LBB0_1108:
	s_ashr_i32 s23, s22, 31
	s_lshl_b64 s[24:25], s[22:23], 20
	s_add_u32 s24, s42, s24
	s_addc_u32 s25, s43, s25
	s_and_b64 s[26:27], s[4:5], exec
	ds_read_b128 v[0:3], v143
	ds_read_b128 v[4:7], v143 offset:1024
	ds_read_b128 v[8:11], v143 offset:2048
	s_waitcnt vmcnt(2)
	ds_read_b128 v[12:15], v143 offset:3072
	s_waitcnt vmcnt(1)
	ds_read_b128 v[16:19], v144
	s_waitcnt vmcnt(0)
	ds_read_b128 v[20:23], v144 offset:1024
	ds_read_b128 v[24:27], v144 offset:2048
	ds_read_b128 v[28:31], v144 offset:3072
	s_cselect_b32 s23, s25, s31
	s_cselect_b32 s51, s24, s30
	s_ashr_i32 s21, s20, 31
	s_lshl_b64 s[26:27], s[20:21], 20
	s_add_u32 s26, s44, s26
	s_addc_u32 s27, s45, s27
	s_and_b64 s[36:37], s[4:5], exec
	s_cselect_b32 s21, s27, s35
	s_cselect_b32 s52, s26, s34
	s_add_u32 s40, s30, 0x100
	s_addc_u32 s41, s31, 0
	s_add_u32 s54, s34, 0x100
	s_addc_u32 s55, s35, 0
	s_add_u32 s36, s30, 0x180
	s_addc_u32 s37, s31, 0
	ds_read_b128 v[32:35], v145
	ds_read_b128 v[36:39], v145 offset:1024
	ds_read_b128 v[40:43], v145 offset:2048
	ds_read_b128 v[44:47], v145 offset:3072
	ds_read_b128 v[48:51], v145 offset:4096
	ds_read_b128 v[52:55], v145 offset:5120
	ds_read_b128 v[56:59], v145 offset:6144
	ds_read_b128 v[60:63], v145 offset:7168
	s_add_u32 s38, s34, 0x180
	s_addc_u32 s39, s35, 0
	s_add_u32 s56, s30, 0x80080
	s_addc_u32 s57, s31, 0
	s_add_i32 m0, s2, 0xc000
	s_nop 0
	global_load_lds_dwordx4 v139, s[56:57]
	s_nop 0
	s_add_i32 m0, s2, 0xe000
	s_nop 0
	global_load_lds_dwordx4 v141, s[56:57]
	s_waitcnt vmcnt(8) lgkmcnt(0)
	s_barrier
	v_mfma_f32_16x16x32_bf16 v[64:67], v[0:3], v[32:35], 0
	v_mfma_f32_16x16x32_bf16 v[68:71], v[8:11], v[32:35], 0
	v_mfma_f32_16x16x32_bf16 v[76:79], v[8:11], v[40:43], 0
	v_mfma_f32_16x16x32_bf16 v[72:75], v[0:3], v[40:43], 0
	v_mfma_f32_16x16x32_bf16 v[80:83], v[0:3], v[48:51], 0
	v_mfma_f32_16x16x32_bf16 v[84:87], v[8:11], v[48:51], 0
	v_mfma_f32_16x16x32_bf16 v[92:95], v[8:11], v[56:59], 0
	v_mfma_f32_16x16x32_bf16 v[88:91], v[0:3], v[56:59], 0
	v_mfma_f32_16x16x32_bf16 v[64:67], v[4:7], v[36:39], v[64:67]
	v_mfma_f32_16x16x32_bf16 v[68:71], v[12:15], v[36:39], v[68:71]
	v_mfma_f32_16x16x32_bf16 v[76:79], v[12:15], v[44:47], v[76:79]
	v_mfma_f32_16x16x32_bf16 v[72:75], v[4:7], v[44:47], v[72:75]
	v_mfma_f32_16x16x32_bf16 v[80:83], v[4:7], v[52:55], v[80:83]
	v_mfma_f32_16x16x32_bf16 v[84:87], v[12:15], v[52:55], v[84:87]
	v_mfma_f32_16x16x32_bf16 v[96:99], v[12:15], v[60:63], v[92:95]
	v_mfma_f32_16x16x32_bf16 v[88:91], v[4:7], v[60:63], v[88:91]
	v_mfma_f32_16x16x32_bf16 v[92:95], v[16:19], v[32:35], 0
	v_mfma_f32_16x16x32_bf16 v[32:35], v[24:27], v[32:35], 0
	v_mfma_f32_16x16x32_bf16 v[104:107], v[20:23], v[36:39], v[92:95]
	v_mfma_f32_16x16x32_bf16 v[32:35], v[28:31], v[36:39], v[32:35]
	v_mfma_f32_16x16x32_bf16 v[36:39], v[16:19], v[40:43], 0
	v_mfma_f32_16x16x32_bf16 v[40:43], v[24:27], v[40:43], 0
	v_mfma_f32_16x16x32_bf16 v[36:39], v[20:23], v[44:47], v[36:39]
	v_mfma_f32_16x16x32_bf16 v[40:43], v[28:31], v[44:47], v[40:43]
	v_mfma_f32_16x16x32_bf16 v[44:47], v[16:19], v[48:51], 0
	v_mfma_f32_16x16x32_bf16 v[48:51], v[24:27], v[48:51], 0
	v_mfma_f32_16x16x32_bf16 v[44:47], v[20:23], v[52:55], v[44:47]
	v_mfma_f32_16x16x32_bf16 v[48:51], v[28:31], v[52:55], v[48:51]
	v_mfma_f32_16x16x32_bf16 v[52:55], v[16:19], v[56:59], 0
	v_mfma_f32_16x16x32_bf16 v[56:59], v[24:27], v[56:59], 0
	v_mfma_f32_16x16x32_bf16 v[52:55], v[20:23], v[60:63], v[52:55]
	v_mfma_f32_16x16x32_bf16 v[60:63], v[28:31], v[60:63], v[56:59]
	s_barrier
	s_nop 3
	ds_read_b128 v[56:59], v145 offset:16384
	ds_read_b128 v[92:95], v145 offset:17408
	ds_read_b128 v[100:103], v145 offset:18432
	ds_read_b128 v[108:111], v145 offset:19456
	ds_read_b128 v[112:115], v145 offset:20480
	ds_read_b128 v[116:119], v145 offset:21504
	ds_read_b128 v[120:123], v145 offset:22528
	ds_read_b128 v[124:127], v145 offset:23552
	s_add_i32 m0, s2, 0x10000
	s_nop 0
	global_load_lds_dwordx4 v140, s[54:55]
	s_nop 0
	s_add_i32 m0, s2, 0x12000
	s_nop 0
	global_load_lds_dwordx4 v142, s[54:55]
	s_add_u32 s54, s34, 0x80100
	s_addc_u32 s55, s35, 0
	s_add_i32 m0, s2, 0x14000
	s_nop 0
	global_load_lds_dwordx4 v140, s[54:55]
	s_nop 0
	s_add_i32 m0, s2, 0x16000
	s_nop 0
	global_load_lds_dwordx4 v142, s[54:55]
	s_nop 0
	s_add_i32 m0, s2, 0
	s_nop 0
	global_load_lds_dwordx4 v139, s[40:41]
	s_nop 0
	s_add_i32 m0, s2, 0x2000
	s_nop 0
	global_load_lds_dwordx4 v141, s[40:41]
	s_waitcnt vmcnt(8) lgkmcnt(0)
	s_barrier
	v_mfma_f32_16x16x32_bf16 v[132:135], v[0:3], v[56:59], 0
	v_mfma_f32_16x16x32_bf16 v[152:155], v[0:3], v[100:103], 0
	v_mfma_f32_16x16x32_bf16 v[160:163], v[0:3], v[112:115], 0
	v_mfma_f32_16x16x32_bf16 v[0:3], v[0:3], v[120:123], 0
	v_mfma_f32_16x16x32_bf16 v[132:135], v[4:7], v[92:95], v[132:135]
	v_mfma_f32_16x16x32_bf16 v[152:155], v[4:7], v[108:111], v[152:155]
	v_mfma_f32_16x16x32_bf16 v[160:163], v[4:7], v[116:119], v[160:163]
	v_mfma_f32_16x16x32_bf16 v[0:3], v[4:7], v[124:127], v[0:3]
	v_mfma_f32_16x16x32_bf16 v[4:7], v[8:11], v[120:123], 0
	v_mfma_f32_16x16x32_bf16 v[148:151], v[8:11], v[56:59], 0
	v_mfma_f32_16x16x32_bf16 v[156:159], v[8:11], v[100:103], 0
	v_mfma_f32_16x16x32_bf16 v[164:167], v[8:11], v[112:115], 0
	v_mfma_f32_16x16x32_bf16 v[4:7], v[12:15], v[124:127], v[4:7]
	v_mfma_f32_16x16x32_bf16 v[148:151], v[12:15], v[92:95], v[148:151]
	v_mfma_f32_16x16x32_bf16 v[156:159], v[12:15], v[108:111], v[156:159]
	v_mfma_f32_16x16x32_bf16 v[164:167], v[12:15], v[116:119], v[164:167]
	v_mfma_f32_16x16x32_bf16 v[12:15], v[24:27], v[56:59], 0
	v_mfma_f32_16x16x32_bf16 v[168:171], v[28:31], v[92:95], v[12:15]
	v_mfma_f32_16x16x32_bf16 v[12:15], v[16:19], v[100:103], 0
	v_mfma_f32_16x16x32_bf16 v[172:175], v[20:23], v[108:111], v[12:15]
	v_mfma_f32_16x16x32_bf16 v[12:15], v[24:27], v[100:103], 0
	v_mfma_f32_16x16x32_bf16 v[176:179], v[28:31], v[108:111], v[12:15]
	v_mfma_f32_16x16x32_bf16 v[12:15], v[16:19], v[112:115], 0
	v_mfma_f32_16x16x32_bf16 v[180:183], v[20:23], v[116:119], v[12:15]
	v_mfma_f32_16x16x32_bf16 v[12:15], v[24:27], v[112:115], 0
	v_mfma_f32_16x16x32_bf16 v[8:11], v[16:19], v[56:59], 0
	v_mfma_f32_16x16x32_bf16 v[184:187], v[28:31], v[116:119], v[12:15]
	v_mfma_f32_16x16x32_bf16 v[12:15], v[16:19], v[120:123], 0
	v_mfma_f32_16x16x32_bf16 v[8:11], v[20:23], v[92:95], v[8:11]
	v_mfma_f32_16x16x32_bf16 v[188:191], v[20:23], v[124:127], v[12:15]
	v_mfma_f32_16x16x32_bf16 v[12:15], v[24:27], v[120:123], 0
	v_mfma_f32_16x16x32_bf16 v[192:195], v[28:31], v[124:127], v[12:15]
	s_barrier
	s_nop 4
	ds_read_b128 v[12:15], v146
	ds_read_b128 v[16:19], v146 offset:1024
	ds_read_b128 v[24:27], v146 offset:2048
	ds_read_b128 v[196:199], v146 offset:3072
	ds_read_b128 v[200:203], v147
	ds_read_b128 v[204:207], v147 offset:1024
	ds_read_b128 v[208:211], v147 offset:2048
	ds_read_b128 v[212:215], v147 offset:3072
	ds_read_b128 v[20:23], v145 offset:32768
	ds_read_b128 v[28:31], v145 offset:33792
	ds_read_b128 v[216:219], v145 offset:34816
	ds_read_b128 v[220:223], v145 offset:35840
	ds_read_b128 v[224:227], v145 offset:36864
	ds_read_b128 v[228:231], v145 offset:37888
	ds_read_b128 v[232:235], v145 offset:38912
	ds_read_b128 v[236:239], v145 offset:39936
	s_add_u32 s40, s30, 0x80100
	s_addc_u32 s41, s31, 0
	s_add_i32 m0, s2, 0x4000
	s_nop 0
	global_load_lds_dwordx4 v139, s[40:41]
	s_nop 0
	s_add_i32 m0, s2, 0x6000
	s_nop 0
	global_load_lds_dwordx4 v141, s[40:41]
	s_waitcnt vmcnt(8) lgkmcnt(0)
	s_barrier
	v_mfma_f32_16x16x32_bf16 v[56:59], v[12:15], v[20:23], v[64:67]
	v_mfma_f32_16x16x32_bf16 v[116:119], v[16:19], v[28:31], v[56:59]
	v_mfma_f32_16x16x32_bf16 v[56:59], v[24:27], v[20:23], v[68:71]
	v_mfma_f32_16x16x32_bf16 v[112:115], v[196:199], v[28:31], v[56:59]
	v_mfma_f32_16x16x32_bf16 v[56:59], v[12:15], v[216:219], v[72:75]
	v_mfma_f32_16x16x32_bf16 v[108:111], v[16:19], v[220:223], v[56:59]
	v_mfma_f32_16x16x32_bf16 v[56:59], v[24:27], v[216:219], v[76:79]
	v_mfma_f32_16x16x32_bf16 v[100:103], v[196:199], v[220:223], v[56:59]
	v_mfma_f32_16x16x32_bf16 v[56:59], v[12:15], v[224:227], v[80:83]
	v_mfma_f32_16x16x32_bf16 v[92:95], v[16:19], v[228:231], v[56:59]
	v_mfma_f32_16x16x32_bf16 v[56:59], v[24:27], v[224:227], v[84:87]
	v_mfma_f32_16x16x32_bf16 v[84:87], v[196:199], v[228:231], v[56:59]
	v_mfma_f32_16x16x32_bf16 v[56:59], v[12:15], v[232:235], v[88:91]
	v_mfma_f32_16x16x32_bf16 v[72:75], v[16:19], v[236:239], v[56:59]
	v_mfma_f32_16x16x32_bf16 v[56:59], v[24:27], v[232:235], v[96:99]
	v_mfma_f32_16x16x32_bf16 v[56:59], v[196:199], v[236:239], v[56:59]
	v_mfma_f32_16x16x32_bf16 v[64:67], v[200:203], v[20:23], v[104:107]
	v_mfma_f32_16x16x32_bf16 v[20:23], v[208:211], v[20:23], v[32:35]
	v_mfma_f32_16x16x32_bf16 v[120:123], v[212:215], v[28:31], v[20:23]
	v_mfma_f32_16x16x32_bf16 v[20:23], v[200:203], v[216:219], v[36:39]
	v_mfma_f32_16x16x32_bf16 v[104:107], v[204:207], v[220:223], v[20:23]
	v_mfma_f32_16x16x32_bf16 v[20:23], v[208:211], v[216:219], v[40:43]
	v_mfma_f32_16x16x32_bf16 v[96:99], v[212:215], v[220:223], v[20:23]
	v_mfma_f32_16x16x32_bf16 v[20:23], v[200:203], v[224:227], v[44:47]
	v_mfma_f32_16x16x32_bf16 v[88:91], v[204:207], v[228:231], v[20:23]
	v_mfma_f32_16x16x32_bf16 v[20:23], v[208:211], v[224:227], v[48:51]
	v_mfma_f32_16x16x32_bf16 v[80:83], v[212:215], v[228:231], v[20:23]
	v_mfma_f32_16x16x32_bf16 v[20:23], v[200:203], v[232:235], v[52:55]
	v_mfma_f32_16x16x32_bf16 v[124:127], v[204:207], v[28:31], v[64:67]
	v_mfma_f32_16x16x32_bf16 v[64:67], v[204:207], v[236:239], v[20:23]
	v_mfma_f32_16x16x32_bf16 v[20:23], v[208:211], v[232:235], v[60:63]
	v_mfma_f32_16x16x32_bf16 v[48:51], v[212:215], v[236:239], v[20:23]
	s_barrier
	ds_read_b128 v[32:35], v145 offset:49152
	ds_read_b128 v[40:43], v145 offset:50176
	ds_read_b128 v[216:219], v145 offset:51200
	ds_read_b128 v[220:223], v145 offset:52224
	ds_read_b128 v[224:227], v145 offset:53248
	ds_read_b128 v[228:231], v145 offset:54272
	ds_read_b128 v[232:235], v145 offset:55296
	ds_read_b128 v[236:239], v145 offset:56320
	s_add_i32 m0, s2, 0x18000
	s_nop 0
	global_load_lds_dwordx4 v140, s[38:39]
	s_nop 0
	s_add_i32 m0, s2, 0x1a000
	s_nop 0
	global_load_lds_dwordx4 v142, s[38:39]
	s_add_u32 s38, s34, 0x80180
	s_addc_u32 s39, s35, 0
	s_add_i32 m0, s2, 0x1c000
	s_nop 0
	global_load_lds_dwordx4 v140, s[38:39]
	s_nop 0
	s_add_i32 m0, s2, 0x1e000
	s_nop 0
	global_load_lds_dwordx4 v142, s[38:39]
	s_nop 0
	s_add_i32 m0, s2, 0x8000
	s_nop 0
	global_load_lds_dwordx4 v139, s[36:37]
	s_nop 0
	s_add_i32 m0, s2, 0xa000
	s_nop 0
	global_load_lds_dwordx4 v141, s[36:37]
	s_waitcnt vmcnt(8) lgkmcnt(0)
	s_barrier
	v_mfma_f32_16x16x32_bf16 v[20:23], v[12:15], v[32:35], v[132:135]
	v_mfma_f32_16x16x32_bf16 v[76:79], v[16:19], v[40:43], v[20:23]
	v_mfma_f32_16x16x32_bf16 v[20:23], v[24:27], v[32:35], v[148:151]
	v_mfma_f32_16x16x32_bf16 v[60:63], v[196:199], v[40:43], v[20:23]
	v_mfma_f32_16x16x32_bf16 v[20:23], v[12:15], v[216:219], v[152:155]
	v_mfma_f32_16x16x32_bf16 v[44:47], v[16:19], v[220:223], v[20:23]
	v_mfma_f32_16x16x32_bf16 v[20:23], v[24:27], v[216:219], v[156:159]
	v_mfma_f32_16x16x32_bf16 v[36:39], v[196:199], v[220:223], v[20:23]
	v_mfma_f32_16x16x32_bf16 v[20:23], v[12:15], v[224:227], v[160:163]
	v_mfma_f32_16x16x32_bf16 v[0:3], v[12:15], v[232:235], v[0:3]
	v_mfma_f32_16x16x32_bf16 v[28:31], v[16:19], v[228:231], v[20:23]
	v_mfma_f32_16x16x32_bf16 v[20:23], v[24:27], v[224:227], v[164:167]
	v_mfma_f32_16x16x32_bf16 v[12:15], v[16:19], v[236:239], v[0:3]
	v_mfma_f32_16x16x32_bf16 v[0:3], v[24:27], v[232:235], v[4:7]
	v_mfma_f32_16x16x32_bf16 v[20:23], v[196:199], v[228:231], v[20:23]
	v_mfma_f32_16x16x32_bf16 v[4:7], v[196:199], v[236:239], v[0:3]
	v_mfma_f32_16x16x32_bf16 v[0:3], v[200:203], v[32:35], v[8:11]
	v_mfma_f32_16x16x32_bf16 v[68:71], v[204:207], v[40:43], v[0:3]
	v_mfma_f32_16x16x32_bf16 v[0:3], v[208:211], v[32:35], v[168:171]
	v_mfma_f32_16x16x32_bf16 v[52:55], v[212:215], v[40:43], v[0:3]
	v_mfma_f32_16x16x32_bf16 v[0:3], v[200:203], v[216:219], v[172:175]
	v_mfma_f32_16x16x32_bf16 v[40:43], v[204:207], v[220:223], v[0:3]
	v_mfma_f32_16x16x32_bf16 v[0:3], v[208:211], v[216:219], v[176:179]
	v_mfma_f32_16x16x32_bf16 v[32:35], v[212:215], v[220:223], v[0:3]
	v_mfma_f32_16x16x32_bf16 v[0:3], v[200:203], v[224:227], v[180:183]
	v_mfma_f32_16x16x32_bf16 v[24:27], v[204:207], v[228:231], v[0:3]
	v_mfma_f32_16x16x32_bf16 v[0:3], v[208:211], v[224:227], v[184:187]
	v_mfma_f32_16x16x32_bf16 v[16:19], v[212:215], v[228:231], v[0:3]
	v_mfma_f32_16x16x32_bf16 v[0:3], v[200:203], v[232:235], v[188:191]
	v_mfma_f32_16x16x32_bf16 v[8:11], v[204:207], v[236:239], v[0:3]
	v_mfma_f32_16x16x32_bf16 v[0:3], v[208:211], v[232:235], v[192:195]
	v_mfma_f32_16x16x32_bf16 v[0:3], v[212:215], v[236:239], v[0:3]
	s_barrier
	s_add_u32 s53, s30, 0x200
	s_addc_u32 s54, s31, 0
	s_add_u32 s55, s34, 0x200
	s_addc_u32 s56, s35, 0
	s_add_u32 s30, s30, 0x80180
	s_addc_u32 s31, s31, 0
	s_mov_b32 s57, 0
.LBB0_1109:
	ds_read_b128 v[132:135], v143
	ds_read_b128 v[148:151], v143 offset:1024
	ds_read_b128 v[152:155], v143 offset:2048
	ds_read_b128 v[156:159], v143 offset:3072
	ds_read_b128 v[160:163], v144
	ds_read_b128 v[164:167], v144 offset:1024
	ds_read_b128 v[168:171], v144 offset:2048
	ds_read_b128 v[172:175], v144 offset:3072
	ds_read_b128 v[176:179], v145
	ds_read_b128 v[180:183], v145 offset:1024
	ds_read_b128 v[184:187], v145 offset:2048
	ds_read_b128 v[188:191], v145 offset:3072
	ds_read_b128 v[192:195], v145 offset:4096
	ds_read_b128 v[196:199], v145 offset:5120
	ds_read_b128 v[200:203], v145 offset:6144
	ds_read_b128 v[204:207], v145 offset:7168
	s_cmp_eq_u32 s57, 28
	s_cselect_b32 s40, s51, s53
	s_cselect_b32 s41, s23, s54
	s_cselect_b32 s36, s52, s55
	s_cselect_b32 s37, s21, s56
	s_add_u32 s34, s40, 0x80
	s_addc_u32 s35, s41, 0
	s_add_u32 s38, s36, 0x80
	s_addc_u32 s39, s37, 0
	s_add_i32 m0, s2, 0xc000
	s_nop 0
	global_load_lds_dwordx4 v139, s[30:31]
	s_nop 0
	s_add_i32 m0, s2, 0xe000
	s_nop 0
	global_load_lds_dwordx4 v141, s[30:31]
	s_waitcnt vmcnt(8) lgkmcnt(0)
	s_barrier
	v_mfma_f32_16x16x32_bf16 v[116:119], v[132:135], v[176:179], v[116:119]
	v_mfma_f32_16x16x32_bf16 v[112:115], v[152:155], v[176:179], v[112:115]
	v_mfma_f32_16x16x32_bf16 v[100:103], v[152:155], v[184:187], v[100:103]
	v_mfma_f32_16x16x32_bf16 v[108:111], v[132:135], v[184:187], v[108:111]
	v_mfma_f32_16x16x32_bf16 v[92:95], v[132:135], v[192:195], v[92:95]
	v_mfma_f32_16x16x32_bf16 v[84:87], v[152:155], v[192:195], v[84:87]
	v_mfma_f32_16x16x32_bf16 v[56:59], v[152:155], v[200:203], v[56:59]
	v_mfma_f32_16x16x32_bf16 v[72:75], v[132:135], v[200:203], v[72:75]
	v_mfma_f32_16x16x32_bf16 v[116:119], v[148:151], v[180:183], v[116:119]
	v_mfma_f32_16x16x32_bf16 v[112:115], v[156:159], v[180:183], v[112:115]
	v_mfma_f32_16x16x32_bf16 v[100:103], v[156:159], v[188:191], v[100:103]
	v_mfma_f32_16x16x32_bf16 v[108:111], v[148:151], v[188:191], v[108:111]
	v_mfma_f32_16x16x32_bf16 v[92:95], v[148:151], v[196:199], v[92:95]
	v_mfma_f32_16x16x32_bf16 v[84:87], v[156:159], v[196:199], v[84:87]
	v_mfma_f32_16x16x32_bf16 v[56:59], v[156:159], v[204:207], v[56:59]
	v_mfma_f32_16x16x32_bf16 v[72:75], v[148:151], v[204:207], v[72:75]
	v_mfma_f32_16x16x32_bf16 v[124:127], v[160:163], v[176:179], v[124:127]
	v_mfma_f32_16x16x32_bf16 v[120:123], v[168:171], v[176:179], v[120:123]
	v_mfma_f32_16x16x32_bf16 v[96:99], v[168:171], v[184:187], v[96:99]
	v_mfma_f32_16x16x32_bf16 v[104:107], v[160:163], v[184:187], v[104:107]
	v_mfma_f32_16x16x32_bf16 v[88:91], v[160:163], v[192:195], v[88:91]
	v_mfma_f32_16x16x32_bf16 v[80:83], v[168:171], v[192:195], v[80:83]
	v_mfma_f32_16x16x32_bf16 v[48:51], v[168:171], v[200:203], v[48:51]
	v_mfma_f32_16x16x32_bf16 v[64:67], v[160:163], v[200:203], v[64:67]
	v_mfma_f32_16x16x32_bf16 v[124:127], v[164:167], v[180:183], v[124:127]
	v_mfma_f32_16x16x32_bf16 v[120:123], v[172:175], v[180:183], v[120:123]
	v_mfma_f32_16x16x32_bf16 v[96:99], v[172:175], v[188:191], v[96:99]
	v_mfma_f32_16x16x32_bf16 v[104:107], v[164:167], v[188:191], v[104:107]
	v_mfma_f32_16x16x32_bf16 v[88:91], v[164:167], v[196:199], v[88:91]
	v_mfma_f32_16x16x32_bf16 v[80:83], v[172:175], v[196:199], v[80:83]
	v_mfma_f32_16x16x32_bf16 v[48:51], v[172:175], v[204:207], v[48:51]
	v_mfma_f32_16x16x32_bf16 v[64:67], v[164:167], v[204:207], v[64:67]
	s_barrier
	ds_read_b128 v[176:179], v145 offset:16384
	ds_read_b128 v[180:183], v145 offset:17408
	ds_read_b128 v[184:187], v145 offset:18432
	ds_read_b128 v[188:191], v145 offset:19456
	ds_read_b128 v[192:195], v145 offset:20480
	ds_read_b128 v[196:199], v145 offset:21504
	ds_read_b128 v[200:203], v145 offset:22528
	ds_read_b128 v[204:207], v145 offset:23552
	s_add_i32 m0, s2, 0x10000
	s_nop 0
	global_load_lds_dwordx4 v140, s[36:37]
	s_nop 0
	s_add_i32 m0, s2, 0x12000
	s_nop 0
	global_load_lds_dwordx4 v142, s[36:37]
	s_add_u32 s58, s36, 0x80000
	s_addc_u32 s59, s37, 0
	s_add_i32 m0, s2, 0x14000
	s_nop 0
	global_load_lds_dwordx4 v140, s[58:59]
	s_nop 0
	s_add_i32 m0, s2, 0x16000
	s_nop 0
	global_load_lds_dwordx4 v142, s[58:59]
	s_nop 0
	s_add_i32 m0, s2, 0
	s_nop 0
	global_load_lds_dwordx4 v139, s[40:41]
	s_nop 0
	s_add_i32 m0, s2, 0x2000
	s_nop 0
	global_load_lds_dwordx4 v141, s[40:41]
	s_waitcnt vmcnt(8) lgkmcnt(0)
	s_barrier
	v_mfma_f32_16x16x32_bf16 v[76:79], v[132:135], v[176:179], v[76:79]
	v_mfma_f32_16x16x32_bf16 v[60:63], v[152:155], v[176:179], v[60:63]
	v_mfma_f32_16x16x32_bf16 v[36:39], v[152:155], v[184:187], v[36:39]
	v_mfma_f32_16x16x32_bf16 v[44:47], v[132:135], v[184:187], v[44:47]
	v_mfma_f32_16x16x32_bf16 v[28:31], v[132:135], v[192:195], v[28:31]
	v_mfma_f32_16x16x32_bf16 v[20:23], v[152:155], v[192:195], v[20:23]
	v_mfma_f32_16x16x32_bf16 v[4:7], v[152:155], v[200:203], v[4:7]
	v_mfma_f32_16x16x32_bf16 v[12:15], v[132:135], v[200:203], v[12:15]
	v_mfma_f32_16x16x32_bf16 v[76:79], v[148:151], v[180:183], v[76:79]
	v_mfma_f32_16x16x32_bf16 v[60:63], v[156:159], v[180:183], v[60:63]
	v_mfma_f32_16x16x32_bf16 v[36:39], v[156:159], v[188:191], v[36:39]
	v_mfma_f32_16x16x32_bf16 v[44:47], v[148:151], v[188:191], v[44:47]
	v_mfma_f32_16x16x32_bf16 v[28:31], v[148:151], v[196:199], v[28:31]
	v_mfma_f32_16x16x32_bf16 v[20:23], v[156:159], v[196:199], v[20:23]
	v_mfma_f32_16x16x32_bf16 v[4:7], v[156:159], v[204:207], v[4:7]
	v_mfma_f32_16x16x32_bf16 v[12:15], v[148:151], v[204:207], v[12:15]
	v_mfma_f32_16x16x32_bf16 v[68:71], v[160:163], v[176:179], v[68:71]
	v_mfma_f32_16x16x32_bf16 v[52:55], v[168:171], v[176:179], v[52:55]
	v_mfma_f32_16x16x32_bf16 v[32:35], v[168:171], v[184:187], v[32:35]
	v_mfma_f32_16x16x32_bf16 v[40:43], v[160:163], v[184:187], v[40:43]
	v_mfma_f32_16x16x32_bf16 v[24:27], v[160:163], v[192:195], v[24:27]
	v_mfma_f32_16x16x32_bf16 v[16:19], v[168:171], v[192:195], v[16:19]
	v_mfma_f32_16x16x32_bf16 v[0:3], v[168:171], v[200:203], v[0:3]
	v_mfma_f32_16x16x32_bf16 v[8:11], v[160:163], v[200:203], v[8:11]
	v_mfma_f32_16x16x32_bf16 v[68:71], v[164:167], v[180:183], v[68:71]
	v_mfma_f32_16x16x32_bf16 v[52:55], v[172:175], v[180:183], v[52:55]
	v_mfma_f32_16x16x32_bf16 v[32:35], v[172:175], v[188:191], v[32:35]
	v_mfma_f32_16x16x32_bf16 v[40:43], v[164:167], v[188:191], v[40:43]
	v_mfma_f32_16x16x32_bf16 v[24:27], v[164:167], v[196:199], v[24:27]
	v_mfma_f32_16x16x32_bf16 v[16:19], v[172:175], v[196:199], v[16:19]
	v_mfma_f32_16x16x32_bf16 v[0:3], v[172:175], v[204:207], v[0:3]
	v_mfma_f32_16x16x32_bf16 v[8:11], v[164:167], v[204:207], v[8:11]
	s_barrier
	ds_read_b128 v[132:135], v146
	ds_read_b128 v[148:151], v146 offset:1024
	ds_read_b128 v[152:155], v146 offset:2048
	ds_read_b128 v[156:159], v146 offset:3072
	ds_read_b128 v[160:163], v147
	ds_read_b128 v[164:167], v147 offset:1024
	ds_read_b128 v[168:171], v147 offset:2048
	ds_read_b128 v[172:175], v147 offset:3072
	ds_read_b128 v[176:179], v145 offset:32768
	ds_read_b128 v[180:183], v145 offset:33792
	ds_read_b128 v[184:187], v145 offset:34816
	ds_read_b128 v[188:191], v145 offset:35840
	ds_read_b128 v[192:195], v145 offset:36864
	ds_read_b128 v[196:199], v145 offset:37888
	ds_read_b128 v[200:203], v145 offset:38912
	ds_read_b128 v[204:207], v145 offset:39936
	s_add_u32 s40, s40, 0x80000
	s_addc_u32 s41, s41, 0
	s_add_i32 m0, s2, 0x4000
	s_nop 0
	global_load_lds_dwordx4 v139, s[40:41]
	s_nop 0
	s_add_i32 m0, s2, 0x6000
	s_nop 0
	global_load_lds_dwordx4 v141, s[40:41]
	s_waitcnt vmcnt(8) lgkmcnt(0)
	s_barrier
	v_mfma_f32_16x16x32_bf16 v[116:119], v[132:135], v[176:179], v[116:119]
	v_mfma_f32_16x16x32_bf16 v[112:115], v[152:155], v[176:179], v[112:115]
	v_mfma_f32_16x16x32_bf16 v[100:103], v[152:155], v[184:187], v[100:103]
	v_mfma_f32_16x16x32_bf16 v[108:111], v[132:135], v[184:187], v[108:111]
	v_mfma_f32_16x16x32_bf16 v[92:95], v[132:135], v[192:195], v[92:95]
	v_mfma_f32_16x16x32_bf16 v[84:87], v[152:155], v[192:195], v[84:87]
	v_mfma_f32_16x16x32_bf16 v[56:59], v[152:155], v[200:203], v[56:59]
	v_mfma_f32_16x16x32_bf16 v[72:75], v[132:135], v[200:203], v[72:75]
	v_mfma_f32_16x16x32_bf16 v[116:119], v[148:151], v[180:183], v[116:119]
	v_mfma_f32_16x16x32_bf16 v[112:115], v[156:159], v[180:183], v[112:115]
	v_mfma_f32_16x16x32_bf16 v[100:103], v[156:159], v[188:191], v[100:103]
	v_mfma_f32_16x16x32_bf16 v[108:111], v[148:151], v[188:191], v[108:111]
	v_mfma_f32_16x16x32_bf16 v[92:95], v[148:151], v[196:199], v[92:95]
	v_mfma_f32_16x16x32_bf16 v[84:87], v[156:159], v[196:199], v[84:87]
	v_mfma_f32_16x16x32_bf16 v[56:59], v[156:159], v[204:207], v[56:59]
	v_mfma_f32_16x16x32_bf16 v[72:75], v[148:151], v[204:207], v[72:75]
	v_mfma_f32_16x16x32_bf16 v[124:127], v[160:163], v[176:179], v[124:127]
	v_mfma_f32_16x16x32_bf16 v[120:123], v[168:171], v[176:179], v[120:123]
	v_mfma_f32_16x16x32_bf16 v[96:99], v[168:171], v[184:187], v[96:99]
	v_mfma_f32_16x16x32_bf16 v[104:107], v[160:163], v[184:187], v[104:107]
	v_mfma_f32_16x16x32_bf16 v[88:91], v[160:163], v[192:195], v[88:91]
	v_mfma_f32_16x16x32_bf16 v[80:83], v[168:171], v[192:195], v[80:83]
	v_mfma_f32_16x16x32_bf16 v[48:51], v[168:171], v[200:203], v[48:51]
	v_mfma_f32_16x16x32_bf16 v[64:67], v[160:163], v[200:203], v[64:67]
	v_mfma_f32_16x16x32_bf16 v[124:127], v[164:167], v[180:183], v[124:127]
	v_mfma_f32_16x16x32_bf16 v[120:123], v[172:175], v[180:183], v[120:123]
	v_mfma_f32_16x16x32_bf16 v[96:99], v[172:175], v[188:191], v[96:99]
	v_mfma_f32_16x16x32_bf16 v[104:107], v[164:167], v[188:191], v[104:107]
	v_mfma_f32_16x16x32_bf16 v[88:91], v[164:167], v[196:199], v[88:91]
	v_mfma_f32_16x16x32_bf16 v[80:83], v[172:175], v[196:199], v[80:83]
	v_mfma_f32_16x16x32_bf16 v[48:51], v[172:175], v[204:207], v[48:51]
	v_mfma_f32_16x16x32_bf16 v[64:67], v[164:167], v[204:207], v[64:67]
	s_barrier
	ds_read_b128 v[176:179], v145 offset:49152
	ds_read_b128 v[180:183], v145 offset:50176
	ds_read_b128 v[184:187], v145 offset:51200
	ds_read_b128 v[188:191], v145 offset:52224
	ds_read_b128 v[192:195], v145 offset:53248
	ds_read_b128 v[196:199], v145 offset:54272
	ds_read_b128 v[200:203], v145 offset:55296
	ds_read_b128 v[204:207], v145 offset:56320
	s_add_i32 m0, s2, 0x18000
	s_nop 0
	global_load_lds_dwordx4 v140, s[38:39]
	s_nop 0
	s_add_i32 m0, s2, 0x1a000
	s_nop 0
	global_load_lds_dwordx4 v142, s[38:39]
	s_add_u32 s36, s36, 0x80080
	s_addc_u32 s37, s37, 0
	s_add_i32 m0, s2, 0x1c000
	s_nop 0
	global_load_lds_dwordx4 v140, s[36:37]
	s_nop 0
	s_add_i32 m0, s2, 0x1e000
	s_nop 0
	global_load_lds_dwordx4 v142, s[36:37]
	s_nop 0
	s_add_i32 m0, s2, 0x8000
	s_nop 0
	global_load_lds_dwordx4 v139, s[34:35]
	s_nop 0
	s_add_i32 m0, s2, 0xa000
	s_nop 0
	global_load_lds_dwordx4 v141, s[34:35]
	s_waitcnt vmcnt(8) lgkmcnt(0)
	s_barrier
	v_mfma_f32_16x16x32_bf16 v[76:79], v[132:135], v[176:179], v[76:79]
	v_mfma_f32_16x16x32_bf16 v[60:63], v[152:155], v[176:179], v[60:63]
	v_mfma_f32_16x16x32_bf16 v[36:39], v[152:155], v[184:187], v[36:39]
	v_mfma_f32_16x16x32_bf16 v[44:47], v[132:135], v[184:187], v[44:47]
	v_mfma_f32_16x16x32_bf16 v[28:31], v[132:135], v[192:195], v[28:31]
	v_mfma_f32_16x16x32_bf16 v[20:23], v[152:155], v[192:195], v[20:23]
	v_mfma_f32_16x16x32_bf16 v[4:7], v[152:155], v[200:203], v[4:7]
	v_mfma_f32_16x16x32_bf16 v[12:15], v[132:135], v[200:203], v[12:15]
	v_mfma_f32_16x16x32_bf16 v[76:79], v[148:151], v[180:183], v[76:79]
	v_mfma_f32_16x16x32_bf16 v[60:63], v[156:159], v[180:183], v[60:63]
	v_mfma_f32_16x16x32_bf16 v[36:39], v[156:159], v[188:191], v[36:39]
	v_mfma_f32_16x16x32_bf16 v[44:47], v[148:151], v[188:191], v[44:47]
	v_mfma_f32_16x16x32_bf16 v[28:31], v[148:151], v[196:199], v[28:31]
	v_mfma_f32_16x16x32_bf16 v[20:23], v[156:159], v[196:199], v[20:23]
	v_mfma_f32_16x16x32_bf16 v[4:7], v[156:159], v[204:207], v[4:7]
	v_mfma_f32_16x16x32_bf16 v[12:15], v[148:151], v[204:207], v[12:15]
	v_mfma_f32_16x16x32_bf16 v[68:71], v[160:163], v[176:179], v[68:71]
	v_mfma_f32_16x16x32_bf16 v[52:55], v[168:171], v[176:179], v[52:55]
	v_mfma_f32_16x16x32_bf16 v[32:35], v[168:171], v[184:187], v[32:35]
	v_mfma_f32_16x16x32_bf16 v[40:43], v[160:163], v[184:187], v[40:43]
	v_mfma_f32_16x16x32_bf16 v[24:27], v[160:163], v[192:195], v[24:27]
	v_mfma_f32_16x16x32_bf16 v[16:19], v[168:171], v[192:195], v[16:19]
	v_mfma_f32_16x16x32_bf16 v[0:3], v[168:171], v[200:203], v[0:3]
	v_mfma_f32_16x16x32_bf16 v[8:11], v[160:163], v[200:203], v[8:11]
	v_mfma_f32_16x16x32_bf16 v[68:71], v[164:167], v[180:183], v[68:71]
	v_mfma_f32_16x16x32_bf16 v[52:55], v[172:175], v[180:183], v[52:55]
	v_mfma_f32_16x16x32_bf16 v[32:35], v[172:175], v[188:191], v[32:35]
	v_mfma_f32_16x16x32_bf16 v[40:43], v[164:167], v[188:191], v[40:43]
	v_mfma_f32_16x16x32_bf16 v[24:27], v[164:167], v[196:199], v[24:27]
	v_mfma_f32_16x16x32_bf16 v[16:19], v[172:175], v[196:199], v[16:19]
	v_mfma_f32_16x16x32_bf16 v[0:3], v[172:175], v[204:207], v[0:3]
	v_mfma_f32_16x16x32_bf16 v[8:11], v[164:167], v[204:207], v[8:11]
	s_barrier
	s_add_i32 s57, s57, 2
	s_add_u32 s53, s53, 0x100
	s_addc_u32 s54, s54, 0
	s_add_u32 s55, s55, 0x100
	s_addc_u32 s56, s56, 0
	s_add_u32 s30, s30, 0x100
	s_addc_u32 s31, s31, 0
	s_cmp_gt_u32 s57, 29
	s_cbranch_scc0 .LBB0_1109
	s_and_b64 vcc, exec, s[10:11]
	s_cbranch_vccz .LBB0_1112
	s_barrier

.LBB0_1116:
	s_cmp_lt_u32 s93, 10
	s_cbranch_scc1 .LBB0_1170
	s_waitcnt vmcnt(0) lgkmcnt(0)
	s_barrier
	s_and_saveexec_b64 s[4:5], s[72:73]
	s_cbranch_execz .LBB0_1169
	s_add_u32 s6, s70, 0x4200
	s_addc_u32 s7, s71, 0
	s_add_i32 s2, 0, 0x23f20
	v_mov_b32_e32 v0, s2
	s_waitcnt vmcnt(0) expcnt(0) lgkmcnt(0)
	ds_read_b32 v2, v0
	s_add_i32 s2, 0, 0x23f24
	v_mov_b32_e32 v0, s2
	ds_read_b32 v0, v0
	s_waitcnt lgkmcnt(1)
	v_cmp_ne_u32_e32 vcc, 0, v2
	s_cbranch_vccnz .LBB0_1133
	s_add_u32 s8, s70, 0x4400
	s_addc_u32 s9, s71, 0
	s_add_u32 s10, s70, 0x4500
	s_addc_u32 s11, s71, 0
	s_add_u32 s12, s70, 0x4600
	s_addc_u32 s13, s71, 0
	s_add_u32 s14, s70, 0x4700
	s_addc_u32 s15, s71, 0
	s_add_u32 s16, s70, 0x4800
	s_addc_u32 s17, s71, 0
	s_add_u32 s18, s70, 0x4900
	s_addc_u32 s19, s71, 0
	s_add_u32 s20, s70, 0x4a00
	s_addc_u32 s21, s71, 0
	s_add_u32 s22, s70, 0x4b00
	s_addc_u32 s23, s71, 0
	s_add_u32 s24, s70, 0x4c00
	s_addc_u32 s25, s71, 0
	s_add_u32 s26, s70, 0x4d00
	s_addc_u32 s27, s71, 0
	s_add_u32 s28, s70, 0x4e00
	s_addc_u32 s29, s71, 0
	s_add_u32 s30, s70, 0x4f00
	s_addc_u32 s31, s71, 0
	s_add_u32 s34, s70, 0x5000
	s_addc_u32 s35, s71, 0
	s_load_dwordx2 s[42:43], s[90:91], 0x4
	s_add_u32 s36, s70, 0x5100
	s_addc_u32 s37, s71, 0
	s_add_u32 s38, s70, 0x5200
	s_addc_u32 s39, s71, 0
	s_add_u32 s40, s70, 0x5300
	s_waitcnt lgkmcnt(0)
	s_mul_i32 s2, s42, s33
	s_addc_u32 s41, s71, 0
	s_mul_i32 s2, s2, s43
	s_mov_b32 s48, 1
	v_mov_b32_e32 v16, 0
	s_branch .LBB0_1121

.LBB0_1256:
	s_cmp_lt_i32 s93, 11
	s_cbranch_scc1 .LBB0_1310
	s_waitcnt vmcnt(0) lgkmcnt(0)
	s_barrier
	s_and_saveexec_b64 s[4:5], s[72:73]
	s_cbranch_execz .LBB0_1309
	s_add_i32 s2, 0, 0x23f20
	s_waitcnt vmcnt(0)
	v_mov_b32_e32 v0, s2
	s_waitcnt vmcnt(0) expcnt(0) lgkmcnt(0)
	ds_read_b32 v2, v0
	s_add_i32 s2, 0, 0x23f24
	v_mov_b32_e32 v0, s2
	ds_read_b32 v0, v0
	s_waitcnt lgkmcnt(1)
	v_cmp_ne_u32_e32 vcc, 0, v2
	s_cbranch_vccnz .LBB0_1273
	s_load_dwordx2 s[10:11], s[90:91], 0x4
	s_add_u32 s6, s70, 0x4200
	s_addc_u32 s7, s71, 0
	s_add_u32 s8, s70, 0x4400
	s_addc_u32 s9, s71, 0
	s_waitcnt lgkmcnt(0)
	s_mul_i32 s2, s10, s33
	s_add_u32 s10, s70, 0x4500
	s_mul_i32 s2, s2, s11
	s_addc_u32 s11, s71, 0
	s_add_u32 s12, s70, 0x4600
	s_addc_u32 s13, s71, 0
	s_add_u32 s14, s70, 0x4700
	s_addc_u32 s15, s71, 0
	s_add_u32 s16, s70, 0x4800
	s_addc_u32 s17, s71, 0
	s_add_u32 s18, s70, 0x4900
	s_addc_u32 s19, s71, 0
	s_add_u32 s20, s70, 0x4a00
	s_addc_u32 s21, s71, 0
	s_add_u32 s22, s70, 0x4b00
	s_addc_u32 s23, s71, 0
	s_add_u32 s24, s70, 0x4c00
	s_addc_u32 s25, s71, 0
	s_add_u32 s26, s70, 0x4d00
	s_addc_u32 s27, s71, 0
	s_add_u32 s28, s70, 0x4e00
	s_addc_u32 s29, s71, 0
	s_add_u32 s30, s70, 0x4f00
	s_addc_u32 s31, s71, 0
	s_add_u32 s34, s70, 0x5000
	s_addc_u32 s35, s71, 0
	s_add_u32 s36, s70, 0x5100
	s_addc_u32 s37, s71, 0
	s_add_u32 s38, s70, 0x5200
	s_addc_u32 s39, s71, 0
	s_add_u32 s40, s70, 0x5300
	s_addc_u32 s41, s71, 0
	s_mov_b32 s48, 1
	v_mov_b32_e32 v16, 0
	s_branch .LBB0_1261

.LBB0_1343:
	s_or_b64 exec, exec, s[12:13]
	s_cmp_lt_u32 s93, 12
	s_cbranch_scc1 .LBB0_1397
	s_waitcnt vmcnt(0) lgkmcnt(0)
	s_barrier
	s_and_saveexec_b64 s[4:5], s[72:73]
	s_cbranch_execz .LBB0_1396
	s_add_u32 s6, s70, 0x4200
	s_addc_u32 s7, s71, 0
	s_add_i32 s2, 0, 0x23f20
	v_mov_b32_e32 v0, s2
	s_waitcnt vmcnt(0) expcnt(0) lgkmcnt(0)
	ds_read_b32 v2, v0
	s_add_i32 s2, 0, 0x23f24
	v_mov_b32_e32 v0, s2
	ds_read_b32 v0, v0
	s_waitcnt lgkmcnt(1)
	v_cmp_ne_u32_e32 vcc, 0, v2
	s_cbranch_vccnz .LBB0_1360
	s_add_u32 s8, s70, 0x4400
	s_addc_u32 s9, s71, 0
	s_add_u32 s10, s70, 0x4500
	s_addc_u32 s11, s71, 0
	s_add_u32 s12, s70, 0x4600
	s_addc_u32 s13, s71, 0
	s_add_u32 s14, s70, 0x4700
	s_addc_u32 s15, s71, 0
	s_add_u32 s16, s70, 0x4800
	s_addc_u32 s17, s71, 0
	s_add_u32 s18, s70, 0x4900
	s_addc_u32 s19, s71, 0
	s_add_u32 s20, s70, 0x4a00
	s_addc_u32 s21, s71, 0
	s_add_u32 s22, s70, 0x4b00
	s_addc_u32 s23, s71, 0
	s_add_u32 s24, s70, 0x4c00
	s_addc_u32 s25, s71, 0
	s_add_u32 s26, s70, 0x4d00
	s_addc_u32 s27, s71, 0
	s_add_u32 s28, s70, 0x4e00
	s_addc_u32 s29, s71, 0
	s_add_u32 s30, s70, 0x4f00
	s_addc_u32 s31, s71, 0
	s_add_u32 s34, s70, 0x5000
	s_addc_u32 s35, s71, 0
	s_load_dwordx2 s[42:43], s[90:91], 0x4
	s_add_u32 s36, s70, 0x5100
	s_addc_u32 s37, s71, 0
	s_add_u32 s38, s70, 0x5200
	s_addc_u32 s39, s71, 0
	s_add_u32 s40, s70, 0x5300
	s_waitcnt lgkmcnt(0)
	s_mul_i32 s2, s42, s33
	s_addc_u32 s41, s71, 0
	s_mul_i32 s2, s2, s43
	s_mov_b32 s48, 1
	v_mov_b32_e32 v16, 0
	s_branch .LBB0_1348

.LBB0_1410:
	ds_read_b128 v[0:3], v138
	ds_read_b128 v[4:7], v138 offset:1024
	ds_read_b128 v[8:11], v138 offset:2048
	ds_read_b128 v[12:15], v138 offset:3072
	ds_read_b128 v[16:19], v139
	ds_read_b128 v[20:23], v139 offset:1024
	ds_read_b128 v[24:27], v139 offset:2048
	ds_read_b128 v[28:31], v139 offset:3072
	ds_read_b128 v[32:35], v140
	ds_read_b128 v[36:39], v140 offset:1024
	ds_read_b128 v[40:43], v140 offset:2048
	ds_read_b128 v[44:47], v140 offset:3072
	ds_read_b128 v[48:51], v140 offset:4096
	ds_read_b128 v[52:55], v140 offset:5120
	ds_read_b128 v[56:59], v140 offset:6144
	ds_read_b128 v[60:63], v140 offset:7168
	s_lshl_b64 s[20:21], s[16:17], 19
	s_add_u32 s20, s39, s20
	s_addc_u32 s21, s40, s21
	s_and_b64 s[6:7], exec, s[6:7]
	s_cselect_b32 s2, s21, s29
	s_cselect_b32 s15, s20, s28
	s_add_u32 s6, s28, 0x100
	s_addc_u32 s7, s29, 0
	s_add_u32 s36, s26, 0x100
	s_addc_u32 s37, s27, 0
	s_add_u32 s30, s28, 0x180
	s_addc_u32 s31, s29, 0
	s_add_u32 s34, s26, 0x180
	s_addc_u32 s35, s27, 0
	s_add_u32 s54, s28, 0x40080
	s_addc_u32 s55, s29, 0
	s_add_i32 m0, s47, 0xc000
	s_nop 0
	global_load_lds_dwordx4 v134, s[54:55]
	s_nop 0
	s_add_i32 m0, s47, 0xe000
	s_nop 0
	global_load_lds_dwordx4 v136, s[54:55]
	s_waitcnt vmcnt(8) lgkmcnt(0)
	s_barrier
	v_mfma_f32_16x16x128_f8f6f4 v[64:67], v[0:7], v[32:39], 0
	v_mfma_f32_16x16x128_f8f6f4 v[68:71], v[8:15], v[32:39], 0
	v_mfma_f32_16x16x128_f8f6f4 v[76:79], v[8:15], v[40:47], 0
	v_mfma_f32_16x16x128_f8f6f4 v[72:75], v[0:7], v[40:47], 0
	v_mfma_f32_16x16x128_f8f6f4 v[80:83], v[0:7], v[48:55], 0
	v_mfma_f32_16x16x128_f8f6f4 v[88:91], v[8:15], v[48:55], 0
	v_mfma_f32_16x16x128_f8f6f4 v[104:107], v[8:15], v[56:63], 0
	v_mfma_f32_16x16x128_f8f6f4 v[92:95], v[0:7], v[56:63], 0
	v_mfma_f32_16x16x128_f8f6f4 v[108:111], v[16:23], v[32:39], 0
	v_mfma_f32_16x16x128_f8f6f4 v[124:127], v[24:31], v[32:39], 0
	v_mfma_f32_16x16x128_f8f6f4 v[166:169], v[24:31], v[40:47], 0
	v_mfma_f32_16x16x128_f8f6f4 v[162:165], v[16:23], v[40:47], 0
	v_mfma_f32_16x16x128_f8f6f4 v[170:173], v[16:23], v[48:55], 0
	v_mfma_f32_16x16x128_f8f6f4 v[174:177], v[24:31], v[48:55], 0
	v_mfma_f32_16x16x128_f8f6f4 v[182:185], v[24:31], v[56:63], 0
	v_mfma_f32_16x16x128_f8f6f4 v[178:181], v[16:23], v[56:63], 0
	s_barrier
	ds_read_b128 v[32:35], v140 offset:16384
	ds_read_b128 v[36:39], v140 offset:17408
	ds_read_b128 v[40:43], v140 offset:18432
	ds_read_b128 v[44:47], v140 offset:19456
	ds_read_b128 v[48:51], v140 offset:20480
	ds_read_b128 v[52:55], v140 offset:21504
	ds_read_b128 v[56:59], v140 offset:22528
	ds_read_b128 v[60:63], v140 offset:23552
	s_add_i32 m0, s47, 0x10000
	s_nop 0
	global_load_lds_dwordx4 v135, s[36:37]
	s_nop 0
	s_add_i32 m0, s47, 0x12000
	s_nop 0
	global_load_lds_dwordx4 v137, s[36:37]
	s_add_u32 s36, s26, 0x40100
	s_addc_u32 s37, s27, 0
	s_add_i32 m0, s47, 0x14000
	s_nop 0
	global_load_lds_dwordx4 v135, s[36:37]
	s_nop 0
	s_add_i32 m0, s47, 0x16000
	s_nop 0
	global_load_lds_dwordx4 v137, s[36:37]
	s_nop 0
	s_add_i32 m0, s47, 0
	s_nop 0
	global_load_lds_dwordx4 v134, s[6:7]
	s_nop 0
	s_add_i32 m0, s47, 0x2000
	s_nop 0
	global_load_lds_dwordx4 v136, s[6:7]
	s_waitcnt vmcnt(8) lgkmcnt(0)
	s_barrier
	v_mfma_f32_16x16x128_f8f6f4 v[186:189], v[0:7], v[32:39], 0
	v_mfma_f32_16x16x128_f8f6f4 v[190:193], v[8:15], v[32:39], 0
	v_mfma_f32_16x16x128_f8f6f4 v[198:201], v[8:15], v[40:47], 0
	v_mfma_f32_16x16x128_f8f6f4 v[194:197], v[0:7], v[40:47], 0
	v_mfma_f32_16x16x128_f8f6f4 v[202:205], v[0:7], v[48:55], 0
	v_mfma_f32_16x16x128_f8f6f4 v[206:209], v[8:15], v[48:55], 0
	v_mfma_f32_16x16x128_f8f6f4 v[214:217], v[8:15], v[56:63], 0
	v_mfma_f32_16x16x128_f8f6f4 v[210:213], v[0:7], v[56:63], 0
	v_mfma_f32_16x16x128_f8f6f4 v[218:221], v[16:23], v[32:39], 0
	v_mfma_f32_16x16x128_f8f6f4 v[222:225], v[24:31], v[32:39], 0
	v_mfma_f32_16x16x128_f8f6f4 v[230:233], v[24:31], v[40:47], 0
	v_mfma_f32_16x16x128_f8f6f4 v[226:229], v[16:23], v[40:47], 0
	v_mfma_f32_16x16x128_f8f6f4 v[234:237], v[16:23], v[48:55], 0
	v_mfma_f32_16x16x128_f8f6f4 v[238:241], v[24:31], v[48:55], 0
	v_mfma_f32_16x16x128_f8f6f4 v[246:249], v[24:31], v[56:63], 0
	v_mfma_f32_16x16x128_f8f6f4 v[242:245], v[16:23], v[56:63], 0
	s_barrier
	ds_read_b128 v[0:3], v141
	ds_read_b128 v[4:7], v141 offset:1024
	ds_read_b128 v[8:11], v141 offset:2048
	ds_read_b128 v[12:15], v141 offset:3072
	ds_read_b128 v[146:149], v142
	ds_read_b128 v[150:153], v142 offset:1024
	ds_read_b128 v[154:157], v142 offset:2048
	ds_read_b128 v[158:161], v142 offset:3072
	ds_read_b128 v[16:19], v140 offset:32768
	ds_read_b128 v[20:23], v140 offset:33792
	ds_read_b128 v[24:27], v140 offset:34816
	ds_read_b128 v[28:31], v140 offset:35840
	ds_read_b128 v[32:35], v140 offset:36864
	ds_read_b128 v[36:39], v140 offset:37888
	ds_read_b128 v[40:43], v140 offset:38912
	ds_read_b128 v[44:47], v140 offset:39936
	s_add_u32 s28, s28, 0x40100
	s_addc_u32 s29, s29, 0
	s_add_i32 m0, s47, 0x4000
	s_nop 0
	global_load_lds_dwordx4 v134, s[28:29]
	s_nop 0
	s_add_i32 m0, s47, 0x6000
	s_nop 0
	global_load_lds_dwordx4 v136, s[28:29]
	s_waitcnt vmcnt(8) lgkmcnt(0)
	s_barrier
	v_mfma_f32_16x16x128_f8f6f4 v[112:115], v[0:7], v[16:23], v[64:67]
	v_mfma_f32_16x16x128_f8f6f4 v[116:119], v[8:15], v[16:23], v[68:71]
	v_mfma_f32_16x16x128_f8f6f4 v[100:103], v[0:7], v[24:31], v[72:75]
	v_mfma_f32_16x16x128_f8f6f4 v[96:99], v[8:15], v[24:31], v[76:79]
	v_mfma_f32_16x16x128_f8f6f4 v[84:87], v[0:7], v[32:39], v[80:83]
	v_mfma_f32_16x16x128_f8f6f4 v[80:83], v[8:15], v[32:39], v[88:91]
	v_mfma_f32_16x16x128_f8f6f4 v[60:63], v[0:7], v[40:47], v[92:95]
	v_mfma_f32_16x16x128_f8f6f4 v[56:59], v[8:15], v[40:47], v[104:107]
	v_mfma_f32_16x16x128_f8f6f4 v[120:123], v[146:153], v[16:23], v[108:111]
	v_mfma_f32_16x16x128_f8f6f4 v[124:127], v[154:161], v[16:23], v[124:127]
	v_mfma_f32_16x16x128_f8f6f4 v[108:111], v[146:153], v[24:31], v[162:165]
	v_mfma_f32_16x16x128_f8f6f4 v[104:107], v[154:161], v[24:31], v[166:169]
	v_mfma_f32_16x16x128_f8f6f4 v[92:95], v[146:153], v[32:39], v[170:173]
	v_mfma_f32_16x16x128_f8f6f4 v[88:91], v[154:161], v[32:39], v[174:177]
	v_mfma_f32_16x16x128_f8f6f4 v[76:79], v[146:153], v[40:47], v[178:181]
	v_mfma_f32_16x16x128_f8f6f4 v[72:75], v[154:161], v[40:47], v[182:185]
	s_barrier
	ds_read_b128 v[24:27], v140 offset:49152
	ds_read_b128 v[28:31], v140 offset:50176
	ds_read_b128 v[162:165], v140 offset:51200
	ds_read_b128 v[166:169], v140 offset:52224
	ds_read_b128 v[170:173], v140 offset:53248
	ds_read_b128 v[174:177], v140 offset:54272
	ds_read_b128 v[178:181], v140 offset:55296
	ds_read_b128 v[182:185], v140 offset:56320
	s_add_i32 m0, s47, 0x18000
	s_nop 0
	global_load_lds_dwordx4 v135, s[34:35]
	s_nop 0
	s_add_i32 m0, s47, 0x1a000
	s_nop 0
	global_load_lds_dwordx4 v137, s[34:35]
	s_add_u32 s28, s26, 0x40180
	s_addc_u32 s29, s27, 0
	s_add_i32 m0, s47, 0x1c000
	s_nop 0
	global_load_lds_dwordx4 v135, s[28:29]
	s_nop 0
	s_add_i32 m0, s47, 0x1e000
	s_nop 0
	global_load_lds_dwordx4 v137, s[28:29]
	s_nop 0
	s_add_i32 m0, s47, 0x8000
	s_nop 0
	global_load_lds_dwordx4 v134, s[30:31]
	s_nop 0
	s_add_i32 m0, s47, 0xa000
	s_nop 0
	global_load_lds_dwordx4 v136, s[30:31]
	s_waitcnt vmcnt(8) lgkmcnt(0)
	s_barrier
	v_mfma_f32_16x16x128_f8f6f4 v[52:55], v[0:7], v[24:31], v[186:189]
	v_mfma_f32_16x16x128_f8f6f4 v[48:51], v[8:15], v[24:31], v[190:193]
	v_mfma_f32_16x16x128_f8f6f4 v[36:39], v[0:7], v[162:169], v[194:197]
	v_mfma_f32_16x16x128_f8f6f4 v[32:35], v[8:15], v[162:169], v[198:201]
	v_mfma_f32_16x16x128_f8f6f4 v[20:23], v[0:7], v[170:177], v[202:205]
	v_mfma_f32_16x16x128_f8f6f4 v[16:19], v[8:15], v[170:177], v[206:209]
	v_mfma_f32_16x16x128_f8f6f4 v[4:7], v[0:7], v[178:185], v[210:213]
	v_mfma_f32_16x16x128_f8f6f4 v[0:3], v[8:15], v[178:185], v[214:217]
	v_mfma_f32_16x16x128_f8f6f4 v[68:71], v[146:153], v[24:31], v[218:221]
	v_mfma_f32_16x16x128_f8f6f4 v[64:67], v[154:161], v[24:31], v[222:225]
	v_mfma_f32_16x16x128_f8f6f4 v[44:47], v[146:153], v[162:169], v[226:229]
	v_mfma_f32_16x16x128_f8f6f4 v[40:43], v[154:161], v[162:169], v[230:233]
	v_mfma_f32_16x16x128_f8f6f4 v[28:31], v[146:153], v[170:177], v[234:237]
	v_mfma_f32_16x16x128_f8f6f4 v[24:27], v[154:161], v[170:177], v[238:241]
	v_mfma_f32_16x16x128_f8f6f4 v[12:15], v[146:153], v[178:185], v[242:245]
	v_mfma_f32_16x16x128_f8f6f4 v[8:11], v[154:161], v[178:185], v[246:249]
	s_barrier
	s_add_u32 s17, s26, 0x200
	s_addc_u32 s54, s27, 0
	s_mov_b32 s55, 0
.LBB0_1411:
	ds_read_b128 v[146:149], v138
	ds_read_b128 v[150:153], v138 offset:1024
	ds_read_b128 v[154:157], v138 offset:2048
	ds_read_b128 v[158:161], v138 offset:3072
	ds_read_b128 v[162:165], v139
	ds_read_b128 v[166:169], v139 offset:1024
	ds_read_b128 v[170:173], v139 offset:2048
	ds_read_b128 v[174:177], v139 offset:3072
	ds_read_b128 v[178:181], v140
	ds_read_b128 v[182:185], v140 offset:1024
	ds_read_b128 v[186:189], v140 offset:2048
	ds_read_b128 v[190:193], v140 offset:3072
	ds_read_b128 v[194:197], v140 offset:4096
	ds_read_b128 v[198:201], v140 offset:5120
	ds_read_b128 v[202:205], v140 offset:6144
	ds_read_b128 v[206:209], v140 offset:7168
	s_add_u32 s26, s6, 0x100
	s_addc_u32 s27, s7, 0
	s_cmp_eq_u32 s55, 12
	s_cselect_b32 s36, s15, s26
	s_cselect_b32 s37, s2, s27
	s_cselect_b32 s30, s18, s17
	s_cselect_b32 s31, s19, s54
	s_add_u32 s28, s36, 0x80
	s_addc_u32 s29, s37, 0
	s_add_u32 s34, s30, 0x80
	s_addc_u32 s35, s31, 0
	s_add_u32 s6, s6, 0x40080
	s_addc_u32 s7, s7, 0
	s_add_i32 m0, s47, 0xc000
	s_nop 0
	global_load_lds_dwordx4 v134, s[6:7]
	s_nop 0
	s_add_i32 m0, s47, 0xe000
	s_nop 0
	global_load_lds_dwordx4 v136, s[6:7]
	s_waitcnt vmcnt(8) lgkmcnt(0)
	s_barrier
	v_mfma_f32_16x16x128_f8f6f4 v[112:115], v[146:153], v[178:185], v[112:115]
	v_mfma_f32_16x16x128_f8f6f4 v[116:119], v[154:161], v[178:185], v[116:119]
	v_mfma_f32_16x16x128_f8f6f4 v[96:99], v[154:161], v[186:193], v[96:99]
	v_mfma_f32_16x16x128_f8f6f4 v[100:103], v[146:153], v[186:193], v[100:103]
	v_mfma_f32_16x16x128_f8f6f4 v[210:213], v[146:153], v[194:201], v[84:87]
	v_mfma_f32_16x16x128_f8f6f4 v[214:217], v[154:161], v[194:201], v[80:83]
	v_mfma_f32_16x16x128_f8f6f4 v[222:225], v[154:161], v[202:209], v[56:59]
	v_mfma_f32_16x16x128_f8f6f4 v[218:221], v[146:153], v[202:209], v[60:63]
	v_mfma_f32_16x16x128_f8f6f4 v[120:123], v[162:169], v[178:185], v[120:123]
	v_mfma_f32_16x16x128_f8f6f4 v[124:127], v[170:177], v[178:185], v[124:127]
	v_mfma_f32_16x16x128_f8f6f4 v[108:111], v[162:169], v[186:193], v[108:111]
	v_mfma_f32_16x16x128_f8f6f4 v[104:107], v[170:177], v[186:193], v[104:107]
	v_mfma_f32_16x16x128_f8f6f4 v[178:181], v[162:169], v[194:201], v[92:95]
	v_mfma_f32_16x16x128_f8f6f4 v[182:185], v[170:177], v[194:201], v[88:91]
	v_mfma_f32_16x16x128_f8f6f4 v[186:189], v[162:169], v[202:209], v[76:79]
	v_mfma_f32_16x16x128_f8f6f4 v[190:193], v[170:177], v[202:209], v[72:75]
	s_barrier
	ds_read_b128 v[56:59], v140 offset:16384
	ds_read_b128 v[60:63], v140 offset:17408
	s_nop 2
	ds_read_b128 v[72:75], v140 offset:18432
	ds_read_b128 v[76:79], v140 offset:19456
	ds_read_b128 v[80:83], v140 offset:20480
	ds_read_b128 v[84:87], v140 offset:21504
	ds_read_b128 v[88:91], v140 offset:22528
	ds_read_b128 v[92:95], v140 offset:23552
	s_add_i32 m0, s47, 0x10000
	s_nop 0
	global_load_lds_dwordx4 v135, s[30:31]
	s_nop 0
	s_add_i32 m0, s47, 0x12000
	s_nop 0
	global_load_lds_dwordx4 v137, s[30:31]
	s_add_u32 s6, s30, 0x40000
	s_addc_u32 s7, s31, 0
	s_add_i32 m0, s47, 0x14000
	s_nop 0
	global_load_lds_dwordx4 v135, s[6:7]
	s_nop 0
	s_add_i32 m0, s47, 0x16000
	s_nop 0
	global_load_lds_dwordx4 v137, s[6:7]
	s_nop 0
	s_add_i32 m0, s47, 0
	s_nop 0
	global_load_lds_dwordx4 v134, s[36:37]
	s_nop 0
	s_add_i32 m0, s47, 0x2000
	s_nop 0
	global_load_lds_dwordx4 v136, s[36:37]
	s_waitcnt vmcnt(8) lgkmcnt(0)
	s_barrier
	v_mfma_f32_16x16x128_f8f6f4 v[52:55], v[146:153], v[56:63], v[52:55]
	v_mfma_f32_16x16x128_f8f6f4 v[48:51], v[154:161], v[56:63], v[48:51]
	v_mfma_f32_16x16x128_f8f6f4 v[198:201], v[154:161], v[72:79], v[32:35]
	v_mfma_f32_16x16x128_f8f6f4 v[194:197], v[146:153], v[72:79], v[36:39]
	v_mfma_f32_16x16x128_f8f6f4 v[202:205], v[146:153], v[80:87], v[20:23]
	v_mfma_f32_16x16x128_f8f6f4 v[206:209], v[154:161], v[80:87], v[16:19]
	v_mfma_f32_16x16x128_f8f6f4 v[230:233], v[154:161], v[88:95], v[0:3]
	v_mfma_f32_16x16x128_f8f6f4 v[226:229], v[146:153], v[88:95], v[4:7]
	v_mfma_f32_16x16x128_f8f6f4 v[68:71], v[162:169], v[56:63], v[68:71]
	v_mfma_f32_16x16x128_f8f6f4 v[64:67], v[170:177], v[56:63], v[64:67]
	v_mfma_f32_16x16x128_f8f6f4 v[238:241], v[170:177], v[72:79], v[40:43]
	v_mfma_f32_16x16x128_f8f6f4 v[234:237], v[162:169], v[72:79], v[44:47]
	v_mfma_f32_16x16x128_f8f6f4 v[242:245], v[162:169], v[80:87], v[28:31]
	v_mfma_f32_16x16x128_f8f6f4 v[246:249], v[170:177], v[80:87], v[24:27]
	v_mfma_f32_16x16x128_f8f6f4 v[130:133], v[170:177], v[88:95], v[8:11]
	v_mfma_f32_16x16x128_f8f6f4 v[250:253], v[162:169], v[88:95], v[12:15]
	s_barrier
	ds_read_b128 v[0:3], v141
	ds_read_b128 v[4:7], v141 offset:1024
	s_nop 2
	ds_read_b128 v[8:11], v141 offset:2048
	ds_read_b128 v[12:15], v141 offset:3072
	ds_read_b128 v[146:149], v142
	ds_read_b128 v[150:153], v142 offset:1024
	ds_read_b128 v[154:157], v142 offset:2048
	ds_read_b128 v[158:161], v142 offset:3072
	ds_read_b128 v[16:19], v140 offset:32768
	ds_read_b128 v[20:23], v140 offset:33792
	ds_read_b128 v[24:27], v140 offset:34816
	ds_read_b128 v[28:31], v140 offset:35840
	ds_read_b128 v[32:35], v140 offset:36864
	ds_read_b128 v[36:39], v140 offset:37888
	ds_read_b128 v[40:43], v140 offset:38912
	ds_read_b128 v[44:47], v140 offset:39936
	s_add_u32 s6, s36, 0x40000
	s_addc_u32 s7, s37, 0
	s_add_i32 m0, s47, 0x4000
	s_nop 0
	global_load_lds_dwordx4 v134, s[6:7]
	s_nop 0
	s_add_i32 m0, s47, 0x6000
	s_nop 0
	global_load_lds_dwordx4 v136, s[6:7]
	s_waitcnt vmcnt(8) lgkmcnt(0)
	s_barrier
	v_mfma_f32_16x16x128_f8f6f4 v[112:115], v[0:7], v[16:23], v[112:115]
	v_mfma_f32_16x16x128_f8f6f4 v[116:119], v[8:15], v[16:23], v[116:119]
	v_mfma_f32_16x16x128_f8f6f4 v[96:99], v[8:15], v[24:31], v[96:99]
	v_mfma_f32_16x16x128_f8f6f4 v[100:103], v[0:7], v[24:31], v[100:103]
	v_mfma_f32_16x16x128_f8f6f4 v[84:87], v[0:7], v[32:39], v[210:213]
	v_mfma_f32_16x16x128_f8f6f4 v[80:83], v[8:15], v[32:39], v[214:217]
	v_mfma_f32_16x16x128_f8f6f4 v[56:59], v[8:15], v[40:47], v[222:225]
	v_mfma_f32_16x16x128_f8f6f4 v[60:63], v[0:7], v[40:47], v[218:221]
	v_mfma_f32_16x16x128_f8f6f4 v[120:123], v[146:153], v[16:23], v[120:123]
	v_mfma_f32_16x16x128_f8f6f4 v[124:127], v[154:161], v[16:23], v[124:127]
	v_mfma_f32_16x16x128_f8f6f4 v[104:107], v[154:161], v[24:31], v[104:107]
	v_mfma_f32_16x16x128_f8f6f4 v[108:111], v[146:153], v[24:31], v[108:111]
	v_mfma_f32_16x16x128_f8f6f4 v[92:95], v[146:153], v[32:39], v[178:181]
	v_mfma_f32_16x16x128_f8f6f4 v[88:91], v[154:161], v[32:39], v[182:185]
	v_mfma_f32_16x16x128_f8f6f4 v[72:75], v[154:161], v[40:47], v[190:193]
	v_mfma_f32_16x16x128_f8f6f4 v[76:79], v[146:153], v[40:47], v[186:189]
	s_barrier
	ds_read_b128 v[24:27], v140 offset:49152
	ds_read_b128 v[28:31], v140 offset:50176
	ds_read_b128 v[162:165], v140 offset:51200
	ds_read_b128 v[166:169], v140 offset:52224
	ds_read_b128 v[170:173], v140 offset:53248
	ds_read_b128 v[174:177], v140 offset:54272
	ds_read_b128 v[178:181], v140 offset:55296
	ds_read_b128 v[182:185], v140 offset:56320
	s_add_i32 m0, s47, 0x18000
	s_nop 0
	global_load_lds_dwordx4 v135, s[34:35]
	s_nop 0
	s_add_i32 m0, s47, 0x1a000
	s_nop 0
	global_load_lds_dwordx4 v137, s[34:35]
	s_add_u32 s6, s30, 0x40080
	s_addc_u32 s7, s31, 0
	s_add_i32 m0, s47, 0x1c000
	s_nop 0
	global_load_lds_dwordx4 v135, s[6:7]
	s_nop 0
	s_add_i32 m0, s47, 0x1e000
	s_nop 0
	global_load_lds_dwordx4 v137, s[6:7]
	s_nop 0
	s_add_i32 m0, s47, 0x8000
	s_nop 0
	global_load_lds_dwordx4 v134, s[28:29]
	s_nop 0
	s_add_i32 m0, s47, 0xa000
	s_nop 0
	global_load_lds_dwordx4 v136, s[28:29]
	s_waitcnt vmcnt(8) lgkmcnt(0)
	s_barrier
	v_mfma_f32_16x16x128_f8f6f4 v[52:55], v[0:7], v[24:31], v[52:55]
	v_mfma_f32_16x16x128_f8f6f4 v[48:51], v[8:15], v[24:31], v[48:51]
	v_mfma_f32_16x16x128_f8f6f4 v[36:39], v[0:7], v[162:169], v[194:197]
	v_mfma_f32_16x16x128_f8f6f4 v[32:35], v[8:15], v[162:169], v[198:201]
	v_mfma_f32_16x16x128_f8f6f4 v[20:23], v[0:7], v[170:177], v[202:205]
	v_mfma_f32_16x16x128_f8f6f4 v[16:19], v[8:15], v[170:177], v[206:209]
	v_mfma_f32_16x16x128_f8f6f4 v[4:7], v[0:7], v[178:185], v[226:229]
	v_mfma_f32_16x16x128_f8f6f4 v[0:3], v[8:15], v[178:185], v[230:233]
	v_mfma_f32_16x16x128_f8f6f4 v[68:71], v[146:153], v[24:31], v[68:71]
	v_mfma_f32_16x16x128_f8f6f4 v[64:67], v[154:161], v[24:31], v[64:67]
	v_mfma_f32_16x16x128_f8f6f4 v[44:47], v[146:153], v[162:169], v[234:237]
	v_mfma_f32_16x16x128_f8f6f4 v[40:43], v[154:161], v[162:169], v[238:241]
	v_mfma_f32_16x16x128_f8f6f4 v[28:31], v[146:153], v[170:177], v[242:245]
	v_mfma_f32_16x16x128_f8f6f4 v[24:27], v[154:161], v[170:177], v[246:249]
	v_mfma_f32_16x16x128_f8f6f4 v[12:15], v[146:153], v[178:185], v[250:253]
	v_mfma_f32_16x16x128_f8f6f4 v[8:11], v[154:161], v[178:185], v[130:133]
	s_barrier
	s_add_i32 s55, s55, 2
	s_add_u32 s17, s17, 0x100
	s_addc_u32 s54, s54, 0
	s_cmp_gt_u32 s55, 13
	s_mov_b64 s[6:7], s[26:27]
	s_cbranch_scc0 .LBB0_1411
	s_and_b64 vcc, exec, s[12:13]
	s_cbranch_vccz .LBB0_1414
	s_barrier

.LBB0_1487:
	ds_read_b128 v[0:3], v153
	ds_read_b128 v[4:7], v153 offset:1024
	ds_read_b128 v[8:11], v153 offset:2048
	ds_read_b128 v[12:15], v153 offset:3072
	ds_read_b128 v[16:19], v154
	ds_read_b128 v[20:23], v154 offset:1024
	ds_read_b128 v[24:27], v154 offset:2048
	ds_read_b128 v[28:31], v154 offset:3072
	ds_read_b128 v[32:35], v155
	ds_read_b128 v[36:39], v155 offset:1024
	ds_read_b128 v[40:43], v155 offset:2048
	ds_read_b128 v[44:47], v155 offset:3072
	ds_read_b128 v[48:51], v155 offset:4096
	ds_read_b128 v[52:55], v155 offset:5120
	ds_read_b128 v[56:59], v155 offset:6144
	ds_read_b128 v[60:63], v155 offset:7168
	s_add_u32 s26, s28, 0x100
	s_addc_u32 s27, s29, 0
	s_add_u32 s36, s24, 0x100
	s_addc_u32 s37, s25, 0
	s_add_u32 s30, s28, 0x180
	s_addc_u32 s31, s29, 0
	s_add_u32 s34, s24, 0x180
	s_addc_u32 s35, s25, 0
	s_add_u32 s52, s28, 0xe0080
	s_addc_u32 s53, s29, 0
	s_add_i32 m0, s44, 0xc000
	s_nop 0
	global_load_lds_dwordx4 v149, s[52:53]
	s_nop 0
	s_add_i32 m0, s44, 0xe000
	s_nop 0
	global_load_lds_dwordx4 v151, s[52:53]
	s_waitcnt vmcnt(8) lgkmcnt(0)
	s_barrier
	v_mfma_f32_16x16x128_f8f6f4 v[64:67], v[0:7], v[32:39], 0
	v_mfma_f32_16x16x128_f8f6f4 v[68:71], v[8:15], v[32:39], 0
	v_mfma_f32_16x16x128_f8f6f4 v[76:79], v[8:15], v[40:47], 0
	v_mfma_f32_16x16x128_f8f6f4 v[72:75], v[0:7], v[40:47], 0
	v_mfma_f32_16x16x128_f8f6f4 v[80:83], v[0:7], v[48:55], 0
	v_mfma_f32_16x16x128_f8f6f4 v[88:91], v[8:15], v[48:55], 0
	v_mfma_f32_16x16x128_f8f6f4 v[104:107], v[8:15], v[56:63], 0
	v_mfma_f32_16x16x128_f8f6f4 v[92:95], v[0:7], v[56:63], 0
	v_mfma_f32_16x16x128_f8f6f4 v[108:111], v[16:23], v[32:39], 0
	v_mfma_f32_16x16x128_f8f6f4 v[124:127], v[24:31], v[32:39], 0
	v_mfma_f32_16x16x128_f8f6f4 v[162:165], v[24:31], v[40:47], 0
	v_mfma_f32_16x16x128_f8f6f4 v[158:161], v[16:23], v[40:47], 0
	v_mfma_f32_16x16x128_f8f6f4 v[166:169], v[16:23], v[48:55], 0
	v_mfma_f32_16x16x128_f8f6f4 v[170:173], v[24:31], v[48:55], 0
	v_mfma_f32_16x16x128_f8f6f4 v[178:181], v[24:31], v[56:63], 0
	v_mfma_f32_16x16x128_f8f6f4 v[174:177], v[16:23], v[56:63], 0
	s_barrier
	ds_read_b128 v[32:35], v155 offset:16384
	ds_read_b128 v[36:39], v155 offset:17408
	ds_read_b128 v[40:43], v155 offset:18432
	ds_read_b128 v[44:47], v155 offset:19456
	ds_read_b128 v[48:51], v155 offset:20480
	ds_read_b128 v[52:55], v155 offset:21504
	ds_read_b128 v[56:59], v155 offset:22528
	ds_read_b128 v[60:63], v155 offset:23552
	s_add_i32 m0, s44, 0x10000
	s_nop 0
	global_load_lds_dwordx4 v150, s[36:37]
	s_nop 0
	s_add_i32 m0, s44, 0x12000
	s_nop 0
	global_load_lds_dwordx4 v152, s[36:37]
	s_add_u32 s36, s24, 0xe0100
	s_addc_u32 s37, s25, 0
	s_add_i32 m0, s44, 0x14000
	s_nop 0
	global_load_lds_dwordx4 v150, s[36:37]
	s_nop 0
	s_add_i32 m0, s44, 0x16000
	s_nop 0
	global_load_lds_dwordx4 v152, s[36:37]
	s_nop 0
	s_add_i32 m0, s44, 0
	s_nop 0
	global_load_lds_dwordx4 v149, s[26:27]
	s_nop 0
	s_add_i32 m0, s44, 0x2000
	s_nop 0
	global_load_lds_dwordx4 v151, s[26:27]
	s_waitcnt vmcnt(8) lgkmcnt(0)
	s_barrier
	v_mfma_f32_16x16x128_f8f6f4 v[190:193], v[0:7], v[32:39], 0
	v_mfma_f32_16x16x128_f8f6f4 v[194:197], v[8:15], v[32:39], 0
	v_mfma_f32_16x16x128_f8f6f4 v[202:205], v[8:15], v[40:47], 0
	v_mfma_f32_16x16x128_f8f6f4 v[198:201], v[0:7], v[40:47], 0
	v_mfma_f32_16x16x128_f8f6f4 v[206:209], v[0:7], v[48:55], 0
	v_mfma_f32_16x16x128_f8f6f4 v[210:213], v[8:15], v[48:55], 0
	v_mfma_f32_16x16x128_f8f6f4 v[218:221], v[8:15], v[56:63], 0
	v_mfma_f32_16x16x128_f8f6f4 v[214:217], v[0:7], v[56:63], 0
	v_mfma_f32_16x16x128_f8f6f4 v[222:225], v[16:23], v[32:39], 0
	v_mfma_f32_16x16x128_f8f6f4 v[226:229], v[24:31], v[32:39], 0
	v_mfma_f32_16x16x128_f8f6f4 v[234:237], v[24:31], v[40:47], 0
	v_mfma_f32_16x16x128_f8f6f4 v[230:233], v[16:23], v[40:47], 0
	v_mfma_f32_16x16x128_f8f6f4 v[238:241], v[16:23], v[48:55], 0
	v_mfma_f32_16x16x128_f8f6f4 v[242:245], v[24:31], v[48:55], 0
	v_mfma_f32_16x16x128_f8f6f4 v[250:253], v[24:31], v[56:63], 0
	v_mfma_f32_16x16x128_f8f6f4 v[246:249], v[16:23], v[56:63], 0
	s_barrier
	ds_read_b128 v[0:3], v156
	ds_read_b128 v[4:7], v156 offset:1024
	ds_read_b128 v[16:19], v156 offset:2048
	ds_read_b128 v[20:23], v156 offset:3072
	ds_read_b128 v[132:135], v157
	ds_read_b128 v[136:139], v157 offset:1024
	ds_read_b128 v[140:143], v157 offset:2048
	ds_read_b128 v[144:147], v157 offset:3072
	ds_read_b128 v[8:11], v155 offset:32768
	ds_read_b128 v[12:15], v155 offset:33792
	ds_read_b128 v[24:27], v155 offset:34816
	ds_read_b128 v[28:31], v155 offset:35840
	ds_read_b128 v[32:35], v155 offset:36864
	ds_read_b128 v[36:39], v155 offset:37888
	ds_read_b128 v[40:43], v155 offset:38912
	ds_read_b128 v[44:47], v155 offset:39936
	s_add_u32 s28, s28, 0xe0100
	s_addc_u32 s29, s29, 0
	s_add_i32 m0, s44, 0x4000
	s_nop 0
	global_load_lds_dwordx4 v149, s[28:29]
	s_nop 0
	s_add_i32 m0, s44, 0x6000
	s_nop 0
	global_load_lds_dwordx4 v151, s[28:29]
	s_waitcnt vmcnt(8) lgkmcnt(0)
	s_barrier
	v_mfma_f32_16x16x128_f8f6f4 v[112:115], v[0:7], v[8:15], v[64:67]
	v_mfma_f32_16x16x128_f8f6f4 v[116:119], v[16:23], v[8:15], v[68:71]
	v_mfma_f32_16x16x128_f8f6f4 v[100:103], v[0:7], v[24:31], v[72:75]
	v_mfma_f32_16x16x128_f8f6f4 v[96:99], v[16:23], v[24:31], v[76:79]
	v_mfma_f32_16x16x128_f8f6f4 v[84:87], v[0:7], v[32:39], v[80:83]
	v_mfma_f32_16x16x128_f8f6f4 v[80:83], v[16:23], v[32:39], v[88:91]
	v_mfma_f32_16x16x128_f8f6f4 v[60:63], v[0:7], v[40:47], v[92:95]
	v_mfma_f32_16x16x128_f8f6f4 v[52:55], v[16:23], v[40:47], v[104:107]
	v_mfma_f32_16x16x128_f8f6f4 v[120:123], v[132:139], v[8:15], v[108:111]
	v_mfma_f32_16x16x128_f8f6f4 v[124:127], v[140:147], v[8:15], v[124:127]
	v_mfma_f32_16x16x128_f8f6f4 v[108:111], v[132:139], v[24:31], v[158:161]
	v_mfma_f32_16x16x128_f8f6f4 v[104:107], v[140:147], v[24:31], v[162:165]
	v_mfma_f32_16x16x128_f8f6f4 v[92:95], v[132:139], v[32:39], v[166:169]
	v_mfma_f32_16x16x128_f8f6f4 v[88:91], v[140:147], v[32:39], v[170:173]
	v_mfma_f32_16x16x128_f8f6f4 v[56:59], v[132:139], v[40:47], v[174:177]
	v_mfma_f32_16x16x128_f8f6f4 v[48:51], v[140:147], v[40:47], v[178:181]
	s_barrier
	ds_read_b128 v[158:161], v155 offset:49152
	ds_read_b128 v[162:165], v155 offset:50176
	ds_read_b128 v[166:169], v155 offset:51200
	ds_read_b128 v[170:173], v155 offset:52224
	ds_read_b128 v[174:177], v155 offset:53248
	ds_read_b128 v[178:181], v155 offset:54272
	ds_read_b128 v[182:185], v155 offset:55296
	ds_read_b128 v[186:189], v155 offset:56320
	s_add_i32 m0, s44, 0x18000
	s_nop 0
	global_load_lds_dwordx4 v150, s[34:35]
	s_nop 0
	s_add_i32 m0, s44, 0x1a000
	s_nop 0
	global_load_lds_dwordx4 v152, s[34:35]
	s_add_u32 s28, s24, 0xe0180
	s_addc_u32 s29, s25, 0
	s_add_i32 m0, s44, 0x1c000
	s_nop 0
	global_load_lds_dwordx4 v150, s[28:29]
	s_nop 0
	s_add_i32 m0, s44, 0x1e000
	s_nop 0
	global_load_lds_dwordx4 v152, s[28:29]
	s_nop 0
	s_add_i32 m0, s44, 0x8000
	s_nop 0
	global_load_lds_dwordx4 v149, s[30:31]
	s_nop 0
	s_add_i32 m0, s44, 0xa000
	s_nop 0
	global_load_lds_dwordx4 v151, s[30:31]
	s_waitcnt vmcnt(8) lgkmcnt(0)
	s_barrier
	v_mfma_f32_16x16x128_f8f6f4 v[68:71], v[0:7], v[158:165], v[190:193]
	v_mfma_f32_16x16x128_f8f6f4 v[64:67], v[16:23], v[158:165], v[194:197]
	v_mfma_f32_16x16x128_f8f6f4 v[36:39], v[16:23], v[166:173], v[202:205]
	v_mfma_f32_16x16x128_f8f6f4 v[44:47], v[0:7], v[166:173], v[198:201]
	v_mfma_f32_16x16x128_f8f6f4 v[28:31], v[0:7], v[174:181], v[206:209]
	v_mfma_f32_16x16x128_f8f6f4 v[24:27], v[16:23], v[174:181], v[210:213]
	v_mfma_f32_16x16x128_f8f6f4 v[8:11], v[16:23], v[182:189], v[218:221]
	v_mfma_f32_16x16x128_f8f6f4 v[12:15], v[0:7], v[182:189], v[214:217]
	v_mfma_f32_16x16x128_f8f6f4 v[76:79], v[132:139], v[158:165], v[222:225]
	v_mfma_f32_16x16x128_f8f6f4 v[72:75], v[140:147], v[158:165], v[226:229]
	v_mfma_f32_16x16x128_f8f6f4 v[32:35], v[140:147], v[166:173], v[234:237]
	v_mfma_f32_16x16x128_f8f6f4 v[40:43], v[132:139], v[166:173], v[230:233]
	v_mfma_f32_16x16x128_f8f6f4 v[20:23], v[132:139], v[174:181], v[238:241]
	v_mfma_f32_16x16x128_f8f6f4 v[16:19], v[140:147], v[174:181], v[242:245]
	v_mfma_f32_16x16x128_f8f6f4 v[0:3], v[140:147], v[182:189], v[250:253]
	v_mfma_f32_16x16x128_f8f6f4 v[4:7], v[132:139], v[182:189], v[246:249]
	s_barrier
	s_add_u32 s23, s24, 0x200
	s_addc_u32 s51, s25, 0
	s_mov_b32 s52, 0
.LBB0_1488:
	ds_read_b128 v[132:135], v153
	ds_read_b128 v[136:139], v153 offset:1024
	ds_read_b128 v[140:143], v153 offset:2048
	ds_read_b128 v[144:147], v153 offset:3072
	ds_read_b128 v[158:161], v154
	ds_read_b128 v[162:165], v154 offset:1024
	ds_read_b128 v[166:169], v154 offset:2048
	ds_read_b128 v[170:173], v154 offset:3072
	ds_read_b128 v[174:177], v155
	ds_read_b128 v[178:181], v155 offset:1024
	ds_read_b128 v[182:185], v155 offset:2048
	ds_read_b128 v[186:189], v155 offset:3072
	ds_read_b128 v[190:193], v155 offset:4096
	ds_read_b128 v[194:197], v155 offset:5120
	ds_read_b128 v[198:201], v155 offset:6144
	ds_read_b128 v[202:205], v155 offset:7168
	s_add_u32 s24, s26, 0x100
	s_addc_u32 s25, s27, 0
	s_cmp_eq_u32 s52, 52
	s_cselect_b32 s36, s6, s24
	s_cselect_b32 s37, s7, s25
	s_cselect_b32 s30, s20, s23
	s_cselect_b32 s31, s21, s51
	s_add_u32 s28, s36, 0x80
	s_addc_u32 s29, s37, 0
	s_add_u32 s34, s30, 0x80
	s_addc_u32 s35, s31, 0
	s_add_u32 s26, s26, 0xe0080
	s_addc_u32 s27, s27, 0
	s_add_i32 m0, s44, 0xc000
	s_nop 0
	global_load_lds_dwordx4 v149, s[26:27]
	s_nop 0
	s_add_i32 m0, s44, 0xe000
	s_nop 0
	global_load_lds_dwordx4 v151, s[26:27]
	s_waitcnt vmcnt(8) lgkmcnt(0)
	s_barrier
	v_mfma_f32_16x16x128_f8f6f4 v[112:115], v[132:139], v[174:181], v[112:115]
	v_mfma_f32_16x16x128_f8f6f4 v[116:119], v[140:147], v[174:181], v[116:119]
	v_mfma_f32_16x16x128_f8f6f4 v[96:99], v[140:147], v[182:189], v[96:99]
	v_mfma_f32_16x16x128_f8f6f4 v[100:103], v[132:139], v[182:189], v[100:103]
	v_mfma_f32_16x16x128_f8f6f4 v[206:209], v[132:139], v[190:197], v[84:87]
	v_mfma_f32_16x16x128_f8f6f4 v[210:213], v[140:147], v[190:197], v[80:83]
	v_mfma_f32_16x16x128_f8f6f4 v[218:221], v[140:147], v[198:205], v[52:55]
	v_mfma_f32_16x16x128_f8f6f4 v[214:217], v[132:139], v[198:205], v[60:63]
	v_mfma_f32_16x16x128_f8f6f4 v[120:123], v[158:165], v[174:181], v[120:123]
	v_mfma_f32_16x16x128_f8f6f4 v[124:127], v[166:173], v[174:181], v[124:127]
	v_mfma_f32_16x16x128_f8f6f4 v[108:111], v[158:165], v[182:189], v[108:111]
	v_mfma_f32_16x16x128_f8f6f4 v[104:107], v[166:173], v[182:189], v[104:107]
	v_mfma_f32_16x16x128_f8f6f4 v[174:177], v[158:165], v[190:197], v[92:95]
	v_mfma_f32_16x16x128_f8f6f4 v[178:181], v[166:173], v[190:197], v[88:91]
	v_mfma_f32_16x16x128_f8f6f4 v[182:185], v[158:165], v[198:205], v[56:59]
	v_mfma_f32_16x16x128_f8f6f4 v[186:189], v[166:173], v[198:205], v[48:51]
	s_barrier
	s_nop 4
	ds_read_b128 v[48:51], v155 offset:16384
	ds_read_b128 v[52:55], v155 offset:17408
	ds_read_b128 v[56:59], v155 offset:18432
	ds_read_b128 v[60:63], v155 offset:19456
	ds_read_b128 v[80:83], v155 offset:20480
	ds_read_b128 v[84:87], v155 offset:21504
	ds_read_b128 v[88:91], v155 offset:22528
	ds_read_b128 v[92:95], v155 offset:23552
	s_add_i32 m0, s44, 0x10000
	s_nop 0
	global_load_lds_dwordx4 v150, s[30:31]
	s_nop 0
	s_add_i32 m0, s44, 0x12000
	s_nop 0
	global_load_lds_dwordx4 v152, s[30:31]
	s_add_u32 s26, s30, 0xe0000
	s_addc_u32 s27, s31, 0
	s_add_i32 m0, s44, 0x14000
	s_nop 0
	global_load_lds_dwordx4 v150, s[26:27]
	s_nop 0
	s_add_i32 m0, s44, 0x16000
	s_nop 0
	global_load_lds_dwordx4 v152, s[26:27]
	s_nop 0
	s_add_i32 m0, s44, 0
	s_nop 0
	global_load_lds_dwordx4 v149, s[36:37]
	s_nop 0
	s_add_i32 m0, s44, 0x2000
	s_nop 0
	global_load_lds_dwordx4 v151, s[36:37]
	s_waitcnt vmcnt(8) lgkmcnt(0)
	s_barrier
	v_mfma_f32_16x16x128_f8f6f4 v[68:71], v[132:139], v[48:55], v[68:71]
	v_mfma_f32_16x16x128_f8f6f4 v[64:67], v[140:147], v[48:55], v[64:67]
	v_mfma_f32_16x16x128_f8f6f4 v[194:197], v[140:147], v[56:63], v[36:39]
	v_mfma_f32_16x16x128_f8f6f4 v[190:193], v[132:139], v[56:63], v[44:47]
	v_mfma_f32_16x16x128_f8f6f4 v[198:201], v[132:139], v[80:87], v[28:31]
	v_mfma_f32_16x16x128_f8f6f4 v[202:205], v[140:147], v[80:87], v[24:27]
	v_mfma_f32_16x16x128_f8f6f4 v[226:229], v[140:147], v[88:95], v[8:11]
	v_mfma_f32_16x16x128_f8f6f4 v[222:225], v[132:139], v[88:95], v[12:15]
	v_mfma_f32_16x16x128_f8f6f4 v[76:79], v[158:165], v[48:55], v[76:79]
	v_mfma_f32_16x16x128_f8f6f4 v[72:75], v[166:173], v[48:55], v[72:75]
	v_mfma_f32_16x16x128_f8f6f4 v[234:237], v[166:173], v[56:63], v[32:35]
	v_mfma_f32_16x16x128_f8f6f4 v[230:233], v[158:165], v[56:63], v[40:43]
	v_mfma_f32_16x16x128_f8f6f4 v[238:241], v[158:165], v[80:87], v[20:23]
	v_mfma_f32_16x16x128_f8f6f4 v[242:245], v[166:173], v[80:87], v[16:19]
	v_mfma_f32_16x16x128_f8f6f4 v[250:253], v[166:173], v[88:95], v[0:3]
	v_mfma_f32_16x16x128_f8f6f4 v[246:249], v[158:165], v[88:95], v[4:7]
	s_barrier
	s_nop 4
	ds_read_b128 v[0:3], v156
	ds_read_b128 v[4:7], v156 offset:1024
	ds_read_b128 v[16:19], v156 offset:2048
	ds_read_b128 v[20:23], v156 offset:3072
	ds_read_b128 v[132:135], v157
	ds_read_b128 v[136:139], v157 offset:1024
	ds_read_b128 v[140:143], v157 offset:2048
	ds_read_b128 v[144:147], v157 offset:3072
	ds_read_b128 v[8:11], v155 offset:32768
	ds_read_b128 v[12:15], v155 offset:33792
	ds_read_b128 v[24:27], v155 offset:34816
	ds_read_b128 v[28:31], v155 offset:35840
	ds_read_b128 v[32:35], v155 offset:36864
	ds_read_b128 v[36:39], v155 offset:37888
	ds_read_b128 v[40:43], v155 offset:38912
	ds_read_b128 v[44:47], v155 offset:39936
	s_add_u32 s26, s36, 0xe0000
	s_addc_u32 s27, s37, 0
	s_add_i32 m0, s44, 0x4000
	s_nop 0
	global_load_lds_dwordx4 v149, s[26:27]
	s_nop 0
	s_add_i32 m0, s44, 0x6000
	s_nop 0
	global_load_lds_dwordx4 v151, s[26:27]
	s_waitcnt vmcnt(8) lgkmcnt(0)
	s_barrier
	v_mfma_f32_16x16x128_f8f6f4 v[112:115], v[0:7], v[8:15], v[112:115]
	v_mfma_f32_16x16x128_f8f6f4 v[116:119], v[16:23], v[8:15], v[116:119]
	v_mfma_f32_16x16x128_f8f6f4 v[96:99], v[16:23], v[24:31], v[96:99]
	v_mfma_f32_16x16x128_f8f6f4 v[100:103], v[0:7], v[24:31], v[100:103]
	v_mfma_f32_16x16x128_f8f6f4 v[84:87], v[0:7], v[32:39], v[206:209]
	v_mfma_f32_16x16x128_f8f6f4 v[80:83], v[16:23], v[32:39], v[210:213]
	v_mfma_f32_16x16x128_f8f6f4 v[52:55], v[16:23], v[40:47], v[218:221]
	v_mfma_f32_16x16x128_f8f6f4 v[60:63], v[0:7], v[40:47], v[214:217]
	v_mfma_f32_16x16x128_f8f6f4 v[120:123], v[132:139], v[8:15], v[120:123]
	v_mfma_f32_16x16x128_f8f6f4 v[124:127], v[140:147], v[8:15], v[124:127]
	v_mfma_f32_16x16x128_f8f6f4 v[104:107], v[140:147], v[24:31], v[104:107]
	v_mfma_f32_16x16x128_f8f6f4 v[108:111], v[132:139], v[24:31], v[108:111]
	v_mfma_f32_16x16x128_f8f6f4 v[92:95], v[132:139], v[32:39], v[174:177]
	v_mfma_f32_16x16x128_f8f6f4 v[88:91], v[140:147], v[32:39], v[178:181]
	v_mfma_f32_16x16x128_f8f6f4 v[48:51], v[140:147], v[40:47], v[186:189]
	v_mfma_f32_16x16x128_f8f6f4 v[56:59], v[132:139], v[40:47], v[182:185]
	s_barrier
	ds_read_b128 v[158:161], v155 offset:49152
	ds_read_b128 v[162:165], v155 offset:50176
	ds_read_b128 v[166:169], v155 offset:51200
	ds_read_b128 v[170:173], v155 offset:52224
	ds_read_b128 v[174:177], v155 offset:53248
	ds_read_b128 v[178:181], v155 offset:54272
	ds_read_b128 v[182:185], v155 offset:55296
	ds_read_b128 v[186:189], v155 offset:56320
	s_add_i32 m0, s44, 0x18000
	s_nop 0
	global_load_lds_dwordx4 v150, s[34:35]
	s_nop 0
	s_add_i32 m0, s44, 0x1a000
	s_nop 0
	global_load_lds_dwordx4 v152, s[34:35]
	s_add_u32 s26, s30, 0xe0080
	s_addc_u32 s27, s31, 0
	s_add_i32 m0, s44, 0x1c000
	s_nop 0
	global_load_lds_dwordx4 v150, s[26:27]
	s_nop 0
	s_add_i32 m0, s44, 0x1e000
	s_nop 0
	global_load_lds_dwordx4 v152, s[26:27]
	s_nop 0
	s_add_i32 m0, s44, 0x8000
	s_nop 0
	global_load_lds_dwordx4 v149, s[28:29]
	s_nop 0
	s_add_i32 m0, s44, 0xa000
	s_nop 0
	global_load_lds_dwordx4 v151, s[28:29]
	s_waitcnt vmcnt(8) lgkmcnt(0)
	s_barrier
	v_mfma_f32_16x16x128_f8f6f4 v[68:71], v[0:7], v[158:165], v[68:71]
	v_mfma_f32_16x16x128_f8f6f4 v[64:67], v[16:23], v[158:165], v[64:67]
	v_mfma_f32_16x16x128_f8f6f4 v[36:39], v[16:23], v[166:173], v[194:197]
	v_mfma_f32_16x16x128_f8f6f4 v[44:47], v[0:7], v[166:173], v[190:193]
	v_mfma_f32_16x16x128_f8f6f4 v[28:31], v[0:7], v[174:181], v[198:201]
	v_mfma_f32_16x16x128_f8f6f4 v[24:27], v[16:23], v[174:181], v[202:205]
	v_mfma_f32_16x16x128_f8f6f4 v[8:11], v[16:23], v[182:189], v[226:229]
	v_mfma_f32_16x16x128_f8f6f4 v[12:15], v[0:7], v[182:189], v[222:225]
	v_mfma_f32_16x16x128_f8f6f4 v[76:79], v[132:139], v[158:165], v[76:79]
	v_mfma_f32_16x16x128_f8f6f4 v[72:75], v[140:147], v[158:165], v[72:75]
	v_mfma_f32_16x16x128_f8f6f4 v[32:35], v[140:147], v[166:173], v[234:237]
	v_mfma_f32_16x16x128_f8f6f4 v[40:43], v[132:139], v[166:173], v[230:233]
	v_mfma_f32_16x16x128_f8f6f4 v[20:23], v[132:139], v[174:181], v[238:241]
	v_mfma_f32_16x16x128_f8f6f4 v[16:19], v[140:147], v[174:181], v[242:245]
	v_mfma_f32_16x16x128_f8f6f4 v[0:3], v[140:147], v[182:189], v[250:253]
	v_mfma_f32_16x16x128_f8f6f4 v[4:7], v[132:139], v[182:189], v[246:249]
	s_barrier
	s_add_i32 s52, s52, 2
	s_add_u32 s23, s23, 0x100
	s_addc_u32 s51, s51, 0
	s_cmp_gt_u32 s52, 53
	s_mov_b64 s[26:27], s[24:25]
	s_cbranch_scc0 .LBB0_1488
	s_and_b64 vcc, exec, s[16:17]
	s_cbranch_vccz .LBB0_1491
	s_barrier
